# nt hints plus GEMM trailing barrier moved up by 4 (f16) / 2 (fp8) MFMAs with prio 2 tail
# baseline (speedup 1.0000x reference)
.LBB0_410:
	ds_read_b128 v[152:155], v148
	ds_read_b128 v[156:159], v148 offset:1024
	ds_read_b128 v[160:163], v148 offset:2048
	ds_read_b128 v[164:167], v148 offset:3072
	ds_read_b128 v[168:171], v149
	ds_read_b128 v[172:175], v149 offset:1024
	ds_read_b128 v[176:179], v149 offset:2048
	ds_read_b128 v[180:183], v149 offset:3072
	s_add_u32 s28, s26, 0xfff80080
	s_addc_u32 s29, s27, -1
	s_cmp_eq_u32 s64, 28
	s_cselect_b32 s31, s21, s29
	s_cselect_b32 s30, s60, s28
	s_cselect_b32 s29, s19, s63
	s_cselect_b32 s28, s61, s62
	v_lshl_add_u64 v[184:185], s[26:27], 0, v[138:139]
	s_add_i32 m0, s17, 0xc000
	ds_read_b128 v[188:191], v150
	ds_read_b128 v[192:195], v150 offset:1024
	ds_read_b128 v[196:199], v150 offset:2048
	ds_read_b128 v[200:203], v150 offset:3072
	ds_read_b128 v[204:207], v150 offset:4096
	ds_read_b128 v[208:211], v150 offset:5120
	ds_read_b128 v[212:215], v150 offset:6144
	ds_read_b128 v[216:219], v150 offset:7168
	global_load_lds_dwordx4 v[184:185], off
	v_lshl_add_u64 v[184:185], s[26:27], 0, v[140:141]
	s_add_i32 m0, s17, 0xe000
	s_nop 0
	global_load_lds_dwordx4 v[184:185], off
	s_waitcnt vmcnt(8)
	s_waitcnt lgkmcnt(0)
	s_barrier
	s_setprio 1
	s_waitcnt lgkmcnt(0)
	v_mfma_f32_16x16x32_f16 v[126:129], v[152:155], v[188:191], v[126:129]
	v_mfma_f32_16x16x32_f16 v[122:125], v[160:163], v[188:191], v[122:125]
	v_mfma_f32_16x16x32_f16 v[118:121], v[152:155], v[196:199], v[118:121]
	v_mfma_f32_16x16x32_f16 v[114:117], v[160:163], v[196:199], v[114:117]
	v_mfma_f32_16x16x32_f16 v[102:105], v[152:155], v[204:207], v[102:105]
	v_mfma_f32_16x16x32_f16 v[98:101], v[160:163], v[204:207], v[98:101]
	v_mfma_f32_16x16x32_f16 v[86:89], v[152:155], v[212:215], v[86:89]
	v_mfma_f32_16x16x32_f16 v[82:85], v[160:163], v[212:215], v[82:85]
	v_mfma_f32_16x16x32_f16 v[126:129], v[156:159], v[192:195], v[126:129]
	v_mfma_f32_16x16x32_f16 v[122:125], v[164:167], v[192:195], v[122:125]
	v_mfma_f32_16x16x32_f16 v[118:121], v[156:159], v[200:203], v[118:121]
	v_mfma_f32_16x16x32_f16 v[114:117], v[164:167], v[200:203], v[114:117]
	v_mfma_f32_16x16x32_f16 v[102:105], v[156:159], v[208:211], v[102:105]
	v_mfma_f32_16x16x32_f16 v[98:101], v[164:167], v[208:211], v[98:101]
	v_mfma_f32_16x16x32_f16 v[86:89], v[156:159], v[216:219], v[86:89]
	v_mfma_f32_16x16x32_f16 v[82:85], v[164:167], v[216:219], v[82:85]
	s_setprio 0
	s_setprio 1
	v_mfma_f32_16x16x32_f16 v[110:113], v[168:171], v[188:191], v[110:113]
	v_mfma_f32_16x16x32_f16 v[106:109], v[176:179], v[188:191], v[106:109]
	v_mfma_f32_16x16x32_f16 v[94:97], v[168:171], v[196:199], v[94:97]
	v_mfma_f32_16x16x32_f16 v[90:93], v[176:179], v[196:199], v[90:93]
	v_mfma_f32_16x16x32_f16 v[78:81], v[168:171], v[204:207], v[78:81]
	v_mfma_f32_16x16x32_f16 v[74:77], v[176:179], v[204:207], v[74:77]
	v_mfma_f32_16x16x32_f16 v[70:73], v[168:171], v[212:215], v[70:73]
	v_mfma_f32_16x16x32_f16 v[66:69], v[176:179], v[212:215], v[66:69]
	v_mfma_f32_16x16x32_f16 v[110:113], v[172:175], v[192:195], v[110:113]
	v_mfma_f32_16x16x32_f16 v[106:109], v[180:183], v[192:195], v[106:109]
	v_mfma_f32_16x16x32_f16 v[94:97], v[172:175], v[200:203], v[94:97]
	v_mfma_f32_16x16x32_f16 v[90:93], v[180:183], v[200:203], v[90:93]
	s_setprio 2
	s_barrier
	v_mfma_f32_16x16x32_f16 v[78:81], v[172:175], v[208:211], v[78:81]
	v_mfma_f32_16x16x32_f16 v[74:77], v[180:183], v[208:211], v[74:77]
	v_mfma_f32_16x16x32_f16 v[70:73], v[172:175], v[216:219], v[70:73]
	v_mfma_f32_16x16x32_f16 v[66:69], v[180:183], v[216:219], v[66:69]
	s_setprio 0
	s_nop 0
	s_add_i32 s65, s48, s34
	v_lshl_add_u64 v[184:185], s[28:29], 0, v[134:135]
	s_mov_b32 m0, s65
	ds_read_b128 v[188:191], v150 offset:16384
	ds_read_b128 v[192:195], v150 offset:17408
	ds_read_b128 v[196:199], v150 offset:18432
	ds_read_b128 v[200:203], v150 offset:19456
	ds_read_b128 v[204:207], v150 offset:20480
	ds_read_b128 v[208:211], v150 offset:21504
	ds_read_b128 v[212:215], v150 offset:22528
	ds_read_b128 v[216:219], v150 offset:23552
	global_load_lds_dwordx4 v[184:185], off
	s_add_i32 m0, s65, 0x2000
	s_add_u32 s66, s28, 0x80000
	v_lshl_add_u64 v[220:221], s[28:29], 0, v[130:131]
	s_addc_u32 s67, s29, 0
	s_add_i32 s65, s49, s34
	global_load_lds_dwordx4 v[220:221], off
	v_lshl_add_u64 v[222:223], s[66:67], 0, v[134:135]
	s_mov_b32 m0, s65
	v_lshl_add_u64 v[224:225], s[30:31], 0, v[132:133]
	global_load_lds_dwordx4 v[222:223], off
	v_lshl_add_u64 v[222:223], s[66:67], 0, v[130:131]
	s_add_i32 m0, s65, 0x2000
	s_nop 0
	global_load_lds_dwordx4 v[222:223], off
	v_lshl_add_u64 v[222:223], s[30:31], 0, v[136:137]
	s_mov_b32 m0, s17
	s_nop 0
	global_load_lds_dwordx4 v[222:223], off
	s_mov_b32 m0, s37
	s_nop 0
	global_load_lds_dwordx4 v[224:225], off
	s_waitcnt vmcnt(8)
	s_waitcnt lgkmcnt(0)
	s_barrier
	s_setprio 1
	s_waitcnt lgkmcnt(0)
	v_mfma_f32_16x16x32_f16 v[62:65], v[152:155], v[188:191], v[62:65]
	v_mfma_f32_16x16x32_f16 v[58:61], v[160:163], v[188:191], v[58:61]
	v_mfma_f32_16x16x32_f16 v[54:57], v[152:155], v[196:199], v[54:57]
	v_mfma_f32_16x16x32_f16 v[50:53], v[160:163], v[196:199], v[50:53]
	v_mfma_f32_16x16x32_f16 v[38:41], v[152:155], v[204:207], v[38:41]
	v_mfma_f32_16x16x32_f16 v[34:37], v[160:163], v[204:207], v[34:37]
	v_mfma_f32_16x16x32_f16 v[22:25], v[152:155], v[212:215], v[22:25]
	v_mfma_f32_16x16x32_f16 v[18:21], v[160:163], v[212:215], v[18:21]
	v_mfma_f32_16x16x32_f16 v[62:65], v[156:159], v[192:195], v[62:65]
	v_mfma_f32_16x16x32_f16 v[58:61], v[164:167], v[192:195], v[58:61]
	v_mfma_f32_16x16x32_f16 v[54:57], v[156:159], v[200:203], v[54:57]
	v_mfma_f32_16x16x32_f16 v[50:53], v[164:167], v[200:203], v[50:53]
	v_mfma_f32_16x16x32_f16 v[38:41], v[156:159], v[208:211], v[38:41]
	v_mfma_f32_16x16x32_f16 v[34:37], v[164:167], v[208:211], v[34:37]
	v_mfma_f32_16x16x32_f16 v[22:25], v[156:159], v[216:219], v[22:25]
	v_mfma_f32_16x16x32_f16 v[18:21], v[164:167], v[216:219], v[18:21]
	s_setprio 0
	s_setprio 1
	v_mfma_f32_16x16x32_f16 v[46:49], v[168:171], v[188:191], v[46:49]
	v_mfma_f32_16x16x32_f16 v[42:45], v[176:179], v[188:191], v[42:45]
	v_mfma_f32_16x16x32_f16 v[30:33], v[168:171], v[196:199], v[30:33]
	v_mfma_f32_16x16x32_f16 v[26:29], v[176:179], v[196:199], v[26:29]
	v_mfma_f32_16x16x32_f16 v[14:17], v[168:171], v[204:207], v[14:17]
	v_mfma_f32_16x16x32_f16 v[10:13], v[176:179], v[204:207], v[10:13]
	v_mfma_f32_16x16x32_f16 v[6:9], v[168:171], v[212:215], v[6:9]
	v_mfma_f32_16x16x32_f16 v[2:5], v[176:179], v[212:215], v[2:5]
	v_mfma_f32_16x16x32_f16 v[46:49], v[172:175], v[192:195], v[46:49]
	v_mfma_f32_16x16x32_f16 v[42:45], v[180:183], v[192:195], v[42:45]
	v_mfma_f32_16x16x32_f16 v[30:33], v[172:175], v[200:203], v[30:33]
	v_mfma_f32_16x16x32_f16 v[26:29], v[180:183], v[200:203], v[26:29]
	s_setprio 2
	s_barrier
	v_mfma_f32_16x16x32_f16 v[14:17], v[172:175], v[208:211], v[14:17]
	v_mfma_f32_16x16x32_f16 v[10:13], v[180:183], v[208:211], v[10:13]
	v_mfma_f32_16x16x32_f16 v[6:9], v[172:175], v[216:219], v[6:9]
	v_mfma_f32_16x16x32_f16 v[2:5], v[180:183], v[216:219], v[2:5]
	s_setprio 0
	s_nop 0
	s_add_i32 s65, 0, 0x18000
	v_add_u32_e32 v151, s65, v146
	s_add_i32 s66, 0, 0x1c000
	ds_read_b128 v[152:155], v151
	ds_read_b128 v[156:159], v151 offset:1024
	ds_read_b128 v[160:163], v151 offset:2048
	ds_read_b128 v[164:167], v151 offset:3072
	v_add_u32_e32 v151, s66, v146
	ds_read_b128 v[168:171], v151
	ds_read_b128 v[172:175], v151 offset:1024
	ds_read_b128 v[176:179], v151 offset:2048
	ds_read_b128 v[180:183], v151 offset:3072
	s_add_u32 s30, s30, 0x80000
	s_addc_u32 s31, s31, 0
	s_mov_b32 m0, s38
	v_lshl_add_u64 v[226:227], s[30:31], 0, v[136:137]
	ds_read_b128 v[188:191], v150 offset:32768
	ds_read_b128 v[192:195], v150 offset:33792
	ds_read_b128 v[196:199], v150 offset:34816
	ds_read_b128 v[200:203], v150 offset:35840
	ds_read_b128 v[204:207], v150 offset:36864
	ds_read_b128 v[208:211], v150 offset:37888
	ds_read_b128 v[212:215], v150 offset:38912
	ds_read_b128 v[216:219], v150 offset:39936
	global_load_lds_dwordx4 v[226:227], off
	v_lshl_add_u64 v[226:227], s[30:31], 0, v[132:133]
	s_mov_b32 m0, s39
	s_nop 0
	global_load_lds_dwordx4 v[226:227], off
	s_waitcnt vmcnt(8)
	s_waitcnt lgkmcnt(0)
	s_barrier
	s_setprio 1
	s_waitcnt lgkmcnt(0)
	v_mfma_f32_16x16x32_f16 v[126:129], v[152:155], v[188:191], v[126:129]
	v_mfma_f32_16x16x32_f16 v[122:125], v[160:163], v[188:191], v[122:125]
	v_mfma_f32_16x16x32_f16 v[118:121], v[152:155], v[196:199], v[118:121]
	v_mfma_f32_16x16x32_f16 v[114:117], v[160:163], v[196:199], v[114:117]
	v_mfma_f32_16x16x32_f16 v[102:105], v[152:155], v[204:207], v[102:105]
	v_mfma_f32_16x16x32_f16 v[98:101], v[160:163], v[204:207], v[98:101]
	v_mfma_f32_16x16x32_f16 v[86:89], v[152:155], v[212:215], v[86:89]
	v_mfma_f32_16x16x32_f16 v[82:85], v[160:163], v[212:215], v[82:85]
	v_mfma_f32_16x16x32_f16 v[126:129], v[156:159], v[192:195], v[126:129]
	v_mfma_f32_16x16x32_f16 v[122:125], v[164:167], v[192:195], v[122:125]
	v_mfma_f32_16x16x32_f16 v[118:121], v[156:159], v[200:203], v[118:121]
	v_mfma_f32_16x16x32_f16 v[114:117], v[164:167], v[200:203], v[114:117]
	v_mfma_f32_16x16x32_f16 v[102:105], v[156:159], v[208:211], v[102:105]
	v_mfma_f32_16x16x32_f16 v[98:101], v[164:167], v[208:211], v[98:101]
	v_mfma_f32_16x16x32_f16 v[86:89], v[156:159], v[216:219], v[86:89]
	v_mfma_f32_16x16x32_f16 v[82:85], v[164:167], v[216:219], v[82:85]
	s_setprio 0
	s_setprio 1
	v_mfma_f32_16x16x32_f16 v[110:113], v[168:171], v[188:191], v[110:113]
	v_mfma_f32_16x16x32_f16 v[106:109], v[176:179], v[188:191], v[106:109]
	v_mfma_f32_16x16x32_f16 v[94:97], v[168:171], v[196:199], v[94:97]
	v_mfma_f32_16x16x32_f16 v[90:93], v[176:179], v[196:199], v[90:93]
	v_mfma_f32_16x16x32_f16 v[78:81], v[168:171], v[204:207], v[78:81]
	v_mfma_f32_16x16x32_f16 v[74:77], v[176:179], v[204:207], v[74:77]
	v_mfma_f32_16x16x32_f16 v[70:73], v[168:171], v[212:215], v[70:73]
	v_mfma_f32_16x16x32_f16 v[66:69], v[176:179], v[212:215], v[66:69]
	v_mfma_f32_16x16x32_f16 v[110:113], v[172:175], v[192:195], v[110:113]
	v_mfma_f32_16x16x32_f16 v[106:109], v[180:183], v[192:195], v[106:109]
	v_mfma_f32_16x16x32_f16 v[94:97], v[172:175], v[200:203], v[94:97]
	v_mfma_f32_16x16x32_f16 v[90:93], v[180:183], v[200:203], v[90:93]
	s_setprio 2
	s_barrier
	v_mfma_f32_16x16x32_f16 v[78:81], v[172:175], v[208:211], v[78:81]
	v_mfma_f32_16x16x32_f16 v[74:77], v[180:183], v[208:211], v[74:77]
	v_mfma_f32_16x16x32_f16 v[70:73], v[172:175], v[216:219], v[70:73]
	v_mfma_f32_16x16x32_f16 v[66:69], v[180:183], v[216:219], v[66:69]
	s_setprio 0
	s_nop 0
	s_add_i32 s30, s65, s34
	v_lshl_add_u64 v[184:185], v[184:185], 0, s[12:13]
	s_mov_b32 m0, s30
	ds_read_b128 v[188:191], v150 offset:49152
	ds_read_b128 v[192:195], v150 offset:50176
	ds_read_b128 v[196:199], v150 offset:51200
	ds_read_b128 v[200:203], v150 offset:52224
	ds_read_b128 v[204:207], v150 offset:53248
	ds_read_b128 v[208:211], v150 offset:54272
	ds_read_b128 v[212:215], v150 offset:55296
	ds_read_b128 v[216:219], v150 offset:56320
	global_load_lds_dwordx4 v[184:185], off
	s_add_i32 m0, s30, 0x2000
	s_add_u32 s28, s28, 0x80080
	v_lshl_add_u64 v[184:185], v[220:221], 0, s[12:13]
	s_addc_u32 s29, s29, 0
	s_add_i32 s30, s66, s34
	global_load_lds_dwordx4 v[184:185], off
	v_lshl_add_u64 v[184:185], s[28:29], 0, v[134:135]
	s_mov_b32 m0, s30
	s_nop 0
	global_load_lds_dwordx4 v[184:185], off
	v_lshl_add_u64 v[184:185], s[28:29], 0, v[130:131]
	s_add_i32 m0, s30, 0x2000
	s_nop 0
	global_load_lds_dwordx4 v[184:185], off
	v_lshl_add_u64 v[184:185], v[222:223], 0, s[12:13]
	s_mov_b32 m0, s41
	s_nop 0
	global_load_lds_dwordx4 v[184:185], off
	v_lshl_add_u64 v[184:185], v[224:225], 0, s[12:13]
	s_mov_b32 m0, s46
	s_nop 0
	global_load_lds_dwordx4 v[184:185], off
	s_waitcnt vmcnt(8)
	s_waitcnt lgkmcnt(0)
	s_barrier
	s_setprio 1
	s_waitcnt lgkmcnt(0)
	v_mfma_f32_16x16x32_f16 v[62:65], v[152:155], v[188:191], v[62:65]
	v_mfma_f32_16x16x32_f16 v[58:61], v[160:163], v[188:191], v[58:61]
	v_mfma_f32_16x16x32_f16 v[54:57], v[152:155], v[196:199], v[54:57]
	v_mfma_f32_16x16x32_f16 v[50:53], v[160:163], v[196:199], v[50:53]
	v_mfma_f32_16x16x32_f16 v[38:41], v[152:155], v[204:207], v[38:41]
	v_mfma_f32_16x16x32_f16 v[34:37], v[160:163], v[204:207], v[34:37]
	v_mfma_f32_16x16x32_f16 v[22:25], v[152:155], v[212:215], v[22:25]
	v_mfma_f32_16x16x32_f16 v[18:21], v[160:163], v[212:215], v[18:21]
	v_mfma_f32_16x16x32_f16 v[62:65], v[156:159], v[192:195], v[62:65]
	v_mfma_f32_16x16x32_f16 v[58:61], v[164:167], v[192:195], v[58:61]
	v_mfma_f32_16x16x32_f16 v[54:57], v[156:159], v[200:203], v[54:57]
	v_mfma_f32_16x16x32_f16 v[50:53], v[164:167], v[200:203], v[50:53]
	v_mfma_f32_16x16x32_f16 v[38:41], v[156:159], v[208:211], v[38:41]
	v_mfma_f32_16x16x32_f16 v[34:37], v[164:167], v[208:211], v[34:37]
	v_mfma_f32_16x16x32_f16 v[22:25], v[156:159], v[216:219], v[22:25]
	v_mfma_f32_16x16x32_f16 v[18:21], v[164:167], v[216:219], v[18:21]
	s_setprio 0
	s_setprio 1
	v_mfma_f32_16x16x32_f16 v[46:49], v[168:171], v[188:191], v[46:49]
	v_mfma_f32_16x16x32_f16 v[42:45], v[176:179], v[188:191], v[42:45]
	v_mfma_f32_16x16x32_f16 v[30:33], v[168:171], v[196:199], v[30:33]
	v_mfma_f32_16x16x32_f16 v[26:29], v[176:179], v[196:199], v[26:29]
	v_mfma_f32_16x16x32_f16 v[14:17], v[168:171], v[204:207], v[14:17]
	v_mfma_f32_16x16x32_f16 v[10:13], v[176:179], v[204:207], v[10:13]
	v_mfma_f32_16x16x32_f16 v[6:9], v[168:171], v[212:215], v[6:9]
	v_mfma_f32_16x16x32_f16 v[2:5], v[176:179], v[212:215], v[2:5]
	v_mfma_f32_16x16x32_f16 v[46:49], v[172:175], v[192:195], v[46:49]
	v_mfma_f32_16x16x32_f16 v[42:45], v[180:183], v[192:195], v[42:45]
	v_mfma_f32_16x16x32_f16 v[30:33], v[172:175], v[200:203], v[30:33]
	v_mfma_f32_16x16x32_f16 v[26:29], v[180:183], v[200:203], v[26:29]
	s_setprio 2
	s_barrier
	v_mfma_f32_16x16x32_f16 v[14:17], v[172:175], v[208:211], v[14:17]
	v_mfma_f32_16x16x32_f16 v[10:13], v[180:183], v[208:211], v[10:13]
	v_mfma_f32_16x16x32_f16 v[6:9], v[172:175], v[216:219], v[6:9]
	v_mfma_f32_16x16x32_f16 v[2:5], v[180:183], v[216:219], v[2:5]
	s_setprio 0
	s_nop 0
	s_add_i32 s64, s64, 2
	s_add_u32 s26, s26, 0x100
	s_addc_u32 s27, s27, 0
	s_add_u32 s62, s62, 0x100
	s_addc_u32 s63, s63, 0
	s_cmp_gt_u32 s64, 29
	s_cbranch_scc0 .LBB0_410
	s_and_b64 vcc, exec, s[14:15]
	s_cbranch_vccz .LBB0_413
	s_barrier

.LBB0_628:
	ds_read_b128 v[146:149], v154
	ds_read_b128 v[158:161], v154 offset:1024
	ds_read_b128 v[162:165], v154 offset:2048
	ds_read_b128 v[166:169], v154 offset:3072
	ds_read_b128 v[170:173], v155
	ds_read_b128 v[174:177], v155 offset:1024
	ds_read_b128 v[178:181], v155 offset:2048
	ds_read_b128 v[182:185], v155 offset:3072
	s_add_u32 s28, s26, 0xfff80080
	s_addc_u32 s29, s27, -1
	s_cmp_eq_u32 s63, 28
	s_cselect_b32 s31, s19, s29
	s_cselect_b32 s30, s51, s28
	s_cselect_b32 s29, s17, s62
	s_cselect_b32 s28, s60, s61
	v_lshl_add_u64 v[150:151], s[26:27], 0, v[138:139]
	s_add_i32 m0, s25, 0xc000
	ds_read_b128 v[188:191], v156
	ds_read_b128 v[192:195], v156 offset:1024
	ds_read_b128 v[196:199], v156 offset:2048
	ds_read_b128 v[200:203], v156 offset:3072
	ds_read_b128 v[204:207], v156 offset:4096
	ds_read_b128 v[208:211], v156 offset:5120
	ds_read_b128 v[212:215], v156 offset:6144
	ds_read_b128 v[216:219], v156 offset:7168
	global_load_lds_dwordx4 v[150:151], off
	v_lshl_add_u64 v[150:151], s[26:27], 0, v[140:141]
	s_add_i32 m0, s25, 0xe000
	s_nop 0
	global_load_lds_dwordx4 v[150:151], off
	s_waitcnt vmcnt(8)
	s_waitcnt lgkmcnt(0)
	s_barrier
	s_setprio 1
	s_waitcnt lgkmcnt(0)
	v_mfma_f32_16x16x32_f16 v[126:129], v[146:149], v[188:191], v[126:129]
	v_mfma_f32_16x16x32_f16 v[122:125], v[162:165], v[188:191], v[122:125]
	v_mfma_f32_16x16x32_f16 v[110:113], v[146:149], v[196:199], v[110:113]
	v_mfma_f32_16x16x32_f16 v[106:109], v[162:165], v[196:199], v[106:109]
	v_mfma_f32_16x16x32_f16 v[94:97], v[146:149], v[204:207], v[94:97]
	v_mfma_f32_16x16x32_f16 v[90:93], v[162:165], v[204:207], v[90:93]
	v_mfma_f32_16x16x32_f16 v[78:81], v[146:149], v[212:215], v[78:81]
	v_mfma_f32_16x16x32_f16 v[74:77], v[162:165], v[212:215], v[74:77]
	v_mfma_f32_16x16x32_f16 v[126:129], v[158:161], v[192:195], v[126:129]
	v_mfma_f32_16x16x32_f16 v[122:125], v[166:169], v[192:195], v[122:125]
	v_mfma_f32_16x16x32_f16 v[110:113], v[158:161], v[200:203], v[110:113]
	v_mfma_f32_16x16x32_f16 v[106:109], v[166:169], v[200:203], v[106:109]
	v_mfma_f32_16x16x32_f16 v[94:97], v[158:161], v[208:211], v[94:97]
	v_mfma_f32_16x16x32_f16 v[90:93], v[166:169], v[208:211], v[90:93]
	v_mfma_f32_16x16x32_f16 v[78:81], v[158:161], v[216:219], v[78:81]
	v_mfma_f32_16x16x32_f16 v[74:77], v[166:169], v[216:219], v[74:77]
	s_setprio 0
	s_setprio 1
	v_mfma_f32_16x16x32_f16 v[118:121], v[170:173], v[188:191], v[118:121]
	v_mfma_f32_16x16x32_f16 v[114:117], v[178:181], v[188:191], v[114:117]
	v_mfma_f32_16x16x32_f16 v[102:105], v[170:173], v[196:199], v[102:105]
	v_mfma_f32_16x16x32_f16 v[98:101], v[178:181], v[196:199], v[98:101]
	v_mfma_f32_16x16x32_f16 v[86:89], v[170:173], v[204:207], v[86:89]
	v_mfma_f32_16x16x32_f16 v[82:85], v[178:181], v[204:207], v[82:85]
	v_mfma_f32_16x16x32_f16 v[70:73], v[170:173], v[212:215], v[70:73]
	v_mfma_f32_16x16x32_f16 v[66:69], v[178:181], v[212:215], v[66:69]
	v_mfma_f32_16x16x32_f16 v[118:121], v[174:177], v[192:195], v[118:121]
	v_mfma_f32_16x16x32_f16 v[114:117], v[182:185], v[192:195], v[114:117]
	v_mfma_f32_16x16x32_f16 v[102:105], v[174:177], v[200:203], v[102:105]
	v_mfma_f32_16x16x32_f16 v[98:101], v[182:185], v[200:203], v[98:101]
	s_setprio 2
	s_barrier
	v_mfma_f32_16x16x32_f16 v[86:89], v[174:177], v[208:211], v[86:89]
	v_mfma_f32_16x16x32_f16 v[82:85], v[182:185], v[208:211], v[82:85]
	v_mfma_f32_16x16x32_f16 v[70:73], v[174:177], v[216:219], v[70:73]
	v_mfma_f32_16x16x32_f16 v[66:69], v[182:185], v[216:219], v[66:69]
	s_setprio 0
	s_nop 0
	s_add_i32 s64, s48, s36
	v_lshl_add_u64 v[150:151], s[28:29], 0, v[132:133]
	s_mov_b32 m0, s64
	ds_read_b128 v[188:191], v156 offset:16384
	ds_read_b128 v[192:195], v156 offset:17408
	ds_read_b128 v[196:199], v156 offset:18432
	ds_read_b128 v[200:203], v156 offset:19456
	ds_read_b128 v[204:207], v156 offset:20480
	ds_read_b128 v[208:211], v156 offset:21504
	ds_read_b128 v[212:215], v156 offset:22528
	ds_read_b128 v[216:219], v156 offset:23552
	global_load_lds_dwordx4 v[150:151], off
	s_add_i32 m0, s64, 0x2000
	s_add_u32 s64, s28, 0x80000
	v_lshl_add_u64 v[220:221], s[28:29], 0, v[136:137]
	s_addc_u32 s65, s29, 0
	s_add_i32 s66, s49, s36
	global_load_lds_dwordx4 v[220:221], off
	v_lshl_add_u64 v[222:223], s[64:65], 0, v[132:133]
	s_mov_b32 m0, s66
	v_lshl_add_u64 v[224:225], s[30:31], 0, v[134:135]
	global_load_lds_dwordx4 v[222:223], off
	v_lshl_add_u64 v[222:223], s[64:65], 0, v[136:137]
	s_add_i32 m0, s66, 0x2000
	s_nop 0
	global_load_lds_dwordx4 v[222:223], off
	v_lshl_add_u64 v[222:223], s[30:31], 0, v[130:131]
	s_mov_b32 m0, s25
	s_nop 0
	global_load_lds_dwordx4 v[222:223], off
	s_mov_b32 m0, s37
	s_nop 0
	global_load_lds_dwordx4 v[224:225], off
	s_waitcnt vmcnt(8)
	s_waitcnt lgkmcnt(0)
	s_barrier
	s_setprio 1
	s_waitcnt lgkmcnt(0)
	v_mfma_f32_16x16x32_f16 v[62:65], v[146:149], v[188:191], v[62:65]
	v_mfma_f32_16x16x32_f16 v[58:61], v[162:165], v[188:191], v[58:61]
	v_mfma_f32_16x16x32_f16 v[46:49], v[146:149], v[196:199], v[46:49]
	v_mfma_f32_16x16x32_f16 v[42:45], v[162:165], v[196:199], v[42:45]
	v_mfma_f32_16x16x32_f16 v[30:33], v[146:149], v[204:207], v[30:33]
	v_mfma_f32_16x16x32_f16 v[26:29], v[162:165], v[204:207], v[26:29]
	v_mfma_f32_16x16x32_f16 v[14:17], v[146:149], v[212:215], v[14:17]
	v_mfma_f32_16x16x32_f16 v[10:13], v[162:165], v[212:215], v[10:13]
	v_mfma_f32_16x16x32_f16 v[62:65], v[158:161], v[192:195], v[62:65]
	v_mfma_f32_16x16x32_f16 v[58:61], v[166:169], v[192:195], v[58:61]
	v_mfma_f32_16x16x32_f16 v[46:49], v[158:161], v[200:203], v[46:49]
	v_mfma_f32_16x16x32_f16 v[42:45], v[166:169], v[200:203], v[42:45]
	v_mfma_f32_16x16x32_f16 v[30:33], v[158:161], v[208:211], v[30:33]
	v_mfma_f32_16x16x32_f16 v[26:29], v[166:169], v[208:211], v[26:29]
	v_mfma_f32_16x16x32_f16 v[14:17], v[158:161], v[216:219], v[14:17]
	v_mfma_f32_16x16x32_f16 v[10:13], v[166:169], v[216:219], v[10:13]
	s_setprio 0
	s_setprio 1
	v_mfma_f32_16x16x32_f16 v[54:57], v[170:173], v[188:191], v[54:57]
	v_mfma_f32_16x16x32_f16 v[50:53], v[178:181], v[188:191], v[50:53]
	v_mfma_f32_16x16x32_f16 v[38:41], v[170:173], v[196:199], v[38:41]
	v_mfma_f32_16x16x32_f16 v[34:37], v[178:181], v[196:199], v[34:37]
	v_mfma_f32_16x16x32_f16 v[22:25], v[170:173], v[204:207], v[22:25]
	v_mfma_f32_16x16x32_f16 v[18:21], v[178:181], v[204:207], v[18:21]
	v_mfma_f32_16x16x32_f16 v[6:9], v[170:173], v[212:215], v[6:9]
	v_mfma_f32_16x16x32_f16 v[2:5], v[178:181], v[212:215], v[2:5]
	v_mfma_f32_16x16x32_f16 v[54:57], v[174:177], v[192:195], v[54:57]
	v_mfma_f32_16x16x32_f16 v[50:53], v[182:185], v[192:195], v[50:53]
	v_mfma_f32_16x16x32_f16 v[38:41], v[174:177], v[200:203], v[38:41]
	v_mfma_f32_16x16x32_f16 v[34:37], v[182:185], v[200:203], v[34:37]
	s_setprio 2
	s_barrier
	v_mfma_f32_16x16x32_f16 v[22:25], v[174:177], v[208:211], v[22:25]
	v_mfma_f32_16x16x32_f16 v[18:21], v[182:185], v[208:211], v[18:21]
	v_mfma_f32_16x16x32_f16 v[6:9], v[174:177], v[216:219], v[6:9]
	v_mfma_f32_16x16x32_f16 v[2:5], v[182:185], v[216:219], v[2:5]
	s_setprio 0
	s_nop 0
	s_add_i32 s64, 0, 0x18000
	v_add_u32_e32 v157, s64, v152
	s_add_i32 s65, 0, 0x1c000
	ds_read_b128 v[146:149], v157
	ds_read_b128 v[158:161], v157 offset:1024
	ds_read_b128 v[162:165], v157 offset:2048
	ds_read_b128 v[166:169], v157 offset:3072
	v_add_u32_e32 v157, s65, v152
	ds_read_b128 v[170:173], v157
	ds_read_b128 v[174:177], v157 offset:1024
	ds_read_b128 v[178:181], v157 offset:2048
	ds_read_b128 v[182:185], v157 offset:3072
	s_add_u32 s30, s30, 0x80000
	s_addc_u32 s31, s31, 0
	s_mov_b32 m0, s38
	v_lshl_add_u64 v[226:227], s[30:31], 0, v[130:131]
	ds_read_b128 v[188:191], v156 offset:32768
	ds_read_b128 v[192:195], v156 offset:33792
	ds_read_b128 v[196:199], v156 offset:34816
	ds_read_b128 v[200:203], v156 offset:35840
	ds_read_b128 v[204:207], v156 offset:36864
	ds_read_b128 v[208:211], v156 offset:37888
	ds_read_b128 v[212:215], v156 offset:38912
	ds_read_b128 v[216:219], v156 offset:39936
	global_load_lds_dwordx4 v[226:227], off
	v_lshl_add_u64 v[226:227], s[30:31], 0, v[134:135]
	s_mov_b32 m0, s39
	s_nop 0
	global_load_lds_dwordx4 v[226:227], off
	s_waitcnt vmcnt(8)
	s_waitcnt lgkmcnt(0)
	s_barrier
	s_setprio 1
	s_waitcnt lgkmcnt(0)
	v_mfma_f32_16x16x32_f16 v[126:129], v[146:149], v[188:191], v[126:129]
	v_mfma_f32_16x16x32_f16 v[122:125], v[162:165], v[188:191], v[122:125]
	v_mfma_f32_16x16x32_f16 v[110:113], v[146:149], v[196:199], v[110:113]
	v_mfma_f32_16x16x32_f16 v[106:109], v[162:165], v[196:199], v[106:109]
	v_mfma_f32_16x16x32_f16 v[94:97], v[146:149], v[204:207], v[94:97]
	v_mfma_f32_16x16x32_f16 v[90:93], v[162:165], v[204:207], v[90:93]
	v_mfma_f32_16x16x32_f16 v[78:81], v[146:149], v[212:215], v[78:81]
	v_mfma_f32_16x16x32_f16 v[74:77], v[162:165], v[212:215], v[74:77]
	v_mfma_f32_16x16x32_f16 v[126:129], v[158:161], v[192:195], v[126:129]
	v_mfma_f32_16x16x32_f16 v[122:125], v[166:169], v[192:195], v[122:125]
	v_mfma_f32_16x16x32_f16 v[110:113], v[158:161], v[200:203], v[110:113]
	v_mfma_f32_16x16x32_f16 v[106:109], v[166:169], v[200:203], v[106:109]
	v_mfma_f32_16x16x32_f16 v[94:97], v[158:161], v[208:211], v[94:97]
	v_mfma_f32_16x16x32_f16 v[90:93], v[166:169], v[208:211], v[90:93]
	v_mfma_f32_16x16x32_f16 v[78:81], v[158:161], v[216:219], v[78:81]
	v_mfma_f32_16x16x32_f16 v[74:77], v[166:169], v[216:219], v[74:77]
	s_setprio 0
	s_setprio 1
	v_mfma_f32_16x16x32_f16 v[118:121], v[170:173], v[188:191], v[118:121]
	v_mfma_f32_16x16x32_f16 v[114:117], v[178:181], v[188:191], v[114:117]
	v_mfma_f32_16x16x32_f16 v[102:105], v[170:173], v[196:199], v[102:105]
	v_mfma_f32_16x16x32_f16 v[98:101], v[178:181], v[196:199], v[98:101]
	v_mfma_f32_16x16x32_f16 v[86:89], v[170:173], v[204:207], v[86:89]
	v_mfma_f32_16x16x32_f16 v[82:85], v[178:181], v[204:207], v[82:85]
	v_mfma_f32_16x16x32_f16 v[70:73], v[170:173], v[212:215], v[70:73]
	v_mfma_f32_16x16x32_f16 v[66:69], v[178:181], v[212:215], v[66:69]
	v_mfma_f32_16x16x32_f16 v[118:121], v[174:177], v[192:195], v[118:121]
	v_mfma_f32_16x16x32_f16 v[114:117], v[182:185], v[192:195], v[114:117]
	v_mfma_f32_16x16x32_f16 v[102:105], v[174:177], v[200:203], v[102:105]
	v_mfma_f32_16x16x32_f16 v[98:101], v[182:185], v[200:203], v[98:101]
	s_setprio 2
	s_barrier
	v_mfma_f32_16x16x32_f16 v[86:89], v[174:177], v[208:211], v[86:89]
	v_mfma_f32_16x16x32_f16 v[82:85], v[182:185], v[208:211], v[82:85]
	v_mfma_f32_16x16x32_f16 v[70:73], v[174:177], v[216:219], v[70:73]
	v_mfma_f32_16x16x32_f16 v[66:69], v[182:185], v[216:219], v[66:69]
	s_setprio 0
	s_nop 0
	s_add_i32 s30, s64, s36
	v_lshl_add_u64 v[150:151], v[150:151], 0, s[10:11]
	s_mov_b32 m0, s30
	ds_read_b128 v[188:191], v156 offset:49152
	ds_read_b128 v[192:195], v156 offset:50176
	ds_read_b128 v[196:199], v156 offset:51200
	ds_read_b128 v[200:203], v156 offset:52224
	ds_read_b128 v[204:207], v156 offset:53248
	ds_read_b128 v[208:211], v156 offset:54272
	ds_read_b128 v[212:215], v156 offset:55296
	ds_read_b128 v[216:219], v156 offset:56320
	global_load_lds_dwordx4 v[150:151], off
	s_add_i32 m0, s30, 0x2000
	s_add_u32 s28, s28, 0x80080
	v_lshl_add_u64 v[150:151], v[220:221], 0, s[10:11]
	s_addc_u32 s29, s29, 0
	s_add_i32 s30, s65, s36
	global_load_lds_dwordx4 v[150:151], off
	v_lshl_add_u64 v[150:151], s[28:29], 0, v[132:133]
	s_mov_b32 m0, s30
	s_nop 0
	global_load_lds_dwordx4 v[150:151], off
	v_lshl_add_u64 v[150:151], s[28:29], 0, v[136:137]
	s_add_i32 m0, s30, 0x2000
	s_nop 0
	global_load_lds_dwordx4 v[150:151], off
	v_lshl_add_u64 v[150:151], v[222:223], 0, s[10:11]
	s_mov_b32 m0, s41
	s_nop 0
	global_load_lds_dwordx4 v[150:151], off
	v_lshl_add_u64 v[150:151], v[224:225], 0, s[10:11]
	s_mov_b32 m0, s46
	s_nop 0
	global_load_lds_dwordx4 v[150:151], off
	s_waitcnt vmcnt(8)
	s_waitcnt lgkmcnt(0)
	s_barrier
	s_setprio 1
	s_waitcnt lgkmcnt(0)
	v_mfma_f32_16x16x32_f16 v[62:65], v[146:149], v[188:191], v[62:65]
	v_mfma_f32_16x16x32_f16 v[58:61], v[162:165], v[188:191], v[58:61]
	v_mfma_f32_16x16x32_f16 v[46:49], v[146:149], v[196:199], v[46:49]
	v_mfma_f32_16x16x32_f16 v[42:45], v[162:165], v[196:199], v[42:45]
	v_mfma_f32_16x16x32_f16 v[30:33], v[146:149], v[204:207], v[30:33]
	v_mfma_f32_16x16x32_f16 v[26:29], v[162:165], v[204:207], v[26:29]
	v_mfma_f32_16x16x32_f16 v[14:17], v[146:149], v[212:215], v[14:17]
	v_mfma_f32_16x16x32_f16 v[10:13], v[162:165], v[212:215], v[10:13]
	v_mfma_f32_16x16x32_f16 v[62:65], v[158:161], v[192:195], v[62:65]
	v_mfma_f32_16x16x32_f16 v[58:61], v[166:169], v[192:195], v[58:61]
	v_mfma_f32_16x16x32_f16 v[46:49], v[158:161], v[200:203], v[46:49]
	v_mfma_f32_16x16x32_f16 v[42:45], v[166:169], v[200:203], v[42:45]
	v_mfma_f32_16x16x32_f16 v[30:33], v[158:161], v[208:211], v[30:33]
	v_mfma_f32_16x16x32_f16 v[26:29], v[166:169], v[208:211], v[26:29]
	v_mfma_f32_16x16x32_f16 v[14:17], v[158:161], v[216:219], v[14:17]
	v_mfma_f32_16x16x32_f16 v[10:13], v[166:169], v[216:219], v[10:13]
	s_setprio 0
	s_setprio 1
	v_mfma_f32_16x16x32_f16 v[54:57], v[170:173], v[188:191], v[54:57]
	v_mfma_f32_16x16x32_f16 v[50:53], v[178:181], v[188:191], v[50:53]
	v_mfma_f32_16x16x32_f16 v[38:41], v[170:173], v[196:199], v[38:41]
	v_mfma_f32_16x16x32_f16 v[34:37], v[178:181], v[196:199], v[34:37]
	v_mfma_f32_16x16x32_f16 v[22:25], v[170:173], v[204:207], v[22:25]
	v_mfma_f32_16x16x32_f16 v[18:21], v[178:181], v[204:207], v[18:21]
	v_mfma_f32_16x16x32_f16 v[6:9], v[170:173], v[212:215], v[6:9]
	v_mfma_f32_16x16x32_f16 v[2:5], v[178:181], v[212:215], v[2:5]
	v_mfma_f32_16x16x32_f16 v[54:57], v[174:177], v[192:195], v[54:57]
	v_mfma_f32_16x16x32_f16 v[50:53], v[182:185], v[192:195], v[50:53]
	v_mfma_f32_16x16x32_f16 v[38:41], v[174:177], v[200:203], v[38:41]
	v_mfma_f32_16x16x32_f16 v[34:37], v[182:185], v[200:203], v[34:37]
	s_setprio 2
	s_barrier
	v_mfma_f32_16x16x32_f16 v[22:25], v[174:177], v[208:211], v[22:25]
	v_mfma_f32_16x16x32_f16 v[18:21], v[182:185], v[208:211], v[18:21]
	v_mfma_f32_16x16x32_f16 v[6:9], v[174:177], v[216:219], v[6:9]
	v_mfma_f32_16x16x32_f16 v[2:5], v[182:185], v[216:219], v[2:5]
	s_setprio 0
	s_nop 0
	s_add_i32 s63, s63, 2
	s_add_u32 s26, s26, 0x100
	s_addc_u32 s27, s27, 0
	s_add_u32 s61, s61, 0x100
	s_addc_u32 s62, s62, 0
	s_cmp_gt_u32 s63, 29
	s_cbranch_scc0 .LBB0_628
	s_and_b64 vcc, exec, s[12:13]
	s_cbranch_vccz .LBB0_631
	s_barrier

.LBB0_758:
	ds_read_b128 v[146:149], v152
	ds_read_b128 v[156:159], v152 offset:1024
	ds_read_b128 v[160:163], v152 offset:2048
	ds_read_b128 v[164:167], v152 offset:3072
	ds_read_b128 v[168:171], v153
	ds_read_b128 v[172:175], v153 offset:1024
	ds_read_b128 v[176:179], v153 offset:2048
	ds_read_b128 v[180:183], v153 offset:3072
	s_add_u32 s28, s26, 0xfff80080
	s_addc_u32 s29, s27, -1
	s_cmp_eq_u32 s61, 28
	s_cselect_b32 s31, s19, s29
	s_cselect_b32 s30, s49, s28
	s_cselect_b32 s29, s17, s60
	s_cselect_b32 s28, s50, s51
	v_lshl_add_u64 v[184:185], s[26:27], 0, v[138:139]
	s_add_i32 m0, s25, 0xc000
	ds_read_b128 v[188:191], v154
	ds_read_b128 v[192:195], v154 offset:1024
	ds_read_b128 v[196:199], v154 offset:2048
	ds_read_b128 v[200:203], v154 offset:3072
	ds_read_b128 v[204:207], v154 offset:4096
	ds_read_b128 v[208:211], v154 offset:5120
	ds_read_b128 v[212:215], v154 offset:6144
	ds_read_b128 v[216:219], v154 offset:7168
	global_load_lds_dwordx4 v[184:185], off
	v_lshl_add_u64 v[184:185], s[26:27], 0, v[140:141]
	s_add_i32 m0, s25, 0xe000
	s_nop 0
	global_load_lds_dwordx4 v[184:185], off
	s_waitcnt vmcnt(8)
	s_waitcnt lgkmcnt(0)
	s_barrier
	s_setprio 1
	s_waitcnt lgkmcnt(0)
	v_mfma_f32_16x16x32_f16 v[126:129], v[146:149], v[188:191], v[126:129]
	v_mfma_f32_16x16x32_f16 v[122:125], v[160:163], v[188:191], v[122:125]
	v_mfma_f32_16x16x32_f16 v[110:113], v[146:149], v[196:199], v[110:113]
	v_mfma_f32_16x16x32_f16 v[106:109], v[160:163], v[196:199], v[106:109]
	v_mfma_f32_16x16x32_f16 v[94:97], v[146:149], v[204:207], v[94:97]
	v_mfma_f32_16x16x32_f16 v[90:93], v[160:163], v[204:207], v[90:93]
	v_mfma_f32_16x16x32_f16 v[78:81], v[146:149], v[212:215], v[78:81]
	v_mfma_f32_16x16x32_f16 v[74:77], v[160:163], v[212:215], v[74:77]
	v_mfma_f32_16x16x32_f16 v[126:129], v[156:159], v[192:195], v[126:129]
	v_mfma_f32_16x16x32_f16 v[122:125], v[164:167], v[192:195], v[122:125]
	v_mfma_f32_16x16x32_f16 v[110:113], v[156:159], v[200:203], v[110:113]
	v_mfma_f32_16x16x32_f16 v[106:109], v[164:167], v[200:203], v[106:109]
	v_mfma_f32_16x16x32_f16 v[94:97], v[156:159], v[208:211], v[94:97]
	v_mfma_f32_16x16x32_f16 v[90:93], v[164:167], v[208:211], v[90:93]
	v_mfma_f32_16x16x32_f16 v[78:81], v[156:159], v[216:219], v[78:81]
	v_mfma_f32_16x16x32_f16 v[74:77], v[164:167], v[216:219], v[74:77]
	s_setprio 0
	s_setprio 1
	v_mfma_f32_16x16x32_f16 v[118:121], v[168:171], v[188:191], v[118:121]
	v_mfma_f32_16x16x32_f16 v[114:117], v[176:179], v[188:191], v[114:117]
	v_mfma_f32_16x16x32_f16 v[102:105], v[168:171], v[196:199], v[102:105]
	v_mfma_f32_16x16x32_f16 v[98:101], v[176:179], v[196:199], v[98:101]
	v_mfma_f32_16x16x32_f16 v[86:89], v[168:171], v[204:207], v[86:89]
	v_mfma_f32_16x16x32_f16 v[82:85], v[176:179], v[204:207], v[82:85]
	v_mfma_f32_16x16x32_f16 v[70:73], v[168:171], v[212:215], v[70:73]
	v_mfma_f32_16x16x32_f16 v[66:69], v[176:179], v[212:215], v[66:69]
	v_mfma_f32_16x16x32_f16 v[118:121], v[172:175], v[192:195], v[118:121]
	v_mfma_f32_16x16x32_f16 v[114:117], v[180:183], v[192:195], v[114:117]
	v_mfma_f32_16x16x32_f16 v[102:105], v[172:175], v[200:203], v[102:105]
	v_mfma_f32_16x16x32_f16 v[98:101], v[180:183], v[200:203], v[98:101]
	s_setprio 2
	s_barrier
	v_mfma_f32_16x16x32_f16 v[86:89], v[172:175], v[208:211], v[86:89]
	v_mfma_f32_16x16x32_f16 v[82:85], v[180:183], v[208:211], v[82:85]
	v_mfma_f32_16x16x32_f16 v[70:73], v[172:175], v[216:219], v[70:73]
	v_mfma_f32_16x16x32_f16 v[66:69], v[180:183], v[216:219], v[66:69]
	s_setprio 0
	s_nop 0
	s_add_i32 s62, s44, s34
	v_lshl_add_u64 v[184:185], s[28:29], 0, v[134:135]
	s_mov_b32 m0, s62
	ds_read_b128 v[188:191], v154 offset:16384
	ds_read_b128 v[192:195], v154 offset:17408
	ds_read_b128 v[196:199], v154 offset:18432
	ds_read_b128 v[200:203], v154 offset:19456
	ds_read_b128 v[204:207], v154 offset:20480
	ds_read_b128 v[208:211], v154 offset:21504
	ds_read_b128 v[212:215], v154 offset:22528
	ds_read_b128 v[216:219], v154 offset:23552
	global_load_lds_dwordx4 v[184:185], off
	s_add_i32 m0, s62, 0x2000
	s_add_u32 s62, s28, 0x80000
	v_lshl_add_u64 v[220:221], s[28:29], 0, v[130:131]
	s_addc_u32 s63, s29, 0
	s_add_i32 s64, s45, s34
	global_load_lds_dwordx4 v[220:221], off
	v_lshl_add_u64 v[222:223], s[62:63], 0, v[134:135]
	s_mov_b32 m0, s64
	v_lshl_add_u64 v[224:225], s[30:31], 0, v[132:133]
	global_load_lds_dwordx4 v[222:223], off
	v_lshl_add_u64 v[222:223], s[62:63], 0, v[130:131]
	s_add_i32 m0, s64, 0x2000
	s_nop 0
	global_load_lds_dwordx4 v[222:223], off
	v_lshl_add_u64 v[222:223], s[30:31], 0, v[136:137]
	s_mov_b32 m0, s25
	s_nop 0
	global_load_lds_dwordx4 v[222:223], off
	s_mov_b32 m0, s37
	s_nop 0
	global_load_lds_dwordx4 v[224:225], off
	s_waitcnt vmcnt(8)
	s_waitcnt lgkmcnt(0)
	s_barrier
	s_setprio 1
	s_waitcnt lgkmcnt(0)
	v_mfma_f32_16x16x32_f16 v[62:65], v[146:149], v[188:191], v[62:65]
	v_mfma_f32_16x16x32_f16 v[58:61], v[160:163], v[188:191], v[58:61]
	v_mfma_f32_16x16x32_f16 v[46:49], v[146:149], v[196:199], v[46:49]
	v_mfma_f32_16x16x32_f16 v[42:45], v[160:163], v[196:199], v[42:45]
	v_mfma_f32_16x16x32_f16 v[30:33], v[146:149], v[204:207], v[30:33]
	v_mfma_f32_16x16x32_f16 v[26:29], v[160:163], v[204:207], v[26:29]
	v_mfma_f32_16x16x32_f16 v[14:17], v[146:149], v[212:215], v[14:17]
	v_mfma_f32_16x16x32_f16 v[10:13], v[160:163], v[212:215], v[10:13]
	v_mfma_f32_16x16x32_f16 v[62:65], v[156:159], v[192:195], v[62:65]
	v_mfma_f32_16x16x32_f16 v[58:61], v[164:167], v[192:195], v[58:61]
	v_mfma_f32_16x16x32_f16 v[46:49], v[156:159], v[200:203], v[46:49]
	v_mfma_f32_16x16x32_f16 v[42:45], v[164:167], v[200:203], v[42:45]
	v_mfma_f32_16x16x32_f16 v[30:33], v[156:159], v[208:211], v[30:33]
	v_mfma_f32_16x16x32_f16 v[26:29], v[164:167], v[208:211], v[26:29]
	v_mfma_f32_16x16x32_f16 v[14:17], v[156:159], v[216:219], v[14:17]
	v_mfma_f32_16x16x32_f16 v[10:13], v[164:167], v[216:219], v[10:13]
	s_setprio 0
	s_setprio 1
	v_mfma_f32_16x16x32_f16 v[54:57], v[168:171], v[188:191], v[54:57]
	v_mfma_f32_16x16x32_f16 v[50:53], v[176:179], v[188:191], v[50:53]
	v_mfma_f32_16x16x32_f16 v[38:41], v[168:171], v[196:199], v[38:41]
	v_mfma_f32_16x16x32_f16 v[34:37], v[176:179], v[196:199], v[34:37]
	v_mfma_f32_16x16x32_f16 v[22:25], v[168:171], v[204:207], v[22:25]
	v_mfma_f32_16x16x32_f16 v[18:21], v[176:179], v[204:207], v[18:21]
	v_mfma_f32_16x16x32_f16 v[6:9], v[168:171], v[212:215], v[6:9]
	v_mfma_f32_16x16x32_f16 v[2:5], v[176:179], v[212:215], v[2:5]
	v_mfma_f32_16x16x32_f16 v[54:57], v[172:175], v[192:195], v[54:57]
	v_mfma_f32_16x16x32_f16 v[50:53], v[180:183], v[192:195], v[50:53]
	v_mfma_f32_16x16x32_f16 v[38:41], v[172:175], v[200:203], v[38:41]
	v_mfma_f32_16x16x32_f16 v[34:37], v[180:183], v[200:203], v[34:37]
	s_setprio 2
	s_barrier
	v_mfma_f32_16x16x32_f16 v[22:25], v[172:175], v[208:211], v[22:25]
	v_mfma_f32_16x16x32_f16 v[18:21], v[180:183], v[208:211], v[18:21]
	v_mfma_f32_16x16x32_f16 v[6:9], v[172:175], v[216:219], v[6:9]
	v_mfma_f32_16x16x32_f16 v[2:5], v[180:183], v[216:219], v[2:5]
	s_setprio 0
	s_nop 0
	s_add_i32 s62, 0, 0x18000
	s_add_i32 s63, 0, 0x1c000
	v_add_u32_e32 v164, s62, v150
	v_add_u32_e32 v180, s63, v150
	ds_read_b128 v[146:149], v164
	ds_read_b128 v[156:159], v164 offset:1024
	ds_read_b128 v[160:163], v164 offset:2048
	ds_read_b128 v[164:167], v164 offset:3072
	ds_read_b128 v[168:171], v180
	ds_read_b128 v[172:175], v180 offset:1024
	ds_read_b128 v[176:179], v180 offset:2048
	ds_read_b128 v[180:183], v180 offset:3072
	s_add_u32 s30, s30, 0x80000
	s_addc_u32 s31, s31, 0
	s_mov_b32 m0, s38
	v_lshl_add_u64 v[226:227], s[30:31], 0, v[136:137]
	ds_read_b128 v[188:191], v154 offset:32768
	ds_read_b128 v[192:195], v154 offset:33792
	ds_read_b128 v[196:199], v154 offset:34816
	ds_read_b128 v[200:203], v154 offset:35840
	ds_read_b128 v[204:207], v154 offset:36864
	ds_read_b128 v[208:211], v154 offset:37888
	ds_read_b128 v[212:215], v154 offset:38912
	ds_read_b128 v[216:219], v154 offset:39936
	global_load_lds_dwordx4 v[226:227], off
	v_lshl_add_u64 v[226:227], s[30:31], 0, v[132:133]
	s_mov_b32 m0, s39
	s_nop 0
	global_load_lds_dwordx4 v[226:227], off
	s_waitcnt vmcnt(8)
	s_waitcnt lgkmcnt(0)
	s_barrier
	s_setprio 1
	s_waitcnt lgkmcnt(0)
	v_mfma_f32_16x16x32_f16 v[126:129], v[146:149], v[188:191], v[126:129]
	v_mfma_f32_16x16x32_f16 v[122:125], v[160:163], v[188:191], v[122:125]
	v_mfma_f32_16x16x32_f16 v[110:113], v[146:149], v[196:199], v[110:113]
	v_mfma_f32_16x16x32_f16 v[106:109], v[160:163], v[196:199], v[106:109]
	v_mfma_f32_16x16x32_f16 v[94:97], v[146:149], v[204:207], v[94:97]
	v_mfma_f32_16x16x32_f16 v[90:93], v[160:163], v[204:207], v[90:93]
	v_mfma_f32_16x16x32_f16 v[78:81], v[146:149], v[212:215], v[78:81]
	v_mfma_f32_16x16x32_f16 v[74:77], v[160:163], v[212:215], v[74:77]
	v_mfma_f32_16x16x32_f16 v[126:129], v[156:159], v[192:195], v[126:129]
	v_mfma_f32_16x16x32_f16 v[122:125], v[164:167], v[192:195], v[122:125]
	v_mfma_f32_16x16x32_f16 v[110:113], v[156:159], v[200:203], v[110:113]
	v_mfma_f32_16x16x32_f16 v[106:109], v[164:167], v[200:203], v[106:109]
	v_mfma_f32_16x16x32_f16 v[94:97], v[156:159], v[208:211], v[94:97]
	v_mfma_f32_16x16x32_f16 v[90:93], v[164:167], v[208:211], v[90:93]
	v_mfma_f32_16x16x32_f16 v[78:81], v[156:159], v[216:219], v[78:81]
	v_mfma_f32_16x16x32_f16 v[74:77], v[164:167], v[216:219], v[74:77]
	s_setprio 0
	s_setprio 1
	v_mfma_f32_16x16x32_f16 v[118:121], v[168:171], v[188:191], v[118:121]
	v_mfma_f32_16x16x32_f16 v[114:117], v[176:179], v[188:191], v[114:117]
	v_mfma_f32_16x16x32_f16 v[102:105], v[168:171], v[196:199], v[102:105]
	v_mfma_f32_16x16x32_f16 v[98:101], v[176:179], v[196:199], v[98:101]
	v_mfma_f32_16x16x32_f16 v[86:89], v[168:171], v[204:207], v[86:89]
	v_mfma_f32_16x16x32_f16 v[82:85], v[176:179], v[204:207], v[82:85]
	v_mfma_f32_16x16x32_f16 v[70:73], v[168:171], v[212:215], v[70:73]
	v_mfma_f32_16x16x32_f16 v[66:69], v[176:179], v[212:215], v[66:69]
	v_mfma_f32_16x16x32_f16 v[118:121], v[172:175], v[192:195], v[118:121]
	v_mfma_f32_16x16x32_f16 v[114:117], v[180:183], v[192:195], v[114:117]
	v_mfma_f32_16x16x32_f16 v[102:105], v[172:175], v[200:203], v[102:105]
	v_mfma_f32_16x16x32_f16 v[98:101], v[180:183], v[200:203], v[98:101]
	s_setprio 2
	s_barrier
	v_mfma_f32_16x16x32_f16 v[86:89], v[172:175], v[208:211], v[86:89]
	v_mfma_f32_16x16x32_f16 v[82:85], v[180:183], v[208:211], v[82:85]
	v_mfma_f32_16x16x32_f16 v[70:73], v[172:175], v[216:219], v[70:73]
	v_mfma_f32_16x16x32_f16 v[66:69], v[180:183], v[216:219], v[66:69]
	s_setprio 0
	s_nop 0
	s_add_i32 s30, s62, s34
	v_lshl_add_u64 v[184:185], v[184:185], 0, s[12:13]
	s_mov_b32 m0, s30
	ds_read_b128 v[188:191], v154 offset:49152
	ds_read_b128 v[192:195], v154 offset:50176
	ds_read_b128 v[196:199], v154 offset:51200
	ds_read_b128 v[200:203], v154 offset:52224
	ds_read_b128 v[204:207], v154 offset:53248
	ds_read_b128 v[208:211], v154 offset:54272
	ds_read_b128 v[212:215], v154 offset:55296
	ds_read_b128 v[216:219], v154 offset:56320
	global_load_lds_dwordx4 v[184:185], off
	s_add_i32 m0, s30, 0x2000
	s_add_u32 s28, s28, 0x80080
	v_lshl_add_u64 v[184:185], v[220:221], 0, s[12:13]
	s_addc_u32 s29, s29, 0
	s_add_i32 s30, s63, s34
	global_load_lds_dwordx4 v[184:185], off
	v_lshl_add_u64 v[184:185], s[28:29], 0, v[134:135]
	s_mov_b32 m0, s30
	s_nop 0
	global_load_lds_dwordx4 v[184:185], off
	v_lshl_add_u64 v[184:185], s[28:29], 0, v[130:131]
	s_add_i32 m0, s30, 0x2000
	s_nop 0
	global_load_lds_dwordx4 v[184:185], off
	v_lshl_add_u64 v[184:185], v[222:223], 0, s[12:13]
	s_mov_b32 m0, s41
	s_nop 0
	global_load_lds_dwordx4 v[184:185], off
	v_lshl_add_u64 v[184:185], v[224:225], 0, s[12:13]
	s_mov_b32 m0, s42
	s_nop 0
	global_load_lds_dwordx4 v[184:185], off
	s_waitcnt vmcnt(8)
	s_waitcnt lgkmcnt(0)
	s_barrier
	s_setprio 1
	s_waitcnt lgkmcnt(0)
	v_mfma_f32_16x16x32_f16 v[62:65], v[146:149], v[188:191], v[62:65]
	v_mfma_f32_16x16x32_f16 v[58:61], v[160:163], v[188:191], v[58:61]
	v_mfma_f32_16x16x32_f16 v[46:49], v[146:149], v[196:199], v[46:49]
	v_mfma_f32_16x16x32_f16 v[42:45], v[160:163], v[196:199], v[42:45]
	v_mfma_f32_16x16x32_f16 v[30:33], v[146:149], v[204:207], v[30:33]
	v_mfma_f32_16x16x32_f16 v[26:29], v[160:163], v[204:207], v[26:29]
	v_mfma_f32_16x16x32_f16 v[14:17], v[146:149], v[212:215], v[14:17]
	v_mfma_f32_16x16x32_f16 v[10:13], v[160:163], v[212:215], v[10:13]
	v_mfma_f32_16x16x32_f16 v[62:65], v[156:159], v[192:195], v[62:65]
	v_mfma_f32_16x16x32_f16 v[58:61], v[164:167], v[192:195], v[58:61]
	v_mfma_f32_16x16x32_f16 v[46:49], v[156:159], v[200:203], v[46:49]
	v_mfma_f32_16x16x32_f16 v[42:45], v[164:167], v[200:203], v[42:45]
	v_mfma_f32_16x16x32_f16 v[30:33], v[156:159], v[208:211], v[30:33]
	v_mfma_f32_16x16x32_f16 v[26:29], v[164:167], v[208:211], v[26:29]
	v_mfma_f32_16x16x32_f16 v[14:17], v[156:159], v[216:219], v[14:17]
	v_mfma_f32_16x16x32_f16 v[10:13], v[164:167], v[216:219], v[10:13]
	s_setprio 0
	s_setprio 1
	v_mfma_f32_16x16x32_f16 v[54:57], v[168:171], v[188:191], v[54:57]
	v_mfma_f32_16x16x32_f16 v[50:53], v[176:179], v[188:191], v[50:53]
	v_mfma_f32_16x16x32_f16 v[38:41], v[168:171], v[196:199], v[38:41]
	v_mfma_f32_16x16x32_f16 v[34:37], v[176:179], v[196:199], v[34:37]
	v_mfma_f32_16x16x32_f16 v[22:25], v[168:171], v[204:207], v[22:25]
	v_mfma_f32_16x16x32_f16 v[18:21], v[176:179], v[204:207], v[18:21]
	v_mfma_f32_16x16x32_f16 v[6:9], v[168:171], v[212:215], v[6:9]
	v_mfma_f32_16x16x32_f16 v[2:5], v[176:179], v[212:215], v[2:5]
	v_mfma_f32_16x16x32_f16 v[54:57], v[172:175], v[192:195], v[54:57]
	v_mfma_f32_16x16x32_f16 v[50:53], v[180:183], v[192:195], v[50:53]
	v_mfma_f32_16x16x32_f16 v[38:41], v[172:175], v[200:203], v[38:41]
	v_mfma_f32_16x16x32_f16 v[34:37], v[180:183], v[200:203], v[34:37]
	s_setprio 2
	s_barrier
	v_mfma_f32_16x16x32_f16 v[22:25], v[172:175], v[208:211], v[22:25]
	v_mfma_f32_16x16x32_f16 v[18:21], v[180:183], v[208:211], v[18:21]
	v_mfma_f32_16x16x32_f16 v[6:9], v[172:175], v[216:219], v[6:9]
	v_mfma_f32_16x16x32_f16 v[2:5], v[180:183], v[216:219], v[2:5]
	s_setprio 0
	s_nop 0
	s_add_i32 s61, s61, 2
	s_add_u32 s26, s26, 0x100
	s_addc_u32 s27, s27, 0
	s_add_u32 s51, s51, 0x100
	s_addc_u32 s60, s60, 0
	s_cmp_gt_u32 s61, 29
	s_cbranch_scc0 .LBB0_758
	s_and_b64 vcc, exec, s[14:15]
	s_cbranch_vccz .LBB0_761
	s_barrier

.LBB0_841:
	ds_read_b128 v[26:29], v190
	ds_read_b128 v[30:33], v190 offset:1024
	ds_read_b128 v[18:21], v190 offset:2048
	ds_read_b128 v[22:25], v190 offset:3072
	ds_read_b128 v[10:13], v191
	ds_read_b128 v[14:17], v191 offset:1024
	ds_read_b128 v[2:5], v191 offset:2048
	ds_read_b128 v[6:9], v191 offset:3072
	s_add_u32 s24, s22, 0xfff50080
	s_addc_u32 s25, s23, -1
	s_cmp_eq_u32 s48, 40
	s_cselect_b32 s27, s9, s25
	s_cselect_b32 s26, s8, s24
	s_cselect_b32 s25, s21, s47
	s_cselect_b32 s24, s20, s46
	v_lshl_add_u64 v[218:219], s[22:23], 0, v[170:171]
	s_add_i32 m0, s31, 0xc000
	ds_read_b128 v[178:181], v192
	ds_read_b128 v[182:185], v192 offset:1024
	ds_read_b128 v[194:197], v192 offset:2048
	ds_read_b128 v[198:201], v192 offset:3072
	ds_read_b128 v[202:205], v192 offset:4096
	ds_read_b128 v[206:209], v192 offset:5120
	ds_read_b128 v[210:213], v192 offset:6144
	ds_read_b128 v[214:217], v192 offset:7168
	global_load_lds_dwordx4 v[218:219], off
	v_lshl_add_u64 v[218:219], s[22:23], 0, v[172:173]
	s_add_i32 m0, s31, 0xe000
	s_nop 0
	global_load_lds_dwordx4 v[218:219], off
	s_waitcnt vmcnt(8)
	s_waitcnt lgkmcnt(0)
	s_barrier
	s_setprio 1
	s_waitcnt lgkmcnt(0)
	v_mfma_scale_f32_16x16x128_f8f6f4 v[158:161], v[26:33], v[178:185], v[158:161], v1, v1 op_sel_hi:[0,0,0]
	v_mfma_scale_f32_16x16x128_f8f6f4 v[154:157], v[18:25], v[178:185], v[154:157], v1, v1 op_sel_hi:[0,0,0]
	v_mfma_scale_f32_16x16x128_f8f6f4 v[142:145], v[26:33], v[194:201], v[142:145], v1, v1 op_sel_hi:[0,0,0]
	v_mfma_scale_f32_16x16x128_f8f6f4 v[138:141], v[18:25], v[194:201], v[138:141], v1, v1 op_sel_hi:[0,0,0]
	v_mfma_scale_f32_16x16x128_f8f6f4 v[126:129], v[26:33], v[202:209], v[126:129], v1, v1 op_sel_hi:[0,0,0]
	v_mfma_scale_f32_16x16x128_f8f6f4 v[122:125], v[18:25], v[202:209], v[122:125], v1, v1 op_sel_hi:[0,0,0]
	v_mfma_scale_f32_16x16x128_f8f6f4 v[110:113], v[26:33], v[210:217], v[110:113], v1, v1 op_sel_hi:[0,0,0]
	v_mfma_scale_f32_16x16x128_f8f6f4 v[106:109], v[18:25], v[210:217], v[106:109], v1, v1 op_sel_hi:[0,0,0]
	s_setprio 0
	s_setprio 1
	v_mfma_scale_f32_16x16x128_f8f6f4 v[150:153], v[10:17], v[178:185], v[150:153], v1, v1 op_sel_hi:[0,0,0]
	v_mfma_scale_f32_16x16x128_f8f6f4 v[146:149], v[2:9], v[178:185], v[146:149], v1, v1 op_sel_hi:[0,0,0]
	v_mfma_scale_f32_16x16x128_f8f6f4 v[134:137], v[10:17], v[194:201], v[134:137], v1, v1 op_sel_hi:[0,0,0]
	v_mfma_scale_f32_16x16x128_f8f6f4 v[130:133], v[2:9], v[194:201], v[130:133], v1, v1 op_sel_hi:[0,0,0]
	v_mfma_scale_f32_16x16x128_f8f6f4 v[118:121], v[10:17], v[202:209], v[118:121], v1, v1 op_sel_hi:[0,0,0]
	v_mfma_scale_f32_16x16x128_f8f6f4 v[114:117], v[2:9], v[202:209], v[114:117], v1, v1 op_sel_hi:[0,0,0]
	s_setprio 2
	s_barrier
	v_mfma_scale_f32_16x16x128_f8f6f4 v[102:105], v[10:17], v[210:217], v[102:105], v1, v1 op_sel_hi:[0,0,0]
	v_mfma_scale_f32_16x16x128_f8f6f4 v[98:101], v[2:9], v[210:217], v[98:101], v1, v1 op_sel_hi:[0,0,0]
	s_setprio 0
	s_nop 0
	s_add_i32 s49, s40, s30
	v_lshl_add_u64 v[178:179], s[24:25], 0, v[164:165]
	s_mov_b32 m0, s49
	ds_read_b128 v[194:197], v192 offset:16384
	ds_read_b128 v[198:201], v192 offset:17408
	ds_read_b128 v[202:205], v192 offset:18432
	ds_read_b128 v[206:209], v192 offset:19456
	ds_read_b128 v[210:213], v192 offset:20480
	ds_read_b128 v[214:217], v192 offset:21504
	ds_read_b128 v[218:221], v192 offset:22528
	ds_read_b128 v[222:225], v192 offset:23552
	global_load_lds_dwordx4 v[178:179], off
	s_add_i32 m0, s49, 0x2000
	s_add_u32 s50, s24, 0xb0000
	v_lshl_add_u64 v[180:181], s[24:25], 0, v[168:169]
	s_addc_u32 s51, s25, 0
	s_add_i32 s49, s41, s30
	global_load_lds_dwordx4 v[180:181], off
	v_lshl_add_u64 v[182:183], s[50:51], 0, v[164:165]
	s_mov_b32 m0, s49
	v_lshl_add_u64 v[184:185], s[26:27], 0, v[166:167]
	global_load_lds_dwordx4 v[182:183], off
	v_lshl_add_u64 v[182:183], s[50:51], 0, v[168:169]
	s_add_i32 m0, s49, 0x2000
	s_nop 0
	global_load_lds_dwordx4 v[182:183], off
	v_lshl_add_u64 v[182:183], s[26:27], 0, v[162:163]
	s_mov_b32 m0, s31
	s_nop 0
	global_load_lds_dwordx4 v[182:183], off
	s_mov_b32 m0, s33
	s_nop 0
	global_load_lds_dwordx4 v[184:185], off
	s_waitcnt vmcnt(8)
	s_waitcnt lgkmcnt(0)
	s_barrier
	s_setprio 1
	s_waitcnt lgkmcnt(0)
	v_mfma_scale_f32_16x16x128_f8f6f4 v[94:97], v[26:33], v[194:201], v[94:97], v1, v1 op_sel_hi:[0,0,0]
	v_mfma_scale_f32_16x16x128_f8f6f4 v[90:93], v[18:25], v[194:201], v[90:93], v1, v1 op_sel_hi:[0,0,0]
	v_mfma_scale_f32_16x16x128_f8f6f4 v[78:81], v[26:33], v[202:209], v[78:81], v1, v1 op_sel_hi:[0,0,0]
	v_mfma_scale_f32_16x16x128_f8f6f4 v[74:77], v[18:25], v[202:209], v[74:77], v1, v1 op_sel_hi:[0,0,0]
	v_mfma_scale_f32_16x16x128_f8f6f4 v[62:65], v[26:33], v[210:217], v[62:65], v1, v1 op_sel_hi:[0,0,0]
	v_mfma_scale_f32_16x16x128_f8f6f4 v[58:61], v[18:25], v[210:217], v[58:61], v1, v1 op_sel_hi:[0,0,0]
	v_mfma_scale_f32_16x16x128_f8f6f4 v[46:49], v[26:33], v[218:225], v[46:49], v1, v1 op_sel_hi:[0,0,0]
	v_mfma_scale_f32_16x16x128_f8f6f4 v[42:45], v[18:25], v[218:225], v[42:45], v1, v1 op_sel_hi:[0,0,0]
	s_setprio 0
	s_setprio 1
	v_mfma_scale_f32_16x16x128_f8f6f4 v[86:89], v[10:17], v[194:201], v[86:89], v1, v1 op_sel_hi:[0,0,0]
	v_mfma_scale_f32_16x16x128_f8f6f4 v[82:85], v[2:9], v[194:201], v[82:85], v1, v1 op_sel_hi:[0,0,0]
	v_mfma_scale_f32_16x16x128_f8f6f4 v[70:73], v[10:17], v[202:209], v[70:73], v1, v1 op_sel_hi:[0,0,0]
	v_mfma_scale_f32_16x16x128_f8f6f4 v[66:69], v[2:9], v[202:209], v[66:69], v1, v1 op_sel_hi:[0,0,0]
	v_mfma_scale_f32_16x16x128_f8f6f4 v[54:57], v[10:17], v[210:217], v[54:57], v1, v1 op_sel_hi:[0,0,0]
	v_mfma_scale_f32_16x16x128_f8f6f4 v[50:53], v[2:9], v[210:217], v[50:53], v1, v1 op_sel_hi:[0,0,0]
	s_setprio 2
	s_barrier
	v_mfma_scale_f32_16x16x128_f8f6f4 v[38:41], v[10:17], v[218:225], v[38:41], v1, v1 op_sel_hi:[0,0,0]
	v_mfma_scale_f32_16x16x128_f8f6f4 v[34:37], v[2:9], v[218:225], v[34:37], v1, v1 op_sel_hi:[0,0,0]
	s_setprio 0
	s_nop 0
	s_add_i32 s49, 0, 0x18000
	s_add_i32 s50, 0, 0x1c000
	v_add_u32_e32 v14, s49, v188
	v_add_u32_e32 v30, s50, v188
	ds_read_b128 v[2:5], v14
	ds_read_b128 v[6:9], v14 offset:1024
	ds_read_b128 v[10:13], v14 offset:2048
	ds_read_b128 v[14:17], v14 offset:3072
	ds_read_b128 v[18:21], v30
	ds_read_b128 v[22:25], v30 offset:1024
	ds_read_b128 v[26:29], v30 offset:2048
	ds_read_b128 v[30:33], v30 offset:3072
	s_add_u32 s26, s26, 0xb0000
	s_addc_u32 s27, s27, 0
	s_mov_b32 m0, s34
	v_lshl_add_u64 v[226:227], s[26:27], 0, v[162:163]
	ds_read_b128 v[194:197], v192 offset:32768
	ds_read_b128 v[198:201], v192 offset:33792
	ds_read_b128 v[202:205], v192 offset:34816
	ds_read_b128 v[206:209], v192 offset:35840
	ds_read_b128 v[210:213], v192 offset:36864
	ds_read_b128 v[214:217], v192 offset:37888
	ds_read_b128 v[218:221], v192 offset:38912
	ds_read_b128 v[222:225], v192 offset:39936
	global_load_lds_dwordx4 v[226:227], off
	v_lshl_add_u64 v[226:227], s[26:27], 0, v[166:167]
	s_mov_b32 m0, s35
	s_nop 0
	global_load_lds_dwordx4 v[226:227], off
	s_waitcnt vmcnt(8)
	s_waitcnt lgkmcnt(0)
	s_barrier
	s_setprio 1
	s_waitcnt lgkmcnt(0)
	v_mfma_scale_f32_16x16x128_f8f6f4 v[158:161], v[2:9], v[194:201], v[158:161], v1, v1 op_sel_hi:[0,0,0]
	v_mfma_scale_f32_16x16x128_f8f6f4 v[154:157], v[10:17], v[194:201], v[154:157], v1, v1 op_sel_hi:[0,0,0]
	v_mfma_scale_f32_16x16x128_f8f6f4 v[142:145], v[2:9], v[202:209], v[142:145], v1, v1 op_sel_hi:[0,0,0]
	v_mfma_scale_f32_16x16x128_f8f6f4 v[138:141], v[10:17], v[202:209], v[138:141], v1, v1 op_sel_hi:[0,0,0]
	v_mfma_scale_f32_16x16x128_f8f6f4 v[126:129], v[2:9], v[210:217], v[126:129], v1, v1 op_sel_hi:[0,0,0]
	v_mfma_scale_f32_16x16x128_f8f6f4 v[122:125], v[10:17], v[210:217], v[122:125], v1, v1 op_sel_hi:[0,0,0]
	v_mfma_scale_f32_16x16x128_f8f6f4 v[110:113], v[2:9], v[218:225], v[110:113], v1, v1 op_sel_hi:[0,0,0]
	v_mfma_scale_f32_16x16x128_f8f6f4 v[106:109], v[10:17], v[218:225], v[106:109], v1, v1 op_sel_hi:[0,0,0]
	s_setprio 0
	s_setprio 1
	v_mfma_scale_f32_16x16x128_f8f6f4 v[150:153], v[18:25], v[194:201], v[150:153], v1, v1 op_sel_hi:[0,0,0]
	v_mfma_scale_f32_16x16x128_f8f6f4 v[146:149], v[26:33], v[194:201], v[146:149], v1, v1 op_sel_hi:[0,0,0]
	v_mfma_scale_f32_16x16x128_f8f6f4 v[134:137], v[18:25], v[202:209], v[134:137], v1, v1 op_sel_hi:[0,0,0]
	v_mfma_scale_f32_16x16x128_f8f6f4 v[130:133], v[26:33], v[202:209], v[130:133], v1, v1 op_sel_hi:[0,0,0]
	v_mfma_scale_f32_16x16x128_f8f6f4 v[118:121], v[18:25], v[210:217], v[118:121], v1, v1 op_sel_hi:[0,0,0]
	v_mfma_scale_f32_16x16x128_f8f6f4 v[114:117], v[26:33], v[210:217], v[114:117], v1, v1 op_sel_hi:[0,0,0]
	s_setprio 2
	s_barrier
	v_mfma_scale_f32_16x16x128_f8f6f4 v[102:105], v[18:25], v[218:225], v[102:105], v1, v1 op_sel_hi:[0,0,0]
	v_mfma_scale_f32_16x16x128_f8f6f4 v[98:101], v[26:33], v[218:225], v[98:101], v1, v1 op_sel_hi:[0,0,0]
	s_setprio 0
	s_nop 0
	s_add_i32 s26, s49, s30
	v_lshl_add_u64 v[178:179], v[178:179], 0, s[12:13]
	s_mov_b32 m0, s26
	ds_read_b128 v[194:197], v192 offset:49152
	ds_read_b128 v[198:201], v192 offset:50176
	ds_read_b128 v[202:205], v192 offset:51200
	ds_read_b128 v[206:209], v192 offset:52224
	ds_read_b128 v[210:213], v192 offset:53248
	ds_read_b128 v[214:217], v192 offset:54272
	ds_read_b128 v[218:221], v192 offset:55296
	ds_read_b128 v[222:225], v192 offset:56320
	global_load_lds_dwordx4 v[178:179], off
	s_add_i32 m0, s26, 0x2000
	s_add_u32 s24, s24, 0xb0080
	v_lshl_add_u64 v[178:179], v[180:181], 0, s[12:13]
	s_addc_u32 s25, s25, 0
	s_add_i32 s26, s50, s30
	global_load_lds_dwordx4 v[178:179], off
	v_lshl_add_u64 v[178:179], s[24:25], 0, v[164:165]
	s_mov_b32 m0, s26
	s_nop 0
	global_load_lds_dwordx4 v[178:179], off
	v_lshl_add_u64 v[178:179], s[24:25], 0, v[168:169]
	s_add_i32 m0, s26, 0x2000
	s_nop 0
	global_load_lds_dwordx4 v[178:179], off
	v_lshl_add_u64 v[178:179], v[182:183], 0, s[12:13]
	s_mov_b32 m0, s37
	s_nop 0
	global_load_lds_dwordx4 v[178:179], off
	v_lshl_add_u64 v[178:179], v[184:185], 0, s[12:13]
	s_mov_b32 m0, s38
	s_nop 0
	global_load_lds_dwordx4 v[178:179], off
	s_waitcnt vmcnt(8)
	s_waitcnt lgkmcnt(0)
	s_barrier
	s_setprio 1
	s_waitcnt lgkmcnt(0)
	v_mfma_scale_f32_16x16x128_f8f6f4 v[94:97], v[2:9], v[194:201], v[94:97], v1, v1 op_sel_hi:[0,0,0]
	v_mfma_scale_f32_16x16x128_f8f6f4 v[90:93], v[10:17], v[194:201], v[90:93], v1, v1 op_sel_hi:[0,0,0]
	v_mfma_scale_f32_16x16x128_f8f6f4 v[78:81], v[2:9], v[202:209], v[78:81], v1, v1 op_sel_hi:[0,0,0]
	v_mfma_scale_f32_16x16x128_f8f6f4 v[74:77], v[10:17], v[202:209], v[74:77], v1, v1 op_sel_hi:[0,0,0]
	v_mfma_scale_f32_16x16x128_f8f6f4 v[62:65], v[2:9], v[210:217], v[62:65], v1, v1 op_sel_hi:[0,0,0]
	v_mfma_scale_f32_16x16x128_f8f6f4 v[58:61], v[10:17], v[210:217], v[58:61], v1, v1 op_sel_hi:[0,0,0]
	v_mfma_scale_f32_16x16x128_f8f6f4 v[46:49], v[2:9], v[218:225], v[46:49], v1, v1 op_sel_hi:[0,0,0]
	v_mfma_scale_f32_16x16x128_f8f6f4 v[42:45], v[10:17], v[218:225], v[42:45], v1, v1 op_sel_hi:[0,0,0]
	s_setprio 0
	s_setprio 1
	v_mfma_scale_f32_16x16x128_f8f6f4 v[86:89], v[18:25], v[194:201], v[86:89], v1, v1 op_sel_hi:[0,0,0]
	v_mfma_scale_f32_16x16x128_f8f6f4 v[82:85], v[26:33], v[194:201], v[82:85], v1, v1 op_sel_hi:[0,0,0]
	v_mfma_scale_f32_16x16x128_f8f6f4 v[70:73], v[18:25], v[202:209], v[70:73], v1, v1 op_sel_hi:[0,0,0]
	v_mfma_scale_f32_16x16x128_f8f6f4 v[66:69], v[26:33], v[202:209], v[66:69], v1, v1 op_sel_hi:[0,0,0]
	v_mfma_scale_f32_16x16x128_f8f6f4 v[54:57], v[18:25], v[210:217], v[54:57], v1, v1 op_sel_hi:[0,0,0]
	v_mfma_scale_f32_16x16x128_f8f6f4 v[50:53], v[26:33], v[210:217], v[50:53], v1, v1 op_sel_hi:[0,0,0]
	s_setprio 2
	s_barrier
	v_mfma_scale_f32_16x16x128_f8f6f4 v[38:41], v[18:25], v[218:225], v[38:41], v1, v1 op_sel_hi:[0,0,0]
	v_mfma_scale_f32_16x16x128_f8f6f4 v[34:37], v[26:33], v[218:225], v[34:37], v1, v1 op_sel_hi:[0,0,0]
	s_setprio 0
	s_nop 0
	s_add_i32 s48, s48, 2
	s_add_u32 s22, s22, 0x100
	s_addc_u32 s23, s23, 0
	s_add_u32 s46, s46, 0x100
	s_addc_u32 s47, s47, 0
	s_cmp_gt_u32 s48, 41
	s_cbranch_scc0 .LBB0_841
	s_and_b64 vcc, exec, s[14:15]
	s_cbranch_vccz .LBB0_844
	s_barrier

.LBB0_973:
	ds_read_b128 v[158:161], v155
	ds_read_b128 v[162:165], v155 offset:1024
	ds_read_b128 v[166:169], v155 offset:2048
	ds_read_b128 v[170:173], v155 offset:3072
	ds_read_b128 v[174:177], v156
	ds_read_b128 v[178:181], v156 offset:1024
	ds_read_b128 v[182:185], v156 offset:2048
	ds_read_b128 v[188:191], v156 offset:3072
	s_add_u32 s34, s30, 0xfff80080
	s_addc_u32 s35, s31, -1
	s_cmp_eq_u32 s64, 28
	s_cselect_b32 s37, s9, s35
	s_cselect_b32 s36, s23, s34
	s_cselect_b32 s35, s21, s63
	s_cselect_b32 s34, s29, s62
	v_lshl_add_u64 v[152:153], s[30:31], 0, v[144:145]
	s_add_i32 m0, s39, 0xc000
	ds_read_b128 v[192:195], v157
	ds_read_b128 v[196:199], v157 offset:1024
	ds_read_b128 v[200:203], v157 offset:2048
	ds_read_b128 v[204:207], v157 offset:3072
	ds_read_b128 v[208:211], v157 offset:4096
	ds_read_b128 v[212:215], v157 offset:5120
	ds_read_b128 v[216:219], v157 offset:6144
	ds_read_b128 v[220:223], v157 offset:7168
	global_load_lds_dwordx4 v[152:153], off
	v_lshl_add_u64 v[152:153], s[30:31], 0, v[146:147]
	s_add_i32 m0, s39, 0xe000
	s_nop 0
	global_load_lds_dwordx4 v[152:153], off
	s_waitcnt vmcnt(8)
	s_waitcnt lgkmcnt(0)
	s_barrier
	s_setprio 1
	s_waitcnt lgkmcnt(0)
	v_mfma_f32_16x16x32_f16 v[126:129], v[158:161], v[192:195], v[126:129]
	v_mfma_f32_16x16x32_f16 v[122:125], v[166:169], v[192:195], v[122:125]
	v_mfma_f32_16x16x32_f16 v[110:113], v[158:161], v[200:203], v[110:113]
	v_mfma_f32_16x16x32_f16 v[106:109], v[166:169], v[200:203], v[106:109]
	v_mfma_f32_16x16x32_f16 v[94:97], v[158:161], v[208:211], v[94:97]
	v_mfma_f32_16x16x32_f16 v[90:93], v[166:169], v[208:211], v[90:93]
	v_mfma_f32_16x16x32_f16 v[78:81], v[158:161], v[216:219], v[78:81]
	v_mfma_f32_16x16x32_f16 v[74:77], v[166:169], v[216:219], v[74:77]
	v_mfma_f32_16x16x32_f16 v[126:129], v[162:165], v[196:199], v[126:129]
	v_mfma_f32_16x16x32_f16 v[122:125], v[170:173], v[196:199], v[122:125]
	v_mfma_f32_16x16x32_f16 v[110:113], v[162:165], v[204:207], v[110:113]
	v_mfma_f32_16x16x32_f16 v[106:109], v[170:173], v[204:207], v[106:109]
	v_mfma_f32_16x16x32_f16 v[94:97], v[162:165], v[212:215], v[94:97]
	v_mfma_f32_16x16x32_f16 v[90:93], v[170:173], v[212:215], v[90:93]
	v_mfma_f32_16x16x32_f16 v[78:81], v[162:165], v[220:223], v[78:81]
	v_mfma_f32_16x16x32_f16 v[74:77], v[170:173], v[220:223], v[74:77]
	s_setprio 0
	s_setprio 1
	v_mfma_f32_16x16x32_f16 v[118:121], v[174:177], v[192:195], v[118:121]
	v_mfma_f32_16x16x32_f16 v[114:117], v[182:185], v[192:195], v[114:117]
	v_mfma_f32_16x16x32_f16 v[102:105], v[174:177], v[200:203], v[102:105]
	v_mfma_f32_16x16x32_f16 v[98:101], v[182:185], v[200:203], v[98:101]
	v_mfma_f32_16x16x32_f16 v[86:89], v[174:177], v[208:211], v[86:89]
	v_mfma_f32_16x16x32_f16 v[82:85], v[182:185], v[208:211], v[82:85]
	v_mfma_f32_16x16x32_f16 v[70:73], v[174:177], v[216:219], v[70:73]
	v_mfma_f32_16x16x32_f16 v[66:69], v[182:185], v[216:219], v[66:69]
	v_mfma_f32_16x16x32_f16 v[118:121], v[178:181], v[196:199], v[118:121]
	v_mfma_f32_16x16x32_f16 v[114:117], v[188:191], v[196:199], v[114:117]
	v_mfma_f32_16x16x32_f16 v[102:105], v[178:181], v[204:207], v[102:105]
	v_mfma_f32_16x16x32_f16 v[98:101], v[188:191], v[204:207], v[98:101]
	s_setprio 2
	s_barrier
	v_mfma_f32_16x16x32_f16 v[86:89], v[178:181], v[212:215], v[86:89]
	v_mfma_f32_16x16x32_f16 v[82:85], v[188:191], v[212:215], v[82:85]
	v_mfma_f32_16x16x32_f16 v[70:73], v[178:181], v[220:223], v[70:73]
	v_mfma_f32_16x16x32_f16 v[66:69], v[188:191], v[220:223], v[66:69]
	s_setprio 0
	s_nop 0
	s_add_i32 s65, s49, s38
	v_lshl_add_u64 v[152:153], s[34:35], 0, v[132:133]
	s_mov_b32 m0, s65
	ds_read_b128 v[192:195], v157 offset:16384
	ds_read_b128 v[196:199], v157 offset:17408
	ds_read_b128 v[200:203], v157 offset:18432
	ds_read_b128 v[204:207], v157 offset:19456
	ds_read_b128 v[208:211], v157 offset:20480
	ds_read_b128 v[212:215], v157 offset:21504
	ds_read_b128 v[216:219], v157 offset:22528
	ds_read_b128 v[220:223], v157 offset:23552
	global_load_lds_dwordx4 v[152:153], off
	s_add_i32 m0, s65, 0x2000
	s_add_u32 s66, s34, 0x80000
	v_lshl_add_u64 v[224:225], s[34:35], 0, v[136:137]
	s_addc_u32 s67, s35, 0
	s_add_i32 s65, s50, s38
	global_load_lds_dwordx4 v[224:225], off
	v_lshl_add_u64 v[226:227], s[66:67], 0, v[132:133]
	s_mov_b32 m0, s65
	v_lshl_add_u64 v[228:229], s[36:37], 0, v[134:135]
	global_load_lds_dwordx4 v[226:227], off
	v_lshl_add_u64 v[226:227], s[66:67], 0, v[136:137]
	s_add_i32 m0, s65, 0x2000
	s_nop 0
	global_load_lds_dwordx4 v[226:227], off
	v_lshl_add_u64 v[226:227], s[36:37], 0, v[130:131]
	s_mov_b32 m0, s39
	s_nop 0
	global_load_lds_dwordx4 v[226:227], off
	s_mov_b32 m0, s40
	s_nop 0
	global_load_lds_dwordx4 v[228:229], off
	s_waitcnt vmcnt(8)
	s_waitcnt lgkmcnt(0)
	s_barrier
	s_setprio 1
	s_waitcnt lgkmcnt(0)
	v_mfma_f32_16x16x32_f16 v[62:65], v[158:161], v[192:195], v[62:65]
	v_mfma_f32_16x16x32_f16 v[58:61], v[166:169], v[192:195], v[58:61]
	v_mfma_f32_16x16x32_f16 v[46:49], v[158:161], v[200:203], v[46:49]
	v_mfma_f32_16x16x32_f16 v[42:45], v[166:169], v[200:203], v[42:45]
	v_mfma_f32_16x16x32_f16 v[30:33], v[158:161], v[208:211], v[30:33]
	v_mfma_f32_16x16x32_f16 v[26:29], v[166:169], v[208:211], v[26:29]
	v_mfma_f32_16x16x32_f16 v[14:17], v[158:161], v[216:219], v[14:17]
	v_mfma_f32_16x16x32_f16 v[10:13], v[166:169], v[216:219], v[10:13]
	v_mfma_f32_16x16x32_f16 v[62:65], v[162:165], v[196:199], v[62:65]
	v_mfma_f32_16x16x32_f16 v[58:61], v[170:173], v[196:199], v[58:61]
	v_mfma_f32_16x16x32_f16 v[46:49], v[162:165], v[204:207], v[46:49]
	v_mfma_f32_16x16x32_f16 v[42:45], v[170:173], v[204:207], v[42:45]
	v_mfma_f32_16x16x32_f16 v[30:33], v[162:165], v[212:215], v[30:33]
	v_mfma_f32_16x16x32_f16 v[26:29], v[170:173], v[212:215], v[26:29]
	v_mfma_f32_16x16x32_f16 v[14:17], v[162:165], v[220:223], v[14:17]
	v_mfma_f32_16x16x32_f16 v[10:13], v[170:173], v[220:223], v[10:13]
	s_setprio 0
	s_setprio 1
	v_mfma_f32_16x16x32_f16 v[54:57], v[174:177], v[192:195], v[54:57]
	v_mfma_f32_16x16x32_f16 v[50:53], v[182:185], v[192:195], v[50:53]
	v_mfma_f32_16x16x32_f16 v[38:41], v[174:177], v[200:203], v[38:41]
	v_mfma_f32_16x16x32_f16 v[34:37], v[182:185], v[200:203], v[34:37]
	v_mfma_f32_16x16x32_f16 v[22:25], v[174:177], v[208:211], v[22:25]
	v_mfma_f32_16x16x32_f16 v[18:21], v[182:185], v[208:211], v[18:21]
	v_mfma_f32_16x16x32_f16 v[6:9], v[174:177], v[216:219], v[6:9]
	v_mfma_f32_16x16x32_f16 v[2:5], v[182:185], v[216:219], v[2:5]
	v_mfma_f32_16x16x32_f16 v[54:57], v[178:181], v[196:199], v[54:57]
	v_mfma_f32_16x16x32_f16 v[50:53], v[188:191], v[196:199], v[50:53]
	v_mfma_f32_16x16x32_f16 v[38:41], v[178:181], v[204:207], v[38:41]
	v_mfma_f32_16x16x32_f16 v[34:37], v[188:191], v[204:207], v[34:37]
	s_setprio 2
	s_barrier
	v_mfma_f32_16x16x32_f16 v[22:25], v[178:181], v[212:215], v[22:25]
	v_mfma_f32_16x16x32_f16 v[18:21], v[188:191], v[212:215], v[18:21]
	v_mfma_f32_16x16x32_f16 v[6:9], v[178:181], v[220:223], v[6:9]
	v_mfma_f32_16x16x32_f16 v[2:5], v[188:191], v[220:223], v[2:5]
	s_setprio 0
	s_nop 0
	s_add_i32 s65, 0, 0x18000
	v_add_u32_e32 v138, s65, v141
	s_add_i32 s66, 0, 0x1c000
	ds_read_b128 v[158:161], v138
	ds_read_b128 v[162:165], v138 offset:1024
	ds_read_b128 v[166:169], v138 offset:2048
	ds_read_b128 v[170:173], v138 offset:3072
	v_add_u32_e32 v138, s66, v141
	ds_read_b128 v[174:177], v138
	ds_read_b128 v[178:181], v138 offset:1024
	ds_read_b128 v[182:185], v138 offset:2048
	ds_read_b128 v[188:191], v138 offset:3072
	s_add_u32 s36, s36, 0x80000
	s_addc_u32 s37, s37, 0
	s_mov_b32 m0, s41
	v_lshl_add_u64 v[230:231], s[36:37], 0, v[130:131]
	ds_read_b128 v[192:195], v157 offset:32768
	ds_read_b128 v[196:199], v157 offset:33792
	ds_read_b128 v[200:203], v157 offset:34816
	ds_read_b128 v[204:207], v157 offset:35840
	ds_read_b128 v[208:211], v157 offset:36864
	ds_read_b128 v[212:215], v157 offset:37888
	ds_read_b128 v[216:219], v157 offset:38912
	ds_read_b128 v[220:223], v157 offset:39936
	global_load_lds_dwordx4 v[230:231], off
	v_lshl_add_u64 v[230:231], s[36:37], 0, v[134:135]
	s_mov_b32 m0, s42
	s_nop 0
	global_load_lds_dwordx4 v[230:231], off
	s_waitcnt vmcnt(8)
	s_waitcnt lgkmcnt(0)
	s_barrier
	s_setprio 1
	s_waitcnt lgkmcnt(0)
	v_mfma_f32_16x16x32_f16 v[126:129], v[158:161], v[192:195], v[126:129]
	v_mfma_f32_16x16x32_f16 v[122:125], v[166:169], v[192:195], v[122:125]
	v_mfma_f32_16x16x32_f16 v[110:113], v[158:161], v[200:203], v[110:113]
	v_mfma_f32_16x16x32_f16 v[106:109], v[166:169], v[200:203], v[106:109]
	v_mfma_f32_16x16x32_f16 v[94:97], v[158:161], v[208:211], v[94:97]
	v_mfma_f32_16x16x32_f16 v[90:93], v[166:169], v[208:211], v[90:93]
	v_mfma_f32_16x16x32_f16 v[78:81], v[158:161], v[216:219], v[78:81]
	v_mfma_f32_16x16x32_f16 v[74:77], v[166:169], v[216:219], v[74:77]
	v_mfma_f32_16x16x32_f16 v[126:129], v[162:165], v[196:199], v[126:129]
	v_mfma_f32_16x16x32_f16 v[122:125], v[170:173], v[196:199], v[122:125]
	v_mfma_f32_16x16x32_f16 v[110:113], v[162:165], v[204:207], v[110:113]
	v_mfma_f32_16x16x32_f16 v[106:109], v[170:173], v[204:207], v[106:109]
	v_mfma_f32_16x16x32_f16 v[94:97], v[162:165], v[212:215], v[94:97]
	v_mfma_f32_16x16x32_f16 v[90:93], v[170:173], v[212:215], v[90:93]
	v_mfma_f32_16x16x32_f16 v[78:81], v[162:165], v[220:223], v[78:81]
	v_mfma_f32_16x16x32_f16 v[74:77], v[170:173], v[220:223], v[74:77]
	s_setprio 0
	s_setprio 1
	v_mfma_f32_16x16x32_f16 v[118:121], v[174:177], v[192:195], v[118:121]
	v_mfma_f32_16x16x32_f16 v[114:117], v[182:185], v[192:195], v[114:117]
	v_mfma_f32_16x16x32_f16 v[102:105], v[174:177], v[200:203], v[102:105]
	v_mfma_f32_16x16x32_f16 v[98:101], v[182:185], v[200:203], v[98:101]
	v_mfma_f32_16x16x32_f16 v[86:89], v[174:177], v[208:211], v[86:89]
	v_mfma_f32_16x16x32_f16 v[82:85], v[182:185], v[208:211], v[82:85]
	v_mfma_f32_16x16x32_f16 v[70:73], v[174:177], v[216:219], v[70:73]
	v_mfma_f32_16x16x32_f16 v[66:69], v[182:185], v[216:219], v[66:69]
	v_mfma_f32_16x16x32_f16 v[118:121], v[178:181], v[196:199], v[118:121]
	v_mfma_f32_16x16x32_f16 v[114:117], v[188:191], v[196:199], v[114:117]
	v_mfma_f32_16x16x32_f16 v[102:105], v[178:181], v[204:207], v[102:105]
	v_mfma_f32_16x16x32_f16 v[98:101], v[188:191], v[204:207], v[98:101]
	s_setprio 2
	s_barrier
	v_mfma_f32_16x16x32_f16 v[86:89], v[178:181], v[212:215], v[86:89]
	v_mfma_f32_16x16x32_f16 v[82:85], v[188:191], v[212:215], v[82:85]
	v_mfma_f32_16x16x32_f16 v[70:73], v[178:181], v[220:223], v[70:73]
	v_mfma_f32_16x16x32_f16 v[66:69], v[188:191], v[220:223], v[66:69]
	s_setprio 0
	s_nop 0
	s_add_i32 s36, s65, s38
	v_lshl_add_u64 v[152:153], v[152:153], 0, s[16:17]
	s_mov_b32 m0, s36
	ds_read_b128 v[192:195], v157 offset:49152
	ds_read_b128 v[196:199], v157 offset:50176
	ds_read_b128 v[200:203], v157 offset:51200
	ds_read_b128 v[204:207], v157 offset:52224
	ds_read_b128 v[208:211], v157 offset:53248
	ds_read_b128 v[212:215], v157 offset:54272
	ds_read_b128 v[216:219], v157 offset:55296
	ds_read_b128 v[220:223], v157 offset:56320
	global_load_lds_dwordx4 v[152:153], off
	s_add_i32 m0, s36, 0x2000
	s_add_u32 s34, s34, 0x80080
	v_lshl_add_u64 v[152:153], v[224:225], 0, s[16:17]
	s_addc_u32 s35, s35, 0
	s_add_i32 s36, s66, s38
	global_load_lds_dwordx4 v[152:153], off
	v_lshl_add_u64 v[152:153], s[34:35], 0, v[132:133]
	s_mov_b32 m0, s36
	s_nop 0
	global_load_lds_dwordx4 v[152:153], off
	v_lshl_add_u64 v[152:153], s[34:35], 0, v[136:137]
	s_add_i32 m0, s36, 0x2000
	s_nop 0
	global_load_lds_dwordx4 v[152:153], off
	v_lshl_add_u64 v[152:153], v[226:227], 0, s[16:17]
	s_mov_b32 m0, s45
	s_nop 0
	global_load_lds_dwordx4 v[152:153], off
	v_lshl_add_u64 v[152:153], v[228:229], 0, s[16:17]
	s_mov_b32 m0, s46
	s_nop 0
	global_load_lds_dwordx4 v[152:153], off
	s_waitcnt vmcnt(8)
	s_waitcnt lgkmcnt(0)
	s_barrier
	s_setprio 1
	s_waitcnt lgkmcnt(0)
	v_mfma_f32_16x16x32_f16 v[62:65], v[158:161], v[192:195], v[62:65]
	v_mfma_f32_16x16x32_f16 v[58:61], v[166:169], v[192:195], v[58:61]
	v_mfma_f32_16x16x32_f16 v[46:49], v[158:161], v[200:203], v[46:49]
	v_mfma_f32_16x16x32_f16 v[42:45], v[166:169], v[200:203], v[42:45]
	v_mfma_f32_16x16x32_f16 v[30:33], v[158:161], v[208:211], v[30:33]
	v_mfma_f32_16x16x32_f16 v[26:29], v[166:169], v[208:211], v[26:29]
	v_mfma_f32_16x16x32_f16 v[14:17], v[158:161], v[216:219], v[14:17]
	v_mfma_f32_16x16x32_f16 v[10:13], v[166:169], v[216:219], v[10:13]
	v_mfma_f32_16x16x32_f16 v[62:65], v[162:165], v[196:199], v[62:65]
	v_mfma_f32_16x16x32_f16 v[58:61], v[170:173], v[196:199], v[58:61]
	v_mfma_f32_16x16x32_f16 v[46:49], v[162:165], v[204:207], v[46:49]
	v_mfma_f32_16x16x32_f16 v[42:45], v[170:173], v[204:207], v[42:45]
	v_mfma_f32_16x16x32_f16 v[30:33], v[162:165], v[212:215], v[30:33]
	v_mfma_f32_16x16x32_f16 v[26:29], v[170:173], v[212:215], v[26:29]
	v_mfma_f32_16x16x32_f16 v[14:17], v[162:165], v[220:223], v[14:17]
	v_mfma_f32_16x16x32_f16 v[10:13], v[170:173], v[220:223], v[10:13]
	s_setprio 0
	s_setprio 1
	v_mfma_f32_16x16x32_f16 v[54:57], v[174:177], v[192:195], v[54:57]
	v_mfma_f32_16x16x32_f16 v[50:53], v[182:185], v[192:195], v[50:53]
	v_mfma_f32_16x16x32_f16 v[38:41], v[174:177], v[200:203], v[38:41]
	v_mfma_f32_16x16x32_f16 v[34:37], v[182:185], v[200:203], v[34:37]
	v_mfma_f32_16x16x32_f16 v[22:25], v[174:177], v[208:211], v[22:25]
	v_mfma_f32_16x16x32_f16 v[18:21], v[182:185], v[208:211], v[18:21]
	v_mfma_f32_16x16x32_f16 v[6:9], v[174:177], v[216:219], v[6:9]
	v_mfma_f32_16x16x32_f16 v[2:5], v[182:185], v[216:219], v[2:5]
	v_mfma_f32_16x16x32_f16 v[54:57], v[178:181], v[196:199], v[54:57]
	v_mfma_f32_16x16x32_f16 v[50:53], v[188:191], v[196:199], v[50:53]
	v_mfma_f32_16x16x32_f16 v[38:41], v[178:181], v[204:207], v[38:41]
	v_mfma_f32_16x16x32_f16 v[34:37], v[188:191], v[204:207], v[34:37]
	s_setprio 2
	s_barrier
	v_mfma_f32_16x16x32_f16 v[22:25], v[178:181], v[212:215], v[22:25]
	v_mfma_f32_16x16x32_f16 v[18:21], v[188:191], v[212:215], v[18:21]
	v_mfma_f32_16x16x32_f16 v[6:9], v[178:181], v[220:223], v[6:9]
	v_mfma_f32_16x16x32_f16 v[2:5], v[188:191], v[220:223], v[2:5]
	s_setprio 0
	s_nop 0
	s_add_i32 s64, s64, 2
	s_add_u32 s30, s30, 0x100
	s_addc_u32 s31, s31, 0
	s_add_u32 s62, s62, 0x100
	s_addc_u32 s63, s63, 0
	s_cmp_gt_u32 s64, 29
	s_cbranch_scc0 .LBB0_973
	s_and_b64 vcc, exec, s[18:19]
	s_cbranch_vccz .LBB0_976
	s_barrier

.LBB0_1120:
	ds_read_b128 v[88:91], v85
	ds_read_b128 v[92:95], v85 offset:1024
	ds_read_b128 v[96:99], v85 offset:2048
	ds_read_b128 v[100:103], v85 offset:3072
	s_add_u32 s26, s24, 0xfffd8080
	s_addc_u32 s27, s25, -1
	s_cmp_eq_u32 s51, 4
	s_cselect_b32 s29, s1, s27
	s_cselect_b32 s28, s0, s26
	s_cselect_b32 s27, s23, s50
	s_cselect_b32 s26, s22, s21
	v_lshl_add_u64 v[136:137], s[24:25], 0, v[76:77]
	s_add_i32 m0, s15, 0xc000
	ds_read_b128 v[104:107], v86
	ds_read_b128 v[108:111], v86 offset:1024
	ds_read_b128 v[112:115], v86 offset:2048
	ds_read_b128 v[116:119], v86 offset:3072
	ds_read_b128 v[120:123], v86 offset:4096
	ds_read_b128 v[124:127], v86 offset:5120
	ds_read_b128 v[128:131], v86 offset:6144
	ds_read_b128 v[132:135], v86 offset:7168
	global_load_lds_dwordx4 v[136:137], off
	v_lshl_add_u64 v[136:137], s[24:25], 0, v[78:79]
	s_add_i32 m0, s15, 0xe000
	s_nop 0
	global_load_lds_dwordx4 v[136:137], off
	s_waitcnt vmcnt(8)
	s_waitcnt lgkmcnt(0)
	s_barrier
	s_setprio 1
	s_waitcnt lgkmcnt(0)
	v_mfma_f32_16x16x32_f16 v[62:65], v[88:91], v[104:107], v[62:65]
	v_mfma_f32_16x16x32_f16 v[58:61], v[96:99], v[104:107], v[58:61]
	v_mfma_f32_16x16x32_f16 v[54:57], v[88:91], v[112:115], v[54:57]
	v_mfma_f32_16x16x32_f16 v[50:53], v[96:99], v[112:115], v[50:53]
	v_mfma_f32_16x16x32_f16 v[46:49], v[88:91], v[120:123], v[46:49]
	v_mfma_f32_16x16x32_f16 v[42:45], v[96:99], v[120:123], v[42:45]
	v_mfma_f32_16x16x32_f16 v[38:41], v[88:91], v[128:131], v[38:41]
	v_mfma_f32_16x16x32_f16 v[34:37], v[96:99], v[128:131], v[34:37]
	v_mfma_f32_16x16x32_f16 v[62:65], v[92:95], v[108:111], v[62:65]
	v_mfma_f32_16x16x32_f16 v[58:61], v[100:103], v[108:111], v[58:61]
	v_mfma_f32_16x16x32_f16 v[54:57], v[92:95], v[116:119], v[54:57]
	v_mfma_f32_16x16x32_f16 v[50:53], v[100:103], v[116:119], v[50:53]
	s_setprio 2
	s_barrier
	v_mfma_f32_16x16x32_f16 v[46:49], v[92:95], v[124:127], v[46:49]
	v_mfma_f32_16x16x32_f16 v[42:45], v[100:103], v[124:127], v[42:45]
	v_mfma_f32_16x16x32_f16 v[38:41], v[92:95], v[132:135], v[38:41]
	v_mfma_f32_16x16x32_f16 v[34:37], v[100:103], v[132:135], v[34:37]
	s_setprio 0
	s_setprio 1
	s_setprio 0
	s_nop 0
	s_add_i32 s60, s48, s34
	v_lshl_add_u64 v[136:137], s[26:27], 0, v[70:71]
	s_mov_b32 m0, s60
	ds_read_b128 v[104:107], v86 offset:16384
	ds_read_b128 v[108:111], v86 offset:17408
	ds_read_b128 v[112:115], v86 offset:18432
	ds_read_b128 v[116:119], v86 offset:19456
	ds_read_b128 v[120:123], v86 offset:20480
	ds_read_b128 v[124:127], v86 offset:21504
	ds_read_b128 v[128:131], v86 offset:22528
	ds_read_b128 v[132:135], v86 offset:23552
	global_load_lds_dwordx4 v[136:137], off
	s_add_i32 m0, s60, 0x2000
	s_add_u32 s60, s26, 0x20000
	v_lshl_add_u64 v[138:139], s[26:27], 0, v[66:67]
	s_addc_u32 s61, s27, 0
	global_load_lds_dwordx4 v[138:139], off
	v_lshl_add_u64 v[140:141], s[60:61], 0, v[70:71]
	s_mov_b32 m0, s35
	v_lshl_add_u64 v[142:143], s[28:29], 0, v[68:69]
	global_load_lds_dwordx4 v[140:141], off
	v_lshl_add_u64 v[140:141], s[60:61], 0, v[66:67]
	s_mov_b32 m0, s36
	s_nop 0
	global_load_lds_dwordx4 v[140:141], off
	v_lshl_add_u64 v[140:141], s[28:29], 0, v[72:73]
	s_mov_b32 m0, s15
	s_nop 0
	global_load_lds_dwordx4 v[140:141], off
	s_mov_b32 m0, s37
	s_nop 0
	global_load_lds_dwordx4 v[142:143], off
	s_waitcnt vmcnt(8)
	s_waitcnt lgkmcnt(0)
	s_barrier
	s_setprio 1
	s_waitcnt lgkmcnt(0)
	v_mfma_f32_16x16x32_f16 v[30:33], v[88:91], v[104:107], v[30:33]
	v_mfma_f32_16x16x32_f16 v[26:29], v[96:99], v[104:107], v[26:29]
	v_mfma_f32_16x16x32_f16 v[22:25], v[88:91], v[112:115], v[22:25]
	v_mfma_f32_16x16x32_f16 v[18:21], v[96:99], v[112:115], v[18:21]
	v_mfma_f32_16x16x32_f16 v[14:17], v[88:91], v[120:123], v[14:17]
	v_mfma_f32_16x16x32_f16 v[10:13], v[96:99], v[120:123], v[10:13]
	v_mfma_f32_16x16x32_f16 v[6:9], v[88:91], v[128:131], v[6:9]
	v_mfma_f32_16x16x32_f16 v[2:5], v[96:99], v[128:131], v[2:5]
	v_mfma_f32_16x16x32_f16 v[30:33], v[92:95], v[108:111], v[30:33]
	v_mfma_f32_16x16x32_f16 v[26:29], v[100:103], v[108:111], v[26:29]
	v_mfma_f32_16x16x32_f16 v[22:25], v[92:95], v[116:119], v[22:25]
	v_mfma_f32_16x16x32_f16 v[18:21], v[100:103], v[116:119], v[18:21]
	s_setprio 2
	s_barrier
	v_mfma_f32_16x16x32_f16 v[14:17], v[92:95], v[124:127], v[14:17]
	v_mfma_f32_16x16x32_f16 v[10:13], v[100:103], v[124:127], v[10:13]
	v_mfma_f32_16x16x32_f16 v[6:9], v[92:95], v[132:135], v[6:9]
	v_mfma_f32_16x16x32_f16 v[2:5], v[100:103], v[132:135], v[2:5]
	s_setprio 0
	s_setprio 1
	s_setprio 0
	s_nop 0
	s_add_i32 s60, 0, 0x18000
	v_add_u32_e32 v87, s60, v84
	ds_read_b128 v[88:91], v87
	ds_read_b128 v[92:95], v87 offset:1024
	ds_read_b128 v[96:99], v87 offset:2048
	ds_read_b128 v[100:103], v87 offset:3072
	s_add_u32 s28, s28, 0x28000
	s_addc_u32 s29, s29, 0
	s_mov_b32 m0, s38
	v_lshl_add_u64 v[144:145], s[28:29], 0, v[72:73]
	ds_read_b128 v[104:107], v86 offset:32768
	ds_read_b128 v[108:111], v86 offset:33792
	ds_read_b128 v[112:115], v86 offset:34816
	ds_read_b128 v[116:119], v86 offset:35840
	ds_read_b128 v[120:123], v86 offset:36864
	ds_read_b128 v[124:127], v86 offset:37888
	ds_read_b128 v[128:131], v86 offset:38912
	ds_read_b128 v[132:135], v86 offset:39936
	global_load_lds_dwordx4 v[144:145], off
	v_lshl_add_u64 v[144:145], s[28:29], 0, v[68:69]
	s_mov_b32 m0, s39
	s_nop 0
	global_load_lds_dwordx4 v[144:145], off
	s_waitcnt vmcnt(8)
	s_waitcnt lgkmcnt(0)
	s_barrier
	s_setprio 1
	s_waitcnt lgkmcnt(0)
	v_mfma_f32_16x16x32_f16 v[62:65], v[88:91], v[104:107], v[62:65]
	v_mfma_f32_16x16x32_f16 v[58:61], v[96:99], v[104:107], v[58:61]
	v_mfma_f32_16x16x32_f16 v[54:57], v[88:91], v[112:115], v[54:57]
	v_mfma_f32_16x16x32_f16 v[50:53], v[96:99], v[112:115], v[50:53]
	v_mfma_f32_16x16x32_f16 v[46:49], v[88:91], v[120:123], v[46:49]
	v_mfma_f32_16x16x32_f16 v[42:45], v[96:99], v[120:123], v[42:45]
	v_mfma_f32_16x16x32_f16 v[38:41], v[88:91], v[128:131], v[38:41]
	v_mfma_f32_16x16x32_f16 v[34:37], v[96:99], v[128:131], v[34:37]
	v_mfma_f32_16x16x32_f16 v[62:65], v[92:95], v[108:111], v[62:65]
	v_mfma_f32_16x16x32_f16 v[58:61], v[100:103], v[108:111], v[58:61]
	v_mfma_f32_16x16x32_f16 v[54:57], v[92:95], v[116:119], v[54:57]
	v_mfma_f32_16x16x32_f16 v[50:53], v[100:103], v[116:119], v[50:53]
	s_setprio 2
	s_barrier
	v_mfma_f32_16x16x32_f16 v[46:49], v[92:95], v[124:127], v[46:49]
	v_mfma_f32_16x16x32_f16 v[42:45], v[100:103], v[124:127], v[42:45]
	v_mfma_f32_16x16x32_f16 v[38:41], v[92:95], v[132:135], v[38:41]
	v_mfma_f32_16x16x32_f16 v[34:37], v[100:103], v[132:135], v[34:37]
	s_setprio 0
	s_setprio 1
	s_setprio 0
	s_nop 0
	s_add_i32 s28, s60, s34
	v_lshl_add_u64 v[136:137], v[136:137], 0, s[16:17]
	s_mov_b32 m0, s28
	ds_read_b128 v[104:107], v86 offset:49152
	ds_read_b128 v[108:111], v86 offset:50176
	ds_read_b128 v[112:115], v86 offset:51200
	ds_read_b128 v[116:119], v86 offset:52224
	ds_read_b128 v[120:123], v86 offset:53248
	ds_read_b128 v[124:127], v86 offset:54272
	ds_read_b128 v[128:131], v86 offset:55296
	ds_read_b128 v[132:135], v86 offset:56320
	global_load_lds_dwordx4 v[136:137], off
	s_add_i32 m0, s28, 0x2000
	s_add_u32 s26, s26, 0x20080
	v_lshl_add_u64 v[136:137], v[138:139], 0, s[16:17]
	s_addc_u32 s27, s27, 0
	global_load_lds_dwordx4 v[136:137], off
	v_lshl_add_u64 v[136:137], s[26:27], 0, v[70:71]
	s_mov_b32 m0, s45
	s_nop 0
	global_load_lds_dwordx4 v[136:137], off
	v_lshl_add_u64 v[136:137], s[26:27], 0, v[66:67]
	s_mov_b32 m0, s46
	s_nop 0
	global_load_lds_dwordx4 v[136:137], off
	v_lshl_add_u64 v[136:137], v[140:141], 0, s[16:17]
	s_mov_b32 m0, s43
	s_nop 0
	global_load_lds_dwordx4 v[136:137], off
	v_lshl_add_u64 v[136:137], v[142:143], 0, s[16:17]
	s_mov_b32 m0, s44
	s_nop 0
	global_load_lds_dwordx4 v[136:137], off
	s_waitcnt vmcnt(8)
	s_waitcnt lgkmcnt(0)
	s_barrier
	s_setprio 1
	s_waitcnt lgkmcnt(0)
	v_mfma_f32_16x16x32_f16 v[30:33], v[88:91], v[104:107], v[30:33]
	v_mfma_f32_16x16x32_f16 v[26:29], v[96:99], v[104:107], v[26:29]
	v_mfma_f32_16x16x32_f16 v[22:25], v[88:91], v[112:115], v[22:25]
	v_mfma_f32_16x16x32_f16 v[18:21], v[96:99], v[112:115], v[18:21]
	v_mfma_f32_16x16x32_f16 v[14:17], v[88:91], v[120:123], v[14:17]
	v_mfma_f32_16x16x32_f16 v[10:13], v[96:99], v[120:123], v[10:13]
	v_mfma_f32_16x16x32_f16 v[6:9], v[88:91], v[128:131], v[6:9]
	v_mfma_f32_16x16x32_f16 v[2:5], v[96:99], v[128:131], v[2:5]
	v_mfma_f32_16x16x32_f16 v[30:33], v[92:95], v[108:111], v[30:33]
	v_mfma_f32_16x16x32_f16 v[26:29], v[100:103], v[108:111], v[26:29]
	v_mfma_f32_16x16x32_f16 v[22:25], v[92:95], v[116:119], v[22:25]
	v_mfma_f32_16x16x32_f16 v[18:21], v[100:103], v[116:119], v[18:21]
	s_setprio 2
	s_barrier
	v_mfma_f32_16x16x32_f16 v[14:17], v[92:95], v[124:127], v[14:17]
	v_mfma_f32_16x16x32_f16 v[10:13], v[100:103], v[124:127], v[10:13]
	v_mfma_f32_16x16x32_f16 v[6:9], v[92:95], v[132:135], v[6:9]
	v_mfma_f32_16x16x32_f16 v[2:5], v[100:103], v[132:135], v[2:5]
	s_setprio 0
	s_setprio 1
	s_setprio 0
	s_nop 0
	s_add_i32 s51, s51, 2
	s_add_u32 s24, s24, 0x100
	s_addc_u32 s25, s25, 0
	s_add_u32 s21, s21, 0x100
	s_addc_u32 s50, s50, 0
	s_cmp_gt_u32 s51, 5
	s_cbranch_scc0 .LBB0_1120
	s_and_b64 vcc, exec, s[18:19]
	s_cbranch_vccz .LBB0_1123
	s_barrier

.LBB0_1649:
	ds_read_b128 v[98:101], v174
	ds_read_b128 v[102:105], v174 offset:1024
	ds_read_b128 v[158:161], v174 offset:2048
	ds_read_b128 v[164:167], v174 offset:3072
	ds_read_b128 v[178:181], v175
	ds_read_b128 v[182:185], v175 offset:1024
	ds_read_b128 v[188:191], v175 offset:2048
	ds_read_b128 v[192:195], v175 offset:3072
	s_add_u32 s22, s20, 0xfffd8080
	s_addc_u32 s23, s21, -1
	s_cmp_eq_u32 s50, 6
	s_cselect_b32 s25, s1, s23
	s_cselect_b32 s24, s0, s22
	s_cselect_b32 s23, s19, s49
	s_cselect_b32 s22, s18, s48
	v_lshl_add_u64 v[168:169], s[20:21], 0, v[150:151]
	s_add_i32 m0, s29, 0xc000
	ds_read_b128 v[196:199], v176
	ds_read_b128 v[200:203], v176 offset:1024
	ds_read_b128 v[204:207], v176 offset:2048
	ds_read_b128 v[208:211], v176 offset:3072
	ds_read_b128 v[212:215], v176 offset:4096
	ds_read_b128 v[216:219], v176 offset:5120
	ds_read_b128 v[220:223], v176 offset:6144
	ds_read_b128 v[224:227], v176 offset:7168
	global_load_lds_dwordx4 v[168:169], off
	v_lshl_add_u64 v[168:169], s[20:21], 0, v[152:153]
	s_add_i32 m0, s29, 0xe000
	s_nop 0
	global_load_lds_dwordx4 v[168:169], off
	s_waitcnt vmcnt(8)
	s_waitcnt lgkmcnt(0)
	s_barrier
	s_setprio 1
	s_waitcnt lgkmcnt(0)
	v_mfma_f32_16x16x32_f16 v[134:137], v[98:101], v[196:199], v[134:137]
	v_mfma_f32_16x16x32_f16 v[130:133], v[158:161], v[196:199], v[130:133]
	v_mfma_f32_16x16x32_f16 v[126:129], v[98:101], v[204:207], v[126:129]
	v_mfma_f32_16x16x32_f16 v[122:125], v[158:161], v[204:207], v[122:125]
	v_mfma_f32_16x16x32_f16 v[118:121], v[98:101], v[212:215], v[118:121]
	v_mfma_f32_16x16x32_f16 v[114:117], v[158:161], v[212:215], v[114:117]
	v_mfma_f32_16x16x32_f16 v[110:113], v[98:101], v[220:223], v[110:113]
	v_mfma_f32_16x16x32_f16 v[106:109], v[158:161], v[220:223], v[106:109]
	v_mfma_f32_16x16x32_f16 v[134:137], v[102:105], v[200:203], v[134:137]
	v_mfma_f32_16x16x32_f16 v[130:133], v[164:167], v[200:203], v[130:133]
	v_mfma_f32_16x16x32_f16 v[126:129], v[102:105], v[208:211], v[126:129]
	v_mfma_f32_16x16x32_f16 v[122:125], v[164:167], v[208:211], v[122:125]
	v_mfma_f32_16x16x32_f16 v[118:121], v[102:105], v[216:219], v[118:121]
	v_mfma_f32_16x16x32_f16 v[114:117], v[164:167], v[216:219], v[114:117]
	v_mfma_f32_16x16x32_f16 v[110:113], v[102:105], v[224:227], v[110:113]
	v_mfma_f32_16x16x32_f16 v[106:109], v[164:167], v[224:227], v[106:109]
	s_setprio 0
	s_setprio 1
	v_mfma_f32_16x16x32_f16 v[62:65], v[178:181], v[196:199], v[62:65]
	v_mfma_f32_16x16x32_f16 v[58:61], v[188:191], v[196:199], v[58:61]
	v_mfma_f32_16x16x32_f16 v[54:57], v[178:181], v[204:207], v[54:57]
	v_mfma_f32_16x16x32_f16 v[50:53], v[188:191], v[204:207], v[50:53]
	v_mfma_f32_16x16x32_f16 v[46:49], v[178:181], v[212:215], v[46:49]
	v_mfma_f32_16x16x32_f16 v[42:45], v[188:191], v[212:215], v[42:45]
	v_mfma_f32_16x16x32_f16 v[38:41], v[178:181], v[220:223], v[38:41]
	v_mfma_f32_16x16x32_f16 v[34:37], v[188:191], v[220:223], v[34:37]
	v_mfma_f32_16x16x32_f16 v[62:65], v[182:185], v[200:203], v[62:65]
	v_mfma_f32_16x16x32_f16 v[58:61], v[192:195], v[200:203], v[58:61]
	v_mfma_f32_16x16x32_f16 v[54:57], v[182:185], v[208:211], v[54:57]
	v_mfma_f32_16x16x32_f16 v[50:53], v[192:195], v[208:211], v[50:53]
	s_setprio 2
	s_barrier
	v_mfma_f32_16x16x32_f16 v[46:49], v[182:185], v[216:219], v[46:49]
	v_mfma_f32_16x16x32_f16 v[42:45], v[192:195], v[216:219], v[42:45]
	v_mfma_f32_16x16x32_f16 v[38:41], v[182:185], v[224:227], v[38:41]
	v_mfma_f32_16x16x32_f16 v[34:37], v[192:195], v[224:227], v[34:37]
	s_setprio 0
	s_nop 0
	s_add_i32 s51, s39, s27
	v_lshl_add_u64 v[168:169], s[22:23], 0, v[142:143]
	s_mov_b32 m0, s51
	ds_read_b128 v[196:199], v176 offset:16384
	ds_read_b128 v[200:203], v176 offset:17408
	ds_read_b128 v[204:207], v176 offset:18432
	ds_read_b128 v[208:211], v176 offset:19456
	ds_read_b128 v[212:215], v176 offset:20480
	ds_read_b128 v[216:219], v176 offset:21504
	ds_read_b128 v[220:223], v176 offset:22528
	ds_read_b128 v[224:227], v176 offset:23552
	global_load_lds_dwordx4 v[168:169], off
	s_add_i32 m0, s51, 0x2000
	s_add_u32 s60, s22, 0x28000
	v_lshl_add_u64 v[228:229], s[22:23], 0, v[138:139]
	s_addc_u32 s61, s23, 0
	s_add_i32 s51, s40, s27
	global_load_lds_dwordx4 v[228:229], off
	v_lshl_add_u64 v[230:231], s[60:61], 0, v[142:143]
	s_mov_b32 m0, s51
	v_lshl_add_u64 v[232:233], s[24:25], 0, v[140:141]
	global_load_lds_dwordx4 v[230:231], off
	v_lshl_add_u64 v[230:231], s[60:61], 0, v[138:139]
	s_add_i32 m0, s51, 0x2000
	s_nop 0
	global_load_lds_dwordx4 v[230:231], off
	v_lshl_add_u64 v[230:231], s[24:25], 0, v[144:145]
	s_mov_b32 m0, s29
	s_nop 0
	global_load_lds_dwordx4 v[230:231], off
	s_mov_b32 m0, s30
	s_nop 0
	global_load_lds_dwordx4 v[232:233], off
	s_waitcnt vmcnt(8)
	s_waitcnt lgkmcnt(0)
	s_barrier
	s_setprio 1
	s_waitcnt lgkmcnt(0)
	v_mfma_f32_16x16x32_f16 v[94:97], v[98:101], v[196:199], v[94:97]
	v_mfma_f32_16x16x32_f16 v[90:93], v[158:161], v[196:199], v[90:93]
	v_mfma_f32_16x16x32_f16 v[86:89], v[98:101], v[204:207], v[86:89]
	v_mfma_f32_16x16x32_f16 v[82:85], v[158:161], v[204:207], v[82:85]
	v_mfma_f32_16x16x32_f16 v[78:81], v[98:101], v[212:215], v[78:81]
	v_mfma_f32_16x16x32_f16 v[74:77], v[158:161], v[212:215], v[74:77]
	v_mfma_f32_16x16x32_f16 v[70:73], v[98:101], v[220:223], v[70:73]
	v_mfma_f32_16x16x32_f16 v[66:69], v[158:161], v[220:223], v[66:69]
	v_mfma_f32_16x16x32_f16 v[94:97], v[102:105], v[200:203], v[94:97]
	v_mfma_f32_16x16x32_f16 v[90:93], v[164:167], v[200:203], v[90:93]
	v_mfma_f32_16x16x32_f16 v[86:89], v[102:105], v[208:211], v[86:89]
	v_mfma_f32_16x16x32_f16 v[82:85], v[164:167], v[208:211], v[82:85]
	v_mfma_f32_16x16x32_f16 v[78:81], v[102:105], v[216:219], v[78:81]
	v_mfma_f32_16x16x32_f16 v[74:77], v[164:167], v[216:219], v[74:77]
	v_mfma_f32_16x16x32_f16 v[70:73], v[102:105], v[224:227], v[70:73]
	v_mfma_f32_16x16x32_f16 v[66:69], v[164:167], v[224:227], v[66:69]
	s_setprio 0
	s_setprio 1
	v_mfma_f32_16x16x32_f16 v[30:33], v[178:181], v[196:199], v[30:33]
	v_mfma_f32_16x16x32_f16 v[26:29], v[188:191], v[196:199], v[26:29]
	v_mfma_f32_16x16x32_f16 v[22:25], v[178:181], v[204:207], v[22:25]
	v_mfma_f32_16x16x32_f16 v[18:21], v[188:191], v[204:207], v[18:21]
	v_mfma_f32_16x16x32_f16 v[14:17], v[178:181], v[212:215], v[14:17]
	v_mfma_f32_16x16x32_f16 v[10:13], v[188:191], v[212:215], v[10:13]
	v_mfma_f32_16x16x32_f16 v[6:9], v[178:181], v[220:223], v[6:9]
	v_mfma_f32_16x16x32_f16 v[2:5], v[188:191], v[220:223], v[2:5]
	v_mfma_f32_16x16x32_f16 v[30:33], v[182:185], v[200:203], v[30:33]
	v_mfma_f32_16x16x32_f16 v[26:29], v[192:195], v[200:203], v[26:29]
	v_mfma_f32_16x16x32_f16 v[22:25], v[182:185], v[208:211], v[22:25]
	v_mfma_f32_16x16x32_f16 v[18:21], v[192:195], v[208:211], v[18:21]
	s_setprio 2
	s_barrier
	v_mfma_f32_16x16x32_f16 v[14:17], v[182:185], v[216:219], v[14:17]
	v_mfma_f32_16x16x32_f16 v[10:13], v[192:195], v[216:219], v[10:13]
	v_mfma_f32_16x16x32_f16 v[6:9], v[182:185], v[224:227], v[6:9]
	v_mfma_f32_16x16x32_f16 v[2:5], v[192:195], v[224:227], v[2:5]
	s_setprio 0
	s_nop 0
	s_add_i32 s51, 0, 0x18000
	s_add_i32 s60, 0, 0x1c000
	v_add_u32_e32 v164, s51, v163
	v_add_u32_e32 v177, s60, v163
	ds_read_b128 v[98:101], v164
	ds_read_b128 v[102:105], v164 offset:1024
	ds_read_b128 v[158:161], v164 offset:2048
	ds_read_b128 v[164:167], v164 offset:3072
	ds_read_b128 v[178:181], v177
	ds_read_b128 v[182:185], v177 offset:1024
	ds_read_b128 v[188:191], v177 offset:2048
	ds_read_b128 v[192:195], v177 offset:3072
	s_add_u32 s24, s24, 0x28000
	s_addc_u32 s25, s25, 0
	s_mov_b32 m0, s31
	v_lshl_add_u64 v[234:235], s[24:25], 0, v[144:145]
	ds_read_b128 v[196:199], v176 offset:32768
	ds_read_b128 v[200:203], v176 offset:33792
	ds_read_b128 v[204:207], v176 offset:34816
	ds_read_b128 v[208:211], v176 offset:35840
	ds_read_b128 v[212:215], v176 offset:36864
	ds_read_b128 v[216:219], v176 offset:37888
	ds_read_b128 v[220:223], v176 offset:38912
	ds_read_b128 v[224:227], v176 offset:39936
	global_load_lds_dwordx4 v[234:235], off
	v_lshl_add_u64 v[234:235], s[24:25], 0, v[140:141]
	s_mov_b32 m0, s33
	s_nop 0
	global_load_lds_dwordx4 v[234:235], off
	s_waitcnt vmcnt(8)
	s_waitcnt lgkmcnt(0)
	s_barrier
	s_setprio 1
	s_waitcnt lgkmcnt(0)
	v_mfma_f32_16x16x32_f16 v[134:137], v[98:101], v[196:199], v[134:137]
	v_mfma_f32_16x16x32_f16 v[130:133], v[158:161], v[196:199], v[130:133]
	v_mfma_f32_16x16x32_f16 v[126:129], v[98:101], v[204:207], v[126:129]
	v_mfma_f32_16x16x32_f16 v[122:125], v[158:161], v[204:207], v[122:125]
	v_mfma_f32_16x16x32_f16 v[118:121], v[98:101], v[212:215], v[118:121]
	v_mfma_f32_16x16x32_f16 v[114:117], v[158:161], v[212:215], v[114:117]
	v_mfma_f32_16x16x32_f16 v[110:113], v[98:101], v[220:223], v[110:113]
	v_mfma_f32_16x16x32_f16 v[106:109], v[158:161], v[220:223], v[106:109]
	v_mfma_f32_16x16x32_f16 v[134:137], v[102:105], v[200:203], v[134:137]
	v_mfma_f32_16x16x32_f16 v[130:133], v[164:167], v[200:203], v[130:133]
	v_mfma_f32_16x16x32_f16 v[126:129], v[102:105], v[208:211], v[126:129]
	v_mfma_f32_16x16x32_f16 v[122:125], v[164:167], v[208:211], v[122:125]
	v_mfma_f32_16x16x32_f16 v[118:121], v[102:105], v[216:219], v[118:121]
	v_mfma_f32_16x16x32_f16 v[114:117], v[164:167], v[216:219], v[114:117]
	v_mfma_f32_16x16x32_f16 v[110:113], v[102:105], v[224:227], v[110:113]
	v_mfma_f32_16x16x32_f16 v[106:109], v[164:167], v[224:227], v[106:109]
	s_setprio 0
	s_setprio 1
	v_mfma_f32_16x16x32_f16 v[62:65], v[178:181], v[196:199], v[62:65]
	v_mfma_f32_16x16x32_f16 v[58:61], v[188:191], v[196:199], v[58:61]
	v_mfma_f32_16x16x32_f16 v[54:57], v[178:181], v[204:207], v[54:57]
	v_mfma_f32_16x16x32_f16 v[50:53], v[188:191], v[204:207], v[50:53]
	v_mfma_f32_16x16x32_f16 v[46:49], v[178:181], v[212:215], v[46:49]
	v_mfma_f32_16x16x32_f16 v[42:45], v[188:191], v[212:215], v[42:45]
	v_mfma_f32_16x16x32_f16 v[38:41], v[178:181], v[220:223], v[38:41]
	v_mfma_f32_16x16x32_f16 v[34:37], v[188:191], v[220:223], v[34:37]
	v_mfma_f32_16x16x32_f16 v[62:65], v[182:185], v[200:203], v[62:65]
	v_mfma_f32_16x16x32_f16 v[58:61], v[192:195], v[200:203], v[58:61]
	v_mfma_f32_16x16x32_f16 v[54:57], v[182:185], v[208:211], v[54:57]
	v_mfma_f32_16x16x32_f16 v[50:53], v[192:195], v[208:211], v[50:53]
	s_setprio 2
	s_barrier
	v_mfma_f32_16x16x32_f16 v[46:49], v[182:185], v[216:219], v[46:49]
	v_mfma_f32_16x16x32_f16 v[42:45], v[192:195], v[216:219], v[42:45]
	v_mfma_f32_16x16x32_f16 v[38:41], v[182:185], v[224:227], v[38:41]
	v_mfma_f32_16x16x32_f16 v[34:37], v[192:195], v[224:227], v[34:37]
	s_setprio 0
	s_nop 0
	s_add_i32 s24, s51, s27
	v_lshl_add_u64 v[168:169], v[168:169], 0, s[14:15]
	s_mov_b32 m0, s24
	ds_read_b128 v[196:199], v176 offset:49152
	ds_read_b128 v[200:203], v176 offset:50176
	ds_read_b128 v[204:207], v176 offset:51200
	ds_read_b128 v[208:211], v176 offset:52224
	ds_read_b128 v[212:215], v176 offset:53248
	ds_read_b128 v[216:219], v176 offset:54272
	ds_read_b128 v[220:223], v176 offset:55296
	ds_read_b128 v[224:227], v176 offset:56320
	global_load_lds_dwordx4 v[168:169], off
	s_add_i32 m0, s24, 0x2000
	s_add_u32 s22, s22, 0x28080
	v_lshl_add_u64 v[168:169], v[228:229], 0, s[14:15]
	s_addc_u32 s23, s23, 0
	s_add_i32 s24, s60, s27
	global_load_lds_dwordx4 v[168:169], off
	v_lshl_add_u64 v[168:169], s[22:23], 0, v[142:143]
	s_mov_b32 m0, s24
	s_nop 0
	global_load_lds_dwordx4 v[168:169], off
	v_lshl_add_u64 v[168:169], s[22:23], 0, v[138:139]
	s_add_i32 m0, s24, 0x2000
	s_nop 0
	global_load_lds_dwordx4 v[168:169], off
	v_lshl_add_u64 v[168:169], v[230:231], 0, s[14:15]
	s_mov_b32 m0, s36
	s_nop 0
	global_load_lds_dwordx4 v[168:169], off
	v_lshl_add_u64 v[168:169], v[232:233], 0, s[14:15]
	s_mov_b32 m0, s37
	s_nop 0
	global_load_lds_dwordx4 v[168:169], off
	s_waitcnt vmcnt(8)
	s_waitcnt lgkmcnt(0)
	s_barrier
	s_setprio 1
	s_waitcnt lgkmcnt(0)
	v_mfma_f32_16x16x32_f16 v[94:97], v[98:101], v[196:199], v[94:97]
	v_mfma_f32_16x16x32_f16 v[90:93], v[158:161], v[196:199], v[90:93]
	v_mfma_f32_16x16x32_f16 v[86:89], v[98:101], v[204:207], v[86:89]
	v_mfma_f32_16x16x32_f16 v[82:85], v[158:161], v[204:207], v[82:85]
	v_mfma_f32_16x16x32_f16 v[78:81], v[98:101], v[212:215], v[78:81]
	v_mfma_f32_16x16x32_f16 v[74:77], v[158:161], v[212:215], v[74:77]
	v_mfma_f32_16x16x32_f16 v[70:73], v[98:101], v[220:223], v[70:73]
	v_mfma_f32_16x16x32_f16 v[66:69], v[158:161], v[220:223], v[66:69]
	v_mfma_f32_16x16x32_f16 v[94:97], v[102:105], v[200:203], v[94:97]
	v_mfma_f32_16x16x32_f16 v[90:93], v[164:167], v[200:203], v[90:93]
	v_mfma_f32_16x16x32_f16 v[86:89], v[102:105], v[208:211], v[86:89]
	v_mfma_f32_16x16x32_f16 v[82:85], v[164:167], v[208:211], v[82:85]
	v_mfma_f32_16x16x32_f16 v[78:81], v[102:105], v[216:219], v[78:81]
	v_mfma_f32_16x16x32_f16 v[74:77], v[164:167], v[216:219], v[74:77]
	v_mfma_f32_16x16x32_f16 v[70:73], v[102:105], v[224:227], v[70:73]
	v_mfma_f32_16x16x32_f16 v[66:69], v[164:167], v[224:227], v[66:69]
	s_setprio 0
	s_setprio 1
	v_mfma_f32_16x16x32_f16 v[30:33], v[178:181], v[196:199], v[30:33]
	v_mfma_f32_16x16x32_f16 v[26:29], v[188:191], v[196:199], v[26:29]
	v_mfma_f32_16x16x32_f16 v[22:25], v[178:181], v[204:207], v[22:25]
	v_mfma_f32_16x16x32_f16 v[18:21], v[188:191], v[204:207], v[18:21]
	v_mfma_f32_16x16x32_f16 v[14:17], v[178:181], v[212:215], v[14:17]
	v_mfma_f32_16x16x32_f16 v[10:13], v[188:191], v[212:215], v[10:13]
	v_mfma_f32_16x16x32_f16 v[6:9], v[178:181], v[220:223], v[6:9]
	v_mfma_f32_16x16x32_f16 v[2:5], v[188:191], v[220:223], v[2:5]
	v_mfma_f32_16x16x32_f16 v[30:33], v[182:185], v[200:203], v[30:33]
	v_mfma_f32_16x16x32_f16 v[26:29], v[192:195], v[200:203], v[26:29]
	v_mfma_f32_16x16x32_f16 v[22:25], v[182:185], v[208:211], v[22:25]
	v_mfma_f32_16x16x32_f16 v[18:21], v[192:195], v[208:211], v[18:21]
	s_setprio 2
	s_barrier
	v_mfma_f32_16x16x32_f16 v[14:17], v[182:185], v[216:219], v[14:17]
	v_mfma_f32_16x16x32_f16 v[10:13], v[192:195], v[216:219], v[10:13]
	v_mfma_f32_16x16x32_f16 v[6:9], v[182:185], v[224:227], v[6:9]
	v_mfma_f32_16x16x32_f16 v[2:5], v[192:195], v[224:227], v[2:5]
	s_setprio 0
	s_nop 0
	s_add_i32 s50, s50, 2
	s_add_u32 s20, s20, 0x100
	s_addc_u32 s21, s21, 0
	s_add_u32 s48, s48, 0x100
	s_addc_u32 s49, s49, 0
	s_cmp_gt_u32 s50, 7
	s_cbranch_scc0 .LBB0_1649
	s_and_b64 vcc, exec, s[16:17]
	s_cbranch_vccz .LBB0_1652
	s_barrier

.LBB0_1734:
	ds_read_b128 v[130:133], v177
	ds_read_b128 v[134:137], v177 offset:1024
	ds_read_b128 v[138:141], v177 offset:2048
	ds_read_b128 v[142:145], v177 offset:3072
	ds_read_b128 v[164:167], v178
	ds_read_b128 v[168:171], v178 offset:1024
	ds_read_b128 v[172:175], v178 offset:2048
	ds_read_b128 v[180:183], v178 offset:3072
	s_add_u32 s28, s26, 0xfffc0080
	s_addc_u32 s29, s27, -1
	s_cmp_eq_u32 s50, 12
	s_cselect_b32 s31, s19, s29
	s_cselect_b32 s30, s46, s28
	s_cselect_b32 s29, s17, s49
	s_cselect_b32 s28, s47, s48
	v_lshl_add_u64 v[184:185], s[26:27], 0, v[154:155]
	s_add_i32 m0, s25, 0xc000
	ds_read_b128 v[188:191], v179
	ds_read_b128 v[192:195], v179 offset:1024
	ds_read_b128 v[196:199], v179 offset:2048
	ds_read_b128 v[200:203], v179 offset:3072
	ds_read_b128 v[204:207], v179 offset:4096
	ds_read_b128 v[208:211], v179 offset:5120
	ds_read_b128 v[212:215], v179 offset:6144
	ds_read_b128 v[216:219], v179 offset:7168
	global_load_lds_dwordx4 v[184:185], off
	v_lshl_add_u64 v[184:185], s[26:27], 0, v[156:157]
	s_add_i32 m0, s25, 0xe000
	s_nop 0
	global_load_lds_dwordx4 v[184:185], off
	s_waitcnt vmcnt(8)
	s_waitcnt lgkmcnt(0)
	s_barrier
	s_setprio 1
	s_waitcnt lgkmcnt(0)
	v_mfma_f32_16x16x32_f16 v[126:129], v[130:133], v[188:191], v[126:129]
	v_mfma_f32_16x16x32_f16 v[122:125], v[138:141], v[188:191], v[122:125]
	v_mfma_f32_16x16x32_f16 v[118:121], v[130:133], v[196:199], v[118:121]
	v_mfma_f32_16x16x32_f16 v[114:117], v[138:141], v[196:199], v[114:117]
	v_mfma_f32_16x16x32_f16 v[110:113], v[130:133], v[204:207], v[110:113]
	v_mfma_f32_16x16x32_f16 v[106:109], v[138:141], v[204:207], v[106:109]
	v_mfma_f32_16x16x32_f16 v[102:105], v[130:133], v[212:215], v[102:105]
	v_mfma_f32_16x16x32_f16 v[98:101], v[138:141], v[212:215], v[98:101]
	v_mfma_f32_16x16x32_f16 v[126:129], v[134:137], v[192:195], v[126:129]
	v_mfma_f32_16x16x32_f16 v[122:125], v[142:145], v[192:195], v[122:125]
	v_mfma_f32_16x16x32_f16 v[118:121], v[134:137], v[200:203], v[118:121]
	v_mfma_f32_16x16x32_f16 v[114:117], v[142:145], v[200:203], v[114:117]
	v_mfma_f32_16x16x32_f16 v[110:113], v[134:137], v[208:211], v[110:113]
	v_mfma_f32_16x16x32_f16 v[106:109], v[142:145], v[208:211], v[106:109]
	v_mfma_f32_16x16x32_f16 v[102:105], v[134:137], v[216:219], v[102:105]
	v_mfma_f32_16x16x32_f16 v[98:101], v[142:145], v[216:219], v[98:101]
	s_setprio 0
	s_setprio 1
	v_mfma_f32_16x16x32_f16 v[62:65], v[164:167], v[188:191], v[62:65]
	v_mfma_f32_16x16x32_f16 v[58:61], v[172:175], v[188:191], v[58:61]
	v_mfma_f32_16x16x32_f16 v[54:57], v[164:167], v[196:199], v[54:57]
	v_mfma_f32_16x16x32_f16 v[50:53], v[172:175], v[196:199], v[50:53]
	v_mfma_f32_16x16x32_f16 v[46:49], v[164:167], v[204:207], v[46:49]
	v_mfma_f32_16x16x32_f16 v[42:45], v[172:175], v[204:207], v[42:45]
	v_mfma_f32_16x16x32_f16 v[38:41], v[164:167], v[212:215], v[38:41]
	v_mfma_f32_16x16x32_f16 v[34:37], v[172:175], v[212:215], v[34:37]
	v_mfma_f32_16x16x32_f16 v[62:65], v[168:171], v[192:195], v[62:65]
	v_mfma_f32_16x16x32_f16 v[58:61], v[180:183], v[192:195], v[58:61]
	v_mfma_f32_16x16x32_f16 v[54:57], v[168:171], v[200:203], v[54:57]
	v_mfma_f32_16x16x32_f16 v[50:53], v[180:183], v[200:203], v[50:53]
	s_setprio 2
	s_barrier
	v_mfma_f32_16x16x32_f16 v[46:49], v[168:171], v[208:211], v[46:49]
	v_mfma_f32_16x16x32_f16 v[42:45], v[180:183], v[208:211], v[42:45]
	v_mfma_f32_16x16x32_f16 v[38:41], v[168:171], v[216:219], v[38:41]
	v_mfma_f32_16x16x32_f16 v[34:37], v[180:183], v[216:219], v[34:37]
	s_setprio 0
	s_nop 0
	s_add_i32 s51, s43, s35
	v_lshl_add_u64 v[184:185], s[28:29], 0, v[148:149]
	s_mov_b32 m0, s51
	ds_read_b128 v[188:191], v179 offset:16384
	ds_read_b128 v[192:195], v179 offset:17408
	ds_read_b128 v[196:199], v179 offset:18432
	ds_read_b128 v[200:203], v179 offset:19456
	ds_read_b128 v[204:207], v179 offset:20480
	ds_read_b128 v[208:211], v179 offset:21504
	ds_read_b128 v[212:215], v179 offset:22528
	ds_read_b128 v[216:219], v179 offset:23552
	global_load_lds_dwordx4 v[184:185], off
	s_add_i32 m0, s51, 0x2000
	s_add_u32 s60, s28, 0x40000
	v_lshl_add_u64 v[220:221], s[28:29], 0, v[152:153]
	s_addc_u32 s61, s29, 0
	s_add_i32 s51, s44, s35
	global_load_lds_dwordx4 v[220:221], off
	v_lshl_add_u64 v[222:223], s[60:61], 0, v[148:149]
	s_mov_b32 m0, s51
	v_lshl_add_u64 v[224:225], s[30:31], 0, v[150:151]
	global_load_lds_dwordx4 v[222:223], off
	v_lshl_add_u64 v[222:223], s[60:61], 0, v[152:153]
	s_add_i32 m0, s51, 0x2000
	s_nop 0
	global_load_lds_dwordx4 v[222:223], off
	v_lshl_add_u64 v[222:223], s[30:31], 0, v[146:147]
	s_mov_b32 m0, s25
	s_nop 0
	global_load_lds_dwordx4 v[222:223], off
	s_mov_b32 m0, s36
	s_nop 0
	global_load_lds_dwordx4 v[224:225], off
	s_waitcnt vmcnt(8)
	s_waitcnt lgkmcnt(0)
	s_barrier
	s_setprio 1
	s_waitcnt lgkmcnt(0)
	v_mfma_f32_16x16x32_f16 v[94:97], v[130:133], v[188:191], v[94:97]
	v_mfma_f32_16x16x32_f16 v[90:93], v[138:141], v[188:191], v[90:93]
	v_mfma_f32_16x16x32_f16 v[86:89], v[130:133], v[196:199], v[86:89]
	v_mfma_f32_16x16x32_f16 v[82:85], v[138:141], v[196:199], v[82:85]
	v_mfma_f32_16x16x32_f16 v[78:81], v[130:133], v[204:207], v[78:81]
	v_mfma_f32_16x16x32_f16 v[74:77], v[138:141], v[204:207], v[74:77]
	v_mfma_f32_16x16x32_f16 v[70:73], v[130:133], v[212:215], v[70:73]
	v_mfma_f32_16x16x32_f16 v[66:69], v[138:141], v[212:215], v[66:69]
	v_mfma_f32_16x16x32_f16 v[94:97], v[134:137], v[192:195], v[94:97]
	v_mfma_f32_16x16x32_f16 v[90:93], v[142:145], v[192:195], v[90:93]
	v_mfma_f32_16x16x32_f16 v[86:89], v[134:137], v[200:203], v[86:89]
	v_mfma_f32_16x16x32_f16 v[82:85], v[142:145], v[200:203], v[82:85]
	v_mfma_f32_16x16x32_f16 v[78:81], v[134:137], v[208:211], v[78:81]
	v_mfma_f32_16x16x32_f16 v[74:77], v[142:145], v[208:211], v[74:77]
	v_mfma_f32_16x16x32_f16 v[70:73], v[134:137], v[216:219], v[70:73]
	v_mfma_f32_16x16x32_f16 v[66:69], v[142:145], v[216:219], v[66:69]
	s_setprio 0
	s_setprio 1
	v_mfma_f32_16x16x32_f16 v[30:33], v[164:167], v[188:191], v[30:33]
	v_mfma_f32_16x16x32_f16 v[26:29], v[172:175], v[188:191], v[26:29]
	v_mfma_f32_16x16x32_f16 v[22:25], v[164:167], v[196:199], v[22:25]
	v_mfma_f32_16x16x32_f16 v[18:21], v[172:175], v[196:199], v[18:21]
	v_mfma_f32_16x16x32_f16 v[14:17], v[164:167], v[204:207], v[14:17]
	v_mfma_f32_16x16x32_f16 v[10:13], v[172:175], v[204:207], v[10:13]
	v_mfma_f32_16x16x32_f16 v[6:9], v[164:167], v[212:215], v[6:9]
	v_mfma_f32_16x16x32_f16 v[2:5], v[172:175], v[212:215], v[2:5]
	v_mfma_f32_16x16x32_f16 v[30:33], v[168:171], v[192:195], v[30:33]
	v_mfma_f32_16x16x32_f16 v[26:29], v[180:183], v[192:195], v[26:29]
	v_mfma_f32_16x16x32_f16 v[22:25], v[168:171], v[200:203], v[22:25]
	v_mfma_f32_16x16x32_f16 v[18:21], v[180:183], v[200:203], v[18:21]
	s_setprio 2
	s_barrier
	v_mfma_f32_16x16x32_f16 v[14:17], v[168:171], v[208:211], v[14:17]
	v_mfma_f32_16x16x32_f16 v[10:13], v[180:183], v[208:211], v[10:13]
	v_mfma_f32_16x16x32_f16 v[6:9], v[168:171], v[216:219], v[6:9]
	v_mfma_f32_16x16x32_f16 v[2:5], v[180:183], v[216:219], v[2:5]
	s_setprio 0
	s_nop 0
	s_add_i32 s51, 0, 0x18000
	s_add_i32 s60, 0, 0x1c000
	v_add_u32_e32 v142, s51, v163
	v_add_u32_e32 v180, s60, v163
	ds_read_b128 v[130:133], v142
	ds_read_b128 v[134:137], v142 offset:1024
	ds_read_b128 v[138:141], v142 offset:2048
	ds_read_b128 v[142:145], v142 offset:3072
	ds_read_b128 v[164:167], v180
	ds_read_b128 v[168:171], v180 offset:1024
	ds_read_b128 v[172:175], v180 offset:2048
	ds_read_b128 v[180:183], v180 offset:3072
	s_add_u32 s30, s30, 0x40000
	s_addc_u32 s31, s31, 0
	s_mov_b32 m0, s37
	v_lshl_add_u64 v[226:227], s[30:31], 0, v[146:147]
	ds_read_b128 v[188:191], v179 offset:32768
	ds_read_b128 v[192:195], v179 offset:33792
	ds_read_b128 v[196:199], v179 offset:34816
	ds_read_b128 v[200:203], v179 offset:35840
	ds_read_b128 v[204:207], v179 offset:36864
	ds_read_b128 v[208:211], v179 offset:37888
	ds_read_b128 v[212:215], v179 offset:38912
	ds_read_b128 v[216:219], v179 offset:39936
	global_load_lds_dwordx4 v[226:227], off
	v_lshl_add_u64 v[226:227], s[30:31], 0, v[150:151]
	s_mov_b32 m0, s38
	s_nop 0
	global_load_lds_dwordx4 v[226:227], off
	s_waitcnt vmcnt(8)
	s_waitcnt lgkmcnt(0)
	s_barrier
	s_setprio 1
	s_waitcnt lgkmcnt(0)
	v_mfma_f32_16x16x32_f16 v[126:129], v[130:133], v[188:191], v[126:129]
	v_mfma_f32_16x16x32_f16 v[122:125], v[138:141], v[188:191], v[122:125]
	v_mfma_f32_16x16x32_f16 v[118:121], v[130:133], v[196:199], v[118:121]
	v_mfma_f32_16x16x32_f16 v[114:117], v[138:141], v[196:199], v[114:117]
	v_mfma_f32_16x16x32_f16 v[110:113], v[130:133], v[204:207], v[110:113]
	v_mfma_f32_16x16x32_f16 v[106:109], v[138:141], v[204:207], v[106:109]
	v_mfma_f32_16x16x32_f16 v[102:105], v[130:133], v[212:215], v[102:105]
	v_mfma_f32_16x16x32_f16 v[98:101], v[138:141], v[212:215], v[98:101]
	v_mfma_f32_16x16x32_f16 v[126:129], v[134:137], v[192:195], v[126:129]
	v_mfma_f32_16x16x32_f16 v[122:125], v[142:145], v[192:195], v[122:125]
	v_mfma_f32_16x16x32_f16 v[118:121], v[134:137], v[200:203], v[118:121]
	v_mfma_f32_16x16x32_f16 v[114:117], v[142:145], v[200:203], v[114:117]
	v_mfma_f32_16x16x32_f16 v[110:113], v[134:137], v[208:211], v[110:113]
	v_mfma_f32_16x16x32_f16 v[106:109], v[142:145], v[208:211], v[106:109]
	v_mfma_f32_16x16x32_f16 v[102:105], v[134:137], v[216:219], v[102:105]
	v_mfma_f32_16x16x32_f16 v[98:101], v[142:145], v[216:219], v[98:101]
	s_setprio 0
	s_setprio 1
	v_mfma_f32_16x16x32_f16 v[62:65], v[164:167], v[188:191], v[62:65]
	v_mfma_f32_16x16x32_f16 v[58:61], v[172:175], v[188:191], v[58:61]
	v_mfma_f32_16x16x32_f16 v[54:57], v[164:167], v[196:199], v[54:57]
	v_mfma_f32_16x16x32_f16 v[50:53], v[172:175], v[196:199], v[50:53]
	v_mfma_f32_16x16x32_f16 v[46:49], v[164:167], v[204:207], v[46:49]
	v_mfma_f32_16x16x32_f16 v[42:45], v[172:175], v[204:207], v[42:45]
	v_mfma_f32_16x16x32_f16 v[38:41], v[164:167], v[212:215], v[38:41]
	v_mfma_f32_16x16x32_f16 v[34:37], v[172:175], v[212:215], v[34:37]
	v_mfma_f32_16x16x32_f16 v[62:65], v[168:171], v[192:195], v[62:65]
	v_mfma_f32_16x16x32_f16 v[58:61], v[180:183], v[192:195], v[58:61]
	v_mfma_f32_16x16x32_f16 v[54:57], v[168:171], v[200:203], v[54:57]
	v_mfma_f32_16x16x32_f16 v[50:53], v[180:183], v[200:203], v[50:53]
	s_setprio 2
	s_barrier
	v_mfma_f32_16x16x32_f16 v[46:49], v[168:171], v[208:211], v[46:49]
	v_mfma_f32_16x16x32_f16 v[42:45], v[180:183], v[208:211], v[42:45]
	v_mfma_f32_16x16x32_f16 v[38:41], v[168:171], v[216:219], v[38:41]
	v_mfma_f32_16x16x32_f16 v[34:37], v[180:183], v[216:219], v[34:37]
	s_setprio 0
	s_nop 0
	s_add_i32 s30, s51, s35
	v_lshl_add_u64 v[184:185], v[184:185], 0, s[12:13]
	s_mov_b32 m0, s30
	ds_read_b128 v[188:191], v179 offset:49152
	ds_read_b128 v[192:195], v179 offset:50176
	ds_read_b128 v[196:199], v179 offset:51200
	ds_read_b128 v[200:203], v179 offset:52224
	ds_read_b128 v[204:207], v179 offset:53248
	ds_read_b128 v[208:211], v179 offset:54272
	ds_read_b128 v[212:215], v179 offset:55296
	ds_read_b128 v[216:219], v179 offset:56320
	global_load_lds_dwordx4 v[184:185], off
	s_add_i32 m0, s30, 0x2000
	s_add_u32 s28, s28, 0x40080
	v_lshl_add_u64 v[184:185], v[220:221], 0, s[12:13]
	s_addc_u32 s29, s29, 0
	s_add_i32 s30, s60, s35
	global_load_lds_dwordx4 v[184:185], off
	v_lshl_add_u64 v[184:185], s[28:29], 0, v[148:149]
	s_mov_b32 m0, s30
	s_nop 0
	global_load_lds_dwordx4 v[184:185], off
	v_lshl_add_u64 v[184:185], s[28:29], 0, v[152:153]
	s_add_i32 m0, s30, 0x2000
	s_nop 0
	global_load_lds_dwordx4 v[184:185], off
	v_lshl_add_u64 v[184:185], v[222:223], 0, s[12:13]
	s_mov_b32 m0, s40
	s_nop 0
	global_load_lds_dwordx4 v[184:185], off
	v_lshl_add_u64 v[184:185], v[224:225], 0, s[12:13]
	s_mov_b32 m0, s41
	s_nop 0
	global_load_lds_dwordx4 v[184:185], off
	s_waitcnt vmcnt(8)
	s_waitcnt lgkmcnt(0)
	s_barrier
	s_setprio 1
	s_waitcnt lgkmcnt(0)
	v_mfma_f32_16x16x32_f16 v[94:97], v[130:133], v[188:191], v[94:97]
	v_mfma_f32_16x16x32_f16 v[90:93], v[138:141], v[188:191], v[90:93]
	v_mfma_f32_16x16x32_f16 v[86:89], v[130:133], v[196:199], v[86:89]
	v_mfma_f32_16x16x32_f16 v[82:85], v[138:141], v[196:199], v[82:85]
	v_mfma_f32_16x16x32_f16 v[78:81], v[130:133], v[204:207], v[78:81]
	v_mfma_f32_16x16x32_f16 v[74:77], v[138:141], v[204:207], v[74:77]
	v_mfma_f32_16x16x32_f16 v[70:73], v[130:133], v[212:215], v[70:73]
	v_mfma_f32_16x16x32_f16 v[66:69], v[138:141], v[212:215], v[66:69]
	v_mfma_f32_16x16x32_f16 v[94:97], v[134:137], v[192:195], v[94:97]
	v_mfma_f32_16x16x32_f16 v[90:93], v[142:145], v[192:195], v[90:93]
	v_mfma_f32_16x16x32_f16 v[86:89], v[134:137], v[200:203], v[86:89]
	v_mfma_f32_16x16x32_f16 v[82:85], v[142:145], v[200:203], v[82:85]
	v_mfma_f32_16x16x32_f16 v[78:81], v[134:137], v[208:211], v[78:81]
	v_mfma_f32_16x16x32_f16 v[74:77], v[142:145], v[208:211], v[74:77]
	v_mfma_f32_16x16x32_f16 v[70:73], v[134:137], v[216:219], v[70:73]
	v_mfma_f32_16x16x32_f16 v[66:69], v[142:145], v[216:219], v[66:69]
	s_setprio 0
	s_setprio 1
	v_mfma_f32_16x16x32_f16 v[30:33], v[164:167], v[188:191], v[30:33]
	v_mfma_f32_16x16x32_f16 v[26:29], v[172:175], v[188:191], v[26:29]
	v_mfma_f32_16x16x32_f16 v[22:25], v[164:167], v[196:199], v[22:25]
	v_mfma_f32_16x16x32_f16 v[18:21], v[172:175], v[196:199], v[18:21]
	v_mfma_f32_16x16x32_f16 v[14:17], v[164:167], v[204:207], v[14:17]
	v_mfma_f32_16x16x32_f16 v[10:13], v[172:175], v[204:207], v[10:13]
	v_mfma_f32_16x16x32_f16 v[6:9], v[164:167], v[212:215], v[6:9]
	v_mfma_f32_16x16x32_f16 v[2:5], v[172:175], v[212:215], v[2:5]
	v_mfma_f32_16x16x32_f16 v[30:33], v[168:171], v[192:195], v[30:33]
	v_mfma_f32_16x16x32_f16 v[26:29], v[180:183], v[192:195], v[26:29]
	v_mfma_f32_16x16x32_f16 v[22:25], v[168:171], v[200:203], v[22:25]
	v_mfma_f32_16x16x32_f16 v[18:21], v[180:183], v[200:203], v[18:21]
	s_setprio 2
	s_barrier
	v_mfma_f32_16x16x32_f16 v[14:17], v[168:171], v[208:211], v[14:17]
	v_mfma_f32_16x16x32_f16 v[10:13], v[180:183], v[208:211], v[10:13]
	v_mfma_f32_16x16x32_f16 v[6:9], v[168:171], v[216:219], v[6:9]
	v_mfma_f32_16x16x32_f16 v[2:5], v[180:183], v[216:219], v[2:5]
	s_setprio 0
	s_nop 0
	s_add_i32 s50, s50, 2
	s_add_u32 s26, s26, 0x100
	s_addc_u32 s27, s27, 0
	s_add_u32 s48, s48, 0x100
	s_addc_u32 s49, s49, 0
	s_cmp_gt_u32 s50, 13
	s_cbranch_scc0 .LBB0_1734
	s_and_b64 vcc, exec, s[14:15]
	s_cbranch_vccz .LBB0_1737
	s_barrier

.LBB0_1813:
	ds_read_b128 v[146:149], v154
	ds_read_b128 v[158:161], v154 offset:1024
	ds_read_b128 v[164:167], v154 offset:2048
	ds_read_b128 v[168:171], v154 offset:3072
	ds_read_b128 v[172:175], v155
	ds_read_b128 v[176:179], v155 offset:1024
	ds_read_b128 v[180:183], v155 offset:2048
	ds_read_b128 v[188:191], v155 offset:3072
	s_add_u32 s36, s34, 0xfff80080
	s_addc_u32 s37, s35, -1
	s_cmp_eq_u32 s65, 28
	s_cselect_b32 s39, s25, s37
	s_cselect_b32 s38, s61, s36
	s_cselect_b32 s37, s23, s64
	s_cselect_b32 s36, s62, s63
	v_lshl_add_u64 v[150:151], s[34:35], 0, v[138:139]
	s_add_i32 m0, s31, 0xc000
	ds_read_b128 v[192:195], v156
	ds_read_b128 v[196:199], v156 offset:1024
	ds_read_b128 v[200:203], v156 offset:2048
	ds_read_b128 v[204:207], v156 offset:3072
	ds_read_b128 v[208:211], v156 offset:4096
	ds_read_b128 v[212:215], v156 offset:5120
	ds_read_b128 v[216:219], v156 offset:6144
	ds_read_b128 v[220:223], v156 offset:7168
	global_load_lds_dwordx4 v[150:151], off
	v_lshl_add_u64 v[150:151], s[34:35], 0, v[140:141]
	s_add_i32 m0, s31, 0xe000
	s_nop 0
	global_load_lds_dwordx4 v[150:151], off
	s_waitcnt vmcnt(8)
	s_waitcnt lgkmcnt(0)
	s_barrier
	s_setprio 1
	s_waitcnt lgkmcnt(0)
	v_mfma_f32_16x16x32_f16 v[126:129], v[146:149], v[192:195], v[126:129]
	v_mfma_f32_16x16x32_f16 v[122:125], v[164:167], v[192:195], v[122:125]
	v_mfma_f32_16x16x32_f16 v[110:113], v[146:149], v[200:203], v[110:113]
	v_mfma_f32_16x16x32_f16 v[106:109], v[164:167], v[200:203], v[106:109]
	v_mfma_f32_16x16x32_f16 v[94:97], v[146:149], v[208:211], v[94:97]
	v_mfma_f32_16x16x32_f16 v[90:93], v[164:167], v[208:211], v[90:93]
	v_mfma_f32_16x16x32_f16 v[78:81], v[146:149], v[216:219], v[78:81]
	v_mfma_f32_16x16x32_f16 v[74:77], v[164:167], v[216:219], v[74:77]
	v_mfma_f32_16x16x32_f16 v[126:129], v[158:161], v[196:199], v[126:129]
	v_mfma_f32_16x16x32_f16 v[122:125], v[168:171], v[196:199], v[122:125]
	v_mfma_f32_16x16x32_f16 v[110:113], v[158:161], v[204:207], v[110:113]
	v_mfma_f32_16x16x32_f16 v[106:109], v[168:171], v[204:207], v[106:109]
	v_mfma_f32_16x16x32_f16 v[94:97], v[158:161], v[212:215], v[94:97]
	v_mfma_f32_16x16x32_f16 v[90:93], v[168:171], v[212:215], v[90:93]
	v_mfma_f32_16x16x32_f16 v[78:81], v[158:161], v[220:223], v[78:81]
	v_mfma_f32_16x16x32_f16 v[74:77], v[168:171], v[220:223], v[74:77]
	s_setprio 0
	s_setprio 1
	v_mfma_f32_16x16x32_f16 v[118:121], v[172:175], v[192:195], v[118:121]
	v_mfma_f32_16x16x32_f16 v[114:117], v[180:183], v[192:195], v[114:117]
	v_mfma_f32_16x16x32_f16 v[102:105], v[172:175], v[200:203], v[102:105]
	v_mfma_f32_16x16x32_f16 v[98:101], v[180:183], v[200:203], v[98:101]
	v_mfma_f32_16x16x32_f16 v[86:89], v[172:175], v[208:211], v[86:89]
	v_mfma_f32_16x16x32_f16 v[82:85], v[180:183], v[208:211], v[82:85]
	v_mfma_f32_16x16x32_f16 v[70:73], v[172:175], v[216:219], v[70:73]
	v_mfma_f32_16x16x32_f16 v[66:69], v[180:183], v[216:219], v[66:69]
	v_mfma_f32_16x16x32_f16 v[118:121], v[176:179], v[196:199], v[118:121]
	v_mfma_f32_16x16x32_f16 v[114:117], v[188:191], v[196:199], v[114:117]
	v_mfma_f32_16x16x32_f16 v[102:105], v[176:179], v[204:207], v[102:105]
	v_mfma_f32_16x16x32_f16 v[98:101], v[188:191], v[204:207], v[98:101]
	s_setprio 2
	s_barrier
	v_mfma_f32_16x16x32_f16 v[86:89], v[176:179], v[212:215], v[86:89]
	v_mfma_f32_16x16x32_f16 v[82:85], v[188:191], v[212:215], v[82:85]
	v_mfma_f32_16x16x32_f16 v[70:73], v[176:179], v[220:223], v[70:73]
	v_mfma_f32_16x16x32_f16 v[66:69], v[188:191], v[220:223], v[66:69]
	s_setprio 0
	s_nop 0
	s_add_i32 s66, s50, s42
	v_lshl_add_u64 v[150:151], s[36:37], 0, v[132:133]
	s_mov_b32 m0, s66
	ds_read_b128 v[192:195], v156 offset:16384
	ds_read_b128 v[196:199], v156 offset:17408
	ds_read_b128 v[200:203], v156 offset:18432
	ds_read_b128 v[204:207], v156 offset:19456
	ds_read_b128 v[208:211], v156 offset:20480
	ds_read_b128 v[212:215], v156 offset:21504
	ds_read_b128 v[216:219], v156 offset:22528
	ds_read_b128 v[220:223], v156 offset:23552
	global_load_lds_dwordx4 v[150:151], off
	s_add_i32 m0, s66, 0x2000
	s_add_u32 s66, s36, 0x80000
	v_lshl_add_u64 v[184:185], s[36:37], 0, v[136:137]
	s_addc_u32 s67, s37, 0
	s_add_i32 s68, s51, s42
	global_load_lds_dwordx4 v[184:185], off
	v_lshl_add_u64 v[224:225], s[66:67], 0, v[132:133]
	s_mov_b32 m0, s68
	v_lshl_add_u64 v[226:227], s[38:39], 0, v[134:135]
	global_load_lds_dwordx4 v[224:225], off
	v_lshl_add_u64 v[224:225], s[66:67], 0, v[136:137]
	s_add_i32 m0, s68, 0x2000
	s_nop 0
	global_load_lds_dwordx4 v[224:225], off
	v_lshl_add_u64 v[224:225], s[38:39], 0, v[130:131]
	s_mov_b32 m0, s31
	s_nop 0
	global_load_lds_dwordx4 v[224:225], off
	s_mov_b32 m0, s43
	s_nop 0
	global_load_lds_dwordx4 v[226:227], off
	s_waitcnt vmcnt(8)
	s_waitcnt lgkmcnt(0)
	s_barrier
	s_setprio 1
	s_waitcnt lgkmcnt(0)
	v_mfma_f32_16x16x32_f16 v[62:65], v[146:149], v[192:195], v[62:65]
	v_mfma_f32_16x16x32_f16 v[58:61], v[164:167], v[192:195], v[58:61]
	v_mfma_f32_16x16x32_f16 v[46:49], v[146:149], v[200:203], v[46:49]
	v_mfma_f32_16x16x32_f16 v[42:45], v[164:167], v[200:203], v[42:45]
	v_mfma_f32_16x16x32_f16 v[30:33], v[146:149], v[208:211], v[30:33]
	v_mfma_f32_16x16x32_f16 v[26:29], v[164:167], v[208:211], v[26:29]
	v_mfma_f32_16x16x32_f16 v[14:17], v[146:149], v[216:219], v[14:17]
	v_mfma_f32_16x16x32_f16 v[10:13], v[164:167], v[216:219], v[10:13]
	v_mfma_f32_16x16x32_f16 v[62:65], v[158:161], v[196:199], v[62:65]
	v_mfma_f32_16x16x32_f16 v[58:61], v[168:171], v[196:199], v[58:61]
	v_mfma_f32_16x16x32_f16 v[46:49], v[158:161], v[204:207], v[46:49]
	v_mfma_f32_16x16x32_f16 v[42:45], v[168:171], v[204:207], v[42:45]
	v_mfma_f32_16x16x32_f16 v[30:33], v[158:161], v[212:215], v[30:33]
	v_mfma_f32_16x16x32_f16 v[26:29], v[168:171], v[212:215], v[26:29]
	v_mfma_f32_16x16x32_f16 v[14:17], v[158:161], v[220:223], v[14:17]
	v_mfma_f32_16x16x32_f16 v[10:13], v[168:171], v[220:223], v[10:13]
	s_setprio 0
	s_setprio 1
	v_mfma_f32_16x16x32_f16 v[54:57], v[172:175], v[192:195], v[54:57]
	v_mfma_f32_16x16x32_f16 v[50:53], v[180:183], v[192:195], v[50:53]
	v_mfma_f32_16x16x32_f16 v[38:41], v[172:175], v[200:203], v[38:41]
	v_mfma_f32_16x16x32_f16 v[34:37], v[180:183], v[200:203], v[34:37]
	v_mfma_f32_16x16x32_f16 v[22:25], v[172:175], v[208:211], v[22:25]
	v_mfma_f32_16x16x32_f16 v[18:21], v[180:183], v[208:211], v[18:21]
	v_mfma_f32_16x16x32_f16 v[6:9], v[172:175], v[216:219], v[6:9]
	v_mfma_f32_16x16x32_f16 v[2:5], v[180:183], v[216:219], v[2:5]
	v_mfma_f32_16x16x32_f16 v[54:57], v[176:179], v[196:199], v[54:57]
	v_mfma_f32_16x16x32_f16 v[50:53], v[188:191], v[196:199], v[50:53]
	v_mfma_f32_16x16x32_f16 v[38:41], v[176:179], v[204:207], v[38:41]
	v_mfma_f32_16x16x32_f16 v[34:37], v[188:191], v[204:207], v[34:37]
	s_setprio 2
	s_barrier
	v_mfma_f32_16x16x32_f16 v[22:25], v[176:179], v[212:215], v[22:25]
	v_mfma_f32_16x16x32_f16 v[18:21], v[188:191], v[212:215], v[18:21]
	v_mfma_f32_16x16x32_f16 v[6:9], v[176:179], v[220:223], v[6:9]
	v_mfma_f32_16x16x32_f16 v[2:5], v[188:191], v[220:223], v[2:5]
	s_setprio 0
	s_nop 0
	s_add_i32 s66, 0, 0x18000
	v_add_u32_e32 v157, s66, v152
	s_add_i32 s67, 0, 0x1c000
	ds_read_b128 v[146:149], v157
	ds_read_b128 v[158:161], v157 offset:1024
	ds_read_b128 v[164:167], v157 offset:2048
	ds_read_b128 v[168:171], v157 offset:3072
	v_add_u32_e32 v157, s67, v152
	ds_read_b128 v[172:175], v157
	ds_read_b128 v[176:179], v157 offset:1024
	ds_read_b128 v[180:183], v157 offset:2048
	ds_read_b128 v[188:191], v157 offset:3072
	s_add_u32 s38, s38, 0x80000
	s_addc_u32 s39, s39, 0
	s_mov_b32 m0, s44
	v_lshl_add_u64 v[228:229], s[38:39], 0, v[130:131]
	ds_read_b128 v[192:195], v156 offset:32768
	ds_read_b128 v[196:199], v156 offset:33792
	ds_read_b128 v[200:203], v156 offset:34816
	ds_read_b128 v[204:207], v156 offset:35840
	ds_read_b128 v[208:211], v156 offset:36864
	ds_read_b128 v[212:215], v156 offset:37888
	ds_read_b128 v[216:219], v156 offset:38912
	ds_read_b128 v[220:223], v156 offset:39936
	global_load_lds_dwordx4 v[228:229], off
	v_lshl_add_u64 v[228:229], s[38:39], 0, v[134:135]
	s_mov_b32 m0, s45
	s_nop 0
	global_load_lds_dwordx4 v[228:229], off
	s_waitcnt vmcnt(8)
	s_waitcnt lgkmcnt(0)
	s_barrier
	s_setprio 1
	s_waitcnt lgkmcnt(0)
	v_mfma_f32_16x16x32_f16 v[126:129], v[146:149], v[192:195], v[126:129]
	v_mfma_f32_16x16x32_f16 v[122:125], v[164:167], v[192:195], v[122:125]
	v_mfma_f32_16x16x32_f16 v[110:113], v[146:149], v[200:203], v[110:113]
	v_mfma_f32_16x16x32_f16 v[106:109], v[164:167], v[200:203], v[106:109]
	v_mfma_f32_16x16x32_f16 v[94:97], v[146:149], v[208:211], v[94:97]
	v_mfma_f32_16x16x32_f16 v[90:93], v[164:167], v[208:211], v[90:93]
	v_mfma_f32_16x16x32_f16 v[78:81], v[146:149], v[216:219], v[78:81]
	v_mfma_f32_16x16x32_f16 v[74:77], v[164:167], v[216:219], v[74:77]
	v_mfma_f32_16x16x32_f16 v[126:129], v[158:161], v[196:199], v[126:129]
	v_mfma_f32_16x16x32_f16 v[122:125], v[168:171], v[196:199], v[122:125]
	v_mfma_f32_16x16x32_f16 v[110:113], v[158:161], v[204:207], v[110:113]
	v_mfma_f32_16x16x32_f16 v[106:109], v[168:171], v[204:207], v[106:109]
	v_mfma_f32_16x16x32_f16 v[94:97], v[158:161], v[212:215], v[94:97]
	v_mfma_f32_16x16x32_f16 v[90:93], v[168:171], v[212:215], v[90:93]
	v_mfma_f32_16x16x32_f16 v[78:81], v[158:161], v[220:223], v[78:81]
	v_mfma_f32_16x16x32_f16 v[74:77], v[168:171], v[220:223], v[74:77]
	s_setprio 0
	s_setprio 1
	v_mfma_f32_16x16x32_f16 v[118:121], v[172:175], v[192:195], v[118:121]
	v_mfma_f32_16x16x32_f16 v[114:117], v[180:183], v[192:195], v[114:117]
	v_mfma_f32_16x16x32_f16 v[102:105], v[172:175], v[200:203], v[102:105]
	v_mfma_f32_16x16x32_f16 v[98:101], v[180:183], v[200:203], v[98:101]
	v_mfma_f32_16x16x32_f16 v[86:89], v[172:175], v[208:211], v[86:89]
	v_mfma_f32_16x16x32_f16 v[82:85], v[180:183], v[208:211], v[82:85]
	v_mfma_f32_16x16x32_f16 v[70:73], v[172:175], v[216:219], v[70:73]
	v_mfma_f32_16x16x32_f16 v[66:69], v[180:183], v[216:219], v[66:69]
	v_mfma_f32_16x16x32_f16 v[118:121], v[176:179], v[196:199], v[118:121]
	v_mfma_f32_16x16x32_f16 v[114:117], v[188:191], v[196:199], v[114:117]
	v_mfma_f32_16x16x32_f16 v[102:105], v[176:179], v[204:207], v[102:105]
	v_mfma_f32_16x16x32_f16 v[98:101], v[188:191], v[204:207], v[98:101]
	s_setprio 2
	s_barrier
	v_mfma_f32_16x16x32_f16 v[86:89], v[176:179], v[212:215], v[86:89]
	v_mfma_f32_16x16x32_f16 v[82:85], v[188:191], v[212:215], v[82:85]
	v_mfma_f32_16x16x32_f16 v[70:73], v[176:179], v[220:223], v[70:73]
	v_mfma_f32_16x16x32_f16 v[66:69], v[188:191], v[220:223], v[66:69]
	s_setprio 0
	s_nop 0
	s_add_i32 s38, s66, s42
	v_lshl_add_u64 v[150:151], v[150:151], 0, s[10:11]
	s_mov_b32 m0, s38
	ds_read_b128 v[192:195], v156 offset:49152
	ds_read_b128 v[196:199], v156 offset:50176
	ds_read_b128 v[200:203], v156 offset:51200
	ds_read_b128 v[204:207], v156 offset:52224
	ds_read_b128 v[208:211], v156 offset:53248
	ds_read_b128 v[212:215], v156 offset:54272
	ds_read_b128 v[216:219], v156 offset:55296
	ds_read_b128 v[220:223], v156 offset:56320
	global_load_lds_dwordx4 v[150:151], off
	s_add_i32 m0, s38, 0x2000
	s_add_u32 s36, s36, 0x80080
	v_lshl_add_u64 v[150:151], v[184:185], 0, s[10:11]
	s_addc_u32 s37, s37, 0
	s_add_i32 s38, s67, s42
	global_load_lds_dwordx4 v[150:151], off
	v_lshl_add_u64 v[150:151], s[36:37], 0, v[132:133]
	s_mov_b32 m0, s38
	s_nop 0
	global_load_lds_dwordx4 v[150:151], off
	v_lshl_add_u64 v[150:151], s[36:37], 0, v[136:137]
	s_add_i32 m0, s38, 0x2000
	s_nop 0
	global_load_lds_dwordx4 v[150:151], off
	v_lshl_add_u64 v[150:151], v[224:225], 0, s[10:11]
	s_mov_b32 m0, s47
	s_nop 0
	global_load_lds_dwordx4 v[150:151], off
	v_lshl_add_u64 v[150:151], v[226:227], 0, s[10:11]
	s_mov_b32 m0, s48
	s_nop 0
	global_load_lds_dwordx4 v[150:151], off
	s_waitcnt vmcnt(8)
	s_waitcnt lgkmcnt(0)
	s_barrier
	s_setprio 1
	s_waitcnt lgkmcnt(0)
	v_mfma_f32_16x16x32_f16 v[62:65], v[146:149], v[192:195], v[62:65]
	v_mfma_f32_16x16x32_f16 v[58:61], v[164:167], v[192:195], v[58:61]
	v_mfma_f32_16x16x32_f16 v[46:49], v[146:149], v[200:203], v[46:49]
	v_mfma_f32_16x16x32_f16 v[42:45], v[164:167], v[200:203], v[42:45]
	v_mfma_f32_16x16x32_f16 v[30:33], v[146:149], v[208:211], v[30:33]
	v_mfma_f32_16x16x32_f16 v[26:29], v[164:167], v[208:211], v[26:29]
	v_mfma_f32_16x16x32_f16 v[14:17], v[146:149], v[216:219], v[14:17]
	v_mfma_f32_16x16x32_f16 v[10:13], v[164:167], v[216:219], v[10:13]
	v_mfma_f32_16x16x32_f16 v[62:65], v[158:161], v[196:199], v[62:65]
	v_mfma_f32_16x16x32_f16 v[58:61], v[168:171], v[196:199], v[58:61]
	v_mfma_f32_16x16x32_f16 v[46:49], v[158:161], v[204:207], v[46:49]
	v_mfma_f32_16x16x32_f16 v[42:45], v[168:171], v[204:207], v[42:45]
	v_mfma_f32_16x16x32_f16 v[30:33], v[158:161], v[212:215], v[30:33]
	v_mfma_f32_16x16x32_f16 v[26:29], v[168:171], v[212:215], v[26:29]
	v_mfma_f32_16x16x32_f16 v[14:17], v[158:161], v[220:223], v[14:17]
	v_mfma_f32_16x16x32_f16 v[10:13], v[168:171], v[220:223], v[10:13]
	s_setprio 0
	s_setprio 1
	v_mfma_f32_16x16x32_f16 v[54:57], v[172:175], v[192:195], v[54:57]
	v_mfma_f32_16x16x32_f16 v[50:53], v[180:183], v[192:195], v[50:53]
	v_mfma_f32_16x16x32_f16 v[38:41], v[172:175], v[200:203], v[38:41]
	v_mfma_f32_16x16x32_f16 v[34:37], v[180:183], v[200:203], v[34:37]
	v_mfma_f32_16x16x32_f16 v[22:25], v[172:175], v[208:211], v[22:25]
	v_mfma_f32_16x16x32_f16 v[18:21], v[180:183], v[208:211], v[18:21]
	v_mfma_f32_16x16x32_f16 v[6:9], v[172:175], v[216:219], v[6:9]
	v_mfma_f32_16x16x32_f16 v[2:5], v[180:183], v[216:219], v[2:5]
	v_mfma_f32_16x16x32_f16 v[54:57], v[176:179], v[196:199], v[54:57]
	v_mfma_f32_16x16x32_f16 v[50:53], v[188:191], v[196:199], v[50:53]
	v_mfma_f32_16x16x32_f16 v[38:41], v[176:179], v[204:207], v[38:41]
	v_mfma_f32_16x16x32_f16 v[34:37], v[188:191], v[204:207], v[34:37]
	s_setprio 2
	s_barrier
	v_mfma_f32_16x16x32_f16 v[22:25], v[176:179], v[212:215], v[22:25]
	v_mfma_f32_16x16x32_f16 v[18:21], v[188:191], v[212:215], v[18:21]
	v_mfma_f32_16x16x32_f16 v[6:9], v[176:179], v[220:223], v[6:9]
	v_mfma_f32_16x16x32_f16 v[2:5], v[188:191], v[220:223], v[2:5]
	s_setprio 0
	s_nop 0
	s_add_i32 s65, s65, 2
	s_add_u32 s34, s34, 0x100
	s_addc_u32 s35, s35, 0
	s_add_u32 s63, s63, 0x100
	s_addc_u32 s64, s64, 0
	s_cmp_gt_u32 s65, 29
	s_cbranch_scc0 .LBB0_1813
	s_and_b64 vcc, exec, s[12:13]
	s_cbranch_vccz .LBB0_1816
	s_barrier

.LBB0_1957:
	ds_read_b128 v[26:29], v194
	ds_read_b128 v[30:33], v194 offset:1024
	ds_read_b128 v[18:21], v194 offset:2048
	ds_read_b128 v[22:25], v194 offset:3072
	ds_read_b128 v[10:13], v195
	ds_read_b128 v[14:17], v195 offset:1024
	ds_read_b128 v[2:5], v195 offset:2048
	ds_read_b128 v[6:9], v195 offset:3072
	s_add_u32 s24, s58, s22
	s_addc_u32 s25, s59, s23
	s_add_u32 s26, s24, 0x50a00100
	s_addc_u32 s27, s25, 0
	s_add_u32 s72, s69, s22
	s_addc_u32 s73, s70, s23
	s_cmpk_eq_i32 s22, 0x700
	s_cselect_b64 vcc, -1, 0
	s_and_b64 s[24:25], vcc, exec
	v_cndmask_b32_e32 v168, v202, v198, vcc
	v_cndmask_b32_e32 v186, v172, v199, vcc
	v_cndmask_b32_e32 v175, v174, v200, vcc
	v_cndmask_b32_e32 v177, v176, v201, vcc
	s_cselect_b32 s27, s1, s27
	s_cselect_b32 s26, s0, s26
	s_cselect_b32 s25, s19, s73
	s_cselect_b32 s24, s68, s72
	v_lshl_add_u64 v[182:183], v[180:181], 0, s[22:23]
	s_add_i32 m0, s36, 0xc000
	ds_read_b128 v[204:207], v196
	ds_read_b128 v[208:211], v196 offset:1024
	ds_read_b128 v[212:215], v196 offset:2048
	ds_read_b128 v[216:219], v196 offset:3072
	ds_read_b128 v[220:223], v196 offset:4096
	ds_read_b128 v[224:227], v196 offset:5120
	ds_read_b128 v[228:231], v196 offset:6144
	ds_read_b128 v[232:235], v196 offset:7168
	global_load_lds_dwordx4 v[182:183], off
	v_lshl_add_u64 v[182:183], v[178:179], 0, s[22:23]
	s_add_i32 m0, s36, 0xe000
	s_nop 0
	global_load_lds_dwordx4 v[182:183], off
	s_waitcnt vmcnt(8)
	s_waitcnt lgkmcnt(0)
	s_barrier
	s_setprio 1
	s_waitcnt lgkmcnt(0)
	v_mfma_scale_f32_16x16x128_f8f6f4 v[158:161], v[26:33], v[204:211], v[158:161], v1, v1 op_sel_hi:[0,0,0]
	v_mfma_scale_f32_16x16x128_f8f6f4 v[150:153], v[18:25], v[204:211], v[150:153], v1, v1 op_sel_hi:[0,0,0]
	v_mfma_scale_f32_16x16x128_f8f6f4 v[142:145], v[26:33], v[212:219], v[142:145], v1, v1 op_sel_hi:[0,0,0]
	v_mfma_scale_f32_16x16x128_f8f6f4 v[134:137], v[18:25], v[212:219], v[134:137], v1, v1 op_sel_hi:[0,0,0]
	v_mfma_scale_f32_16x16x128_f8f6f4 v[126:129], v[26:33], v[220:227], v[126:129], v1, v1 op_sel_hi:[0,0,0]
	v_mfma_scale_f32_16x16x128_f8f6f4 v[118:121], v[18:25], v[220:227], v[118:121], v1, v1 op_sel_hi:[0,0,0]
	v_mfma_scale_f32_16x16x128_f8f6f4 v[110:113], v[26:33], v[228:235], v[110:113], v1, v1 op_sel_hi:[0,0,0]
	v_mfma_scale_f32_16x16x128_f8f6f4 v[102:105], v[18:25], v[228:235], v[102:105], v1, v1 op_sel_hi:[0,0,0]
	s_setprio 0
	s_setprio 1
	v_mfma_scale_f32_16x16x128_f8f6f4 v[154:157], v[10:17], v[204:211], v[154:157], v1, v1 op_sel_hi:[0,0,0]
	v_mfma_scale_f32_16x16x128_f8f6f4 v[146:149], v[2:9], v[204:211], v[146:149], v1, v1 op_sel_hi:[0,0,0]
	v_mfma_scale_f32_16x16x128_f8f6f4 v[138:141], v[10:17], v[212:219], v[138:141], v1, v1 op_sel_hi:[0,0,0]
	v_mfma_scale_f32_16x16x128_f8f6f4 v[130:133], v[2:9], v[212:219], v[130:133], v1, v1 op_sel_hi:[0,0,0]
	v_mfma_scale_f32_16x16x128_f8f6f4 v[122:125], v[10:17], v[220:227], v[122:125], v1, v1 op_sel_hi:[0,0,0]
	v_mfma_scale_f32_16x16x128_f8f6f4 v[114:117], v[2:9], v[220:227], v[114:117], v1, v1 op_sel_hi:[0,0,0]
	s_setprio 2
	s_barrier
	v_mfma_scale_f32_16x16x128_f8f6f4 v[106:109], v[10:17], v[228:235], v[106:109], v1, v1 op_sel_hi:[0,0,0]
	v_mfma_scale_f32_16x16x128_f8f6f4 v[98:101], v[2:9], v[228:235], v[98:101], v1, v1 op_sel_hi:[0,0,0]
	s_setprio 0
	s_nop 0
	s_add_i32 s72, s44, s28
	v_lshl_add_u64 v[182:183], s[24:25], 0, v[166:167]
	s_mov_b32 m0, s72
	ds_read_b128 v[204:207], v196 offset:16384
	ds_read_b128 v[208:211], v196 offset:17408
	ds_read_b128 v[212:215], v196 offset:18432
	ds_read_b128 v[216:219], v196 offset:19456
	ds_read_b128 v[220:223], v196 offset:20480
	ds_read_b128 v[224:227], v196 offset:21504
	ds_read_b128 v[228:231], v196 offset:22528
	ds_read_b128 v[232:235], v196 offset:23552
	global_load_lds_dwordx4 v[182:183], off
	s_add_i32 m0, s72, 0x2000
	s_add_u32 s72, s24, 0x40000
	v_lshl_add_u64 v[184:185], s[24:25], 0, v[164:165]
	s_addc_u32 s73, s25, 0
	s_add_i32 s74, s45, s28
	global_load_lds_dwordx4 v[184:185], off
	v_lshl_add_u64 v[188:189], s[72:73], 0, v[166:167]
	s_mov_b32 m0, s74
	v_mov_b32_e32 v187, v169
	global_load_lds_dwordx4 v[188:189], off
	v_lshl_add_u64 v[188:189], s[72:73], 0, v[164:165]
	s_add_i32 m0, s74, 0x2000
	s_nop 0
	global_load_lds_dwordx4 v[188:189], off
	s_mov_b32 m0, s36
	v_lshl_add_u64 v[188:189], s[26:27], 0, v[168:169]
	global_load_lds_dwordx4 v168, s[26:27]
	s_mov_b32 m0, s37
	s_nop 0
	global_load_lds_dwordx4 v186, s[26:27]
	s_waitcnt vmcnt(8)
	s_waitcnt lgkmcnt(0)
	v_lshl_add_u64 v[186:187], s[26:27], 0, v[186:187]
	s_barrier
	s_setprio 1
	s_waitcnt lgkmcnt(0)
	v_mfma_scale_f32_16x16x128_f8f6f4 v[94:97], v[26:33], v[204:211], v[94:97], v1, v1 op_sel_hi:[0,0,0]
	v_mfma_scale_f32_16x16x128_f8f6f4 v[86:89], v[18:25], v[204:211], v[86:89], v1, v1 op_sel_hi:[0,0,0]
	v_mfma_scale_f32_16x16x128_f8f6f4 v[78:81], v[26:33], v[212:219], v[78:81], v1, v1 op_sel_hi:[0,0,0]
	v_mfma_scale_f32_16x16x128_f8f6f4 v[70:73], v[18:25], v[212:219], v[70:73], v1, v1 op_sel_hi:[0,0,0]
	v_mfma_scale_f32_16x16x128_f8f6f4 v[62:65], v[26:33], v[220:227], v[62:65], v1, v1 op_sel_hi:[0,0,0]
	v_mfma_scale_f32_16x16x128_f8f6f4 v[54:57], v[18:25], v[220:227], v[54:57], v1, v1 op_sel_hi:[0,0,0]
	v_mfma_scale_f32_16x16x128_f8f6f4 v[46:49], v[26:33], v[228:235], v[46:49], v1, v1 op_sel_hi:[0,0,0]
	v_mfma_scale_f32_16x16x128_f8f6f4 v[38:41], v[18:25], v[228:235], v[38:41], v1, v1 op_sel_hi:[0,0,0]
	s_setprio 0
	s_setprio 1
	v_mfma_scale_f32_16x16x128_f8f6f4 v[90:93], v[10:17], v[204:211], v[90:93], v1, v1 op_sel_hi:[0,0,0]
	v_mfma_scale_f32_16x16x128_f8f6f4 v[82:85], v[2:9], v[204:211], v[82:85], v1, v1 op_sel_hi:[0,0,0]
	v_mfma_scale_f32_16x16x128_f8f6f4 v[74:77], v[10:17], v[212:219], v[74:77], v1, v1 op_sel_hi:[0,0,0]
	v_mfma_scale_f32_16x16x128_f8f6f4 v[66:69], v[2:9], v[212:219], v[66:69], v1, v1 op_sel_hi:[0,0,0]
	v_mfma_scale_f32_16x16x128_f8f6f4 v[58:61], v[10:17], v[220:227], v[58:61], v1, v1 op_sel_hi:[0,0,0]
	v_mfma_scale_f32_16x16x128_f8f6f4 v[50:53], v[2:9], v[220:227], v[50:53], v1, v1 op_sel_hi:[0,0,0]
	s_setprio 2
	s_barrier
	v_mfma_scale_f32_16x16x128_f8f6f4 v[42:45], v[10:17], v[228:235], v[42:45], v1, v1 op_sel_hi:[0,0,0]
	v_mfma_scale_f32_16x16x128_f8f6f4 v[34:37], v[2:9], v[228:235], v[34:37], v1, v1 op_sel_hi:[0,0,0]
	s_setprio 0
	s_nop 0
	s_add_i32 s72, 0, 0x18000
	s_add_i32 s73, 0, 0x1c000
	v_add_u32_e32 v14, s72, v192
	v_add_u32_e32 v30, s73, v192
	ds_read_b128 v[2:5], v14
	ds_read_b128 v[6:9], v14 offset:1024
	ds_read_b128 v[10:13], v14 offset:2048
	ds_read_b128 v[14:17], v14 offset:3072
	ds_read_b128 v[18:21], v30
	ds_read_b128 v[22:25], v30 offset:1024
	ds_read_b128 v[26:29], v30 offset:2048
	ds_read_b128 v[30:33], v30 offset:3072
	s_mov_b32 m0, s38
	ds_read_b128 v[204:207], v196 offset:32768
	ds_read_b128 v[208:211], v196 offset:33792
	ds_read_b128 v[212:215], v196 offset:34816
	ds_read_b128 v[216:219], v196 offset:35840
	ds_read_b128 v[220:223], v196 offset:36864
	ds_read_b128 v[224:227], v196 offset:37888
	ds_read_b128 v[228:231], v196 offset:38912
	ds_read_b128 v[232:235], v196 offset:39936
	global_load_lds_dwordx4 v175, s[26:27]
	s_mov_b32 m0, s39
	s_nop 0
	global_load_lds_dwordx4 v177, s[26:27]
	s_waitcnt vmcnt(8)
	s_waitcnt lgkmcnt(0)
	s_barrier
	s_setprio 1
	s_waitcnt lgkmcnt(0)
	v_mfma_scale_f32_16x16x128_f8f6f4 v[158:161], v[2:9], v[204:211], v[158:161], v1, v1 op_sel_hi:[0,0,0]
	v_mfma_scale_f32_16x16x128_f8f6f4 v[150:153], v[10:17], v[204:211], v[150:153], v1, v1 op_sel_hi:[0,0,0]
	v_mfma_scale_f32_16x16x128_f8f6f4 v[142:145], v[2:9], v[212:219], v[142:145], v1, v1 op_sel_hi:[0,0,0]
	v_mfma_scale_f32_16x16x128_f8f6f4 v[134:137], v[10:17], v[212:219], v[134:137], v1, v1 op_sel_hi:[0,0,0]
	v_mfma_scale_f32_16x16x128_f8f6f4 v[126:129], v[2:9], v[220:227], v[126:129], v1, v1 op_sel_hi:[0,0,0]
	v_mfma_scale_f32_16x16x128_f8f6f4 v[118:121], v[10:17], v[220:227], v[118:121], v1, v1 op_sel_hi:[0,0,0]
	v_mfma_scale_f32_16x16x128_f8f6f4 v[110:113], v[2:9], v[228:235], v[110:113], v1, v1 op_sel_hi:[0,0,0]
	v_mfma_scale_f32_16x16x128_f8f6f4 v[102:105], v[10:17], v[228:235], v[102:105], v1, v1 op_sel_hi:[0,0,0]
	s_setprio 0
	s_setprio 1
	v_mfma_scale_f32_16x16x128_f8f6f4 v[154:157], v[18:25], v[204:211], v[154:157], v1, v1 op_sel_hi:[0,0,0]
	v_mfma_scale_f32_16x16x128_f8f6f4 v[146:149], v[26:33], v[204:211], v[146:149], v1, v1 op_sel_hi:[0,0,0]
	v_mfma_scale_f32_16x16x128_f8f6f4 v[138:141], v[18:25], v[212:219], v[138:141], v1, v1 op_sel_hi:[0,0,0]
	v_mfma_scale_f32_16x16x128_f8f6f4 v[130:133], v[26:33], v[212:219], v[130:133], v1, v1 op_sel_hi:[0,0,0]
	v_mfma_scale_f32_16x16x128_f8f6f4 v[122:125], v[18:25], v[220:227], v[122:125], v1, v1 op_sel_hi:[0,0,0]
	v_mfma_scale_f32_16x16x128_f8f6f4 v[114:117], v[26:33], v[220:227], v[114:117], v1, v1 op_sel_hi:[0,0,0]
	s_setprio 2
	s_barrier
	v_mfma_scale_f32_16x16x128_f8f6f4 v[106:109], v[18:25], v[228:235], v[106:109], v1, v1 op_sel_hi:[0,0,0]
	v_mfma_scale_f32_16x16x128_f8f6f4 v[98:101], v[26:33], v[228:235], v[98:101], v1, v1 op_sel_hi:[0,0,0]
	s_setprio 0
	s_nop 0
	s_add_i32 s26, s72, s28
	v_lshl_add_u64 v[182:183], v[182:183], 0, s[10:11]
	s_mov_b32 m0, s26
	ds_read_b128 v[204:207], v196 offset:49152
	ds_read_b128 v[208:211], v196 offset:50176
	ds_read_b128 v[212:215], v196 offset:51200
	ds_read_b128 v[216:219], v196 offset:52224
	ds_read_b128 v[220:223], v196 offset:53248
	ds_read_b128 v[224:227], v196 offset:54272
	ds_read_b128 v[228:231], v196 offset:55296
	ds_read_b128 v[232:235], v196 offset:56320
	global_load_lds_dwordx4 v[182:183], off
	s_add_i32 m0, s26, 0x2000
	s_add_u32 s24, s24, 0x40080
	v_lshl_add_u64 v[182:183], v[184:185], 0, s[10:11]
	s_addc_u32 s25, s25, 0
	s_add_i32 s26, s73, s28
	global_load_lds_dwordx4 v[182:183], off
	v_lshl_add_u64 v[182:183], s[24:25], 0, v[166:167]
	s_mov_b32 m0, s26
	s_nop 0
	global_load_lds_dwordx4 v[182:183], off
	v_lshl_add_u64 v[182:183], s[24:25], 0, v[164:165]
	s_add_i32 m0, s26, 0x2000
	s_nop 0
	global_load_lds_dwordx4 v[182:183], off
	v_lshl_add_u64 v[182:183], v[188:189], 0, s[10:11]
	s_mov_b32 m0, s40
	s_nop 0
	global_load_lds_dwordx4 v[182:183], off
	v_lshl_add_u64 v[182:183], v[186:187], 0, s[10:11]
	s_mov_b32 m0, s41
	s_nop 0
	global_load_lds_dwordx4 v[182:183], off
	s_waitcnt vmcnt(8)
	s_waitcnt lgkmcnt(0)
	s_barrier
	s_setprio 1
	s_waitcnt lgkmcnt(0)
	v_mfma_scale_f32_16x16x128_f8f6f4 v[94:97], v[2:9], v[204:211], v[94:97], v1, v1 op_sel_hi:[0,0,0]
	v_mfma_scale_f32_16x16x128_f8f6f4 v[86:89], v[10:17], v[204:211], v[86:89], v1, v1 op_sel_hi:[0,0,0]
	v_mfma_scale_f32_16x16x128_f8f6f4 v[78:81], v[2:9], v[212:219], v[78:81], v1, v1 op_sel_hi:[0,0,0]
	v_mfma_scale_f32_16x16x128_f8f6f4 v[70:73], v[10:17], v[212:219], v[70:73], v1, v1 op_sel_hi:[0,0,0]
	v_mfma_scale_f32_16x16x128_f8f6f4 v[62:65], v[2:9], v[220:227], v[62:65], v1, v1 op_sel_hi:[0,0,0]
	v_mfma_scale_f32_16x16x128_f8f6f4 v[54:57], v[10:17], v[220:227], v[54:57], v1, v1 op_sel_hi:[0,0,0]
	v_mfma_scale_f32_16x16x128_f8f6f4 v[46:49], v[2:9], v[228:235], v[46:49], v1, v1 op_sel_hi:[0,0,0]
	v_mfma_scale_f32_16x16x128_f8f6f4 v[38:41], v[10:17], v[228:235], v[38:41], v1, v1 op_sel_hi:[0,0,0]
	s_setprio 0
	s_setprio 1
	v_mfma_scale_f32_16x16x128_f8f6f4 v[90:93], v[18:25], v[204:211], v[90:93], v1, v1 op_sel_hi:[0,0,0]
	v_mfma_scale_f32_16x16x128_f8f6f4 v[82:85], v[26:33], v[204:211], v[82:85], v1, v1 op_sel_hi:[0,0,0]
	v_mfma_scale_f32_16x16x128_f8f6f4 v[74:77], v[18:25], v[212:219], v[74:77], v1, v1 op_sel_hi:[0,0,0]
	v_mfma_scale_f32_16x16x128_f8f6f4 v[66:69], v[26:33], v[212:219], v[66:69], v1, v1 op_sel_hi:[0,0,0]
	v_mfma_scale_f32_16x16x128_f8f6f4 v[58:61], v[18:25], v[220:227], v[58:61], v1, v1 op_sel_hi:[0,0,0]
	v_mfma_scale_f32_16x16x128_f8f6f4 v[50:53], v[26:33], v[220:227], v[50:53], v1, v1 op_sel_hi:[0,0,0]
	s_setprio 2
	s_barrier
	v_mfma_scale_f32_16x16x128_f8f6f4 v[42:45], v[18:25], v[228:235], v[42:45], v1, v1 op_sel_hi:[0,0,0]
	v_mfma_scale_f32_16x16x128_f8f6f4 v[34:37], v[26:33], v[228:235], v[34:37], v1, v1 op_sel_hi:[0,0,0]
	s_setprio 0
	s_nop 0
	s_add_i32 s71, s71, 2
	s_add_u32 s22, s22, 0x100
	s_addc_u32 s23, s23, 0
	s_cmp_gt_u32 s71, 13
	s_cbranch_scc0 .LBB0_1957
	s_and_b64 vcc, exec, s[14:15]
	s_cbranch_vccz .LBB0_1960
	s_barrier

.LBB0_2038:
	ds_read_b128 v[26:29], v200
	ds_read_b128 v[30:33], v200 offset:1024
	ds_read_b128 v[18:21], v200 offset:2048
	ds_read_b128 v[22:25], v200 offset:3072
	ds_read_b128 v[10:13], v201
	ds_read_b128 v[14:17], v201 offset:1024
	ds_read_b128 v[2:5], v201 offset:2048
	ds_read_b128 v[6:9], v201 offset:3072
	s_add_u32 s38, s36, 0xfff20080
	s_addc_u32 s39, s37, -1
	s_cmp_eq_u32 s79, 52
	s_cselect_b64 vcc, -1, 0
	s_cselect_b32 s39, s7, s39
	s_cselect_b32 s38, s6, s38
	v_cndmask_b32_e32 v183, v181, v179, vcc
	v_cndmask_b32_e32 v182, v180, v178, vcc
	v_lshl_add_u64 v[228:229], s[36:37], 0, v[172:173]
	s_add_i32 m0, s60, 0xc000
	ds_read_b128 v[184:187], v202
	ds_read_b128 v[188:191], v202 offset:1024
	ds_read_b128 v[204:207], v202 offset:2048
	ds_read_b128 v[208:211], v202 offset:3072
	ds_read_b128 v[212:215], v202 offset:4096
	ds_read_b128 v[216:219], v202 offset:5120
	ds_read_b128 v[220:223], v202 offset:6144
	ds_read_b128 v[224:227], v202 offset:7168
	global_load_lds_dwordx4 v[228:229], off
	v_lshl_add_u64 v[228:229], s[36:37], 0, v[174:175]
	s_add_i32 m0, s60, 0xe000
	s_nop 0
	global_load_lds_dwordx4 v[228:229], off
	s_waitcnt vmcnt(8)
	s_waitcnt lgkmcnt(0)
	s_barrier
	s_setprio 1
	s_waitcnt lgkmcnt(0)
	v_mfma_scale_f32_16x16x128_f8f6f4 v[158:161], v[26:33], v[184:191], v[158:161], v196, v196 op_sel_hi:[0,0,0]
	v_mfma_scale_f32_16x16x128_f8f6f4 v[154:157], v[18:25], v[184:191], v[154:157], v196, v196 op_sel_hi:[0,0,0]
	v_mfma_scale_f32_16x16x128_f8f6f4 v[150:153], v[26:33], v[204:211], v[150:153], v196, v196 op_sel_hi:[0,0,0]
	v_mfma_scale_f32_16x16x128_f8f6f4 v[142:145], v[18:25], v[204:211], v[142:145], v196, v196 op_sel_hi:[0,0,0]
	v_mfma_scale_f32_16x16x128_f8f6f4 v[134:137], v[26:33], v[212:219], v[134:137], v196, v196 op_sel_hi:[0,0,0]
	v_mfma_scale_f32_16x16x128_f8f6f4 v[126:129], v[18:25], v[212:219], v[126:129], v196, v196 op_sel_hi:[0,0,0]
	v_mfma_scale_f32_16x16x128_f8f6f4 v[118:121], v[26:33], v[220:227], v[118:121], v196, v196 op_sel_hi:[0,0,0]
	v_mfma_scale_f32_16x16x128_f8f6f4 v[110:113], v[18:25], v[220:227], v[110:113], v196, v196 op_sel_hi:[0,0,0]
	s_setprio 0
	s_setprio 1
	v_mfma_scale_f32_16x16x128_f8f6f4 v[146:149], v[10:17], v[184:191], v[146:149], v196, v196 op_sel_hi:[0,0,0]
	v_mfma_scale_f32_16x16x128_f8f6f4 v[138:141], v[2:9], v[184:191], v[138:141], v196, v196 op_sel_hi:[0,0,0]
	v_mfma_scale_f32_16x16x128_f8f6f4 v[130:133], v[10:17], v[204:211], v[130:133], v196, v196 op_sel_hi:[0,0,0]
	v_mfma_scale_f32_16x16x128_f8f6f4 v[122:125], v[2:9], v[204:211], v[122:125], v196, v196 op_sel_hi:[0,0,0]
	v_mfma_scale_f32_16x16x128_f8f6f4 v[114:117], v[10:17], v[212:219], v[114:117], v196, v196 op_sel_hi:[0,0,0]
	v_mfma_scale_f32_16x16x128_f8f6f4 v[106:109], v[2:9], v[212:219], v[106:109], v196, v196 op_sel_hi:[0,0,0]
	s_setprio 2
	s_barrier
	v_mfma_scale_f32_16x16x128_f8f6f4 v[102:105], v[10:17], v[220:227], v[102:105], v196, v196 op_sel_hi:[0,0,0]
	v_mfma_scale_f32_16x16x128_f8f6f4 v[98:101], v[2:9], v[220:227], v[98:101], v196, v196 op_sel_hi:[0,0,0]
	s_setprio 0
	s_nop 0
	s_add_i32 s80, s69, s25
	v_lshl_add_u64 v[184:185], v[182:183], 0, v[170:171]
	s_mov_b32 m0, s80
	ds_read_b128 v[204:207], v202 offset:16384
	ds_read_b128 v[208:211], v202 offset:17408
	ds_read_b128 v[212:215], v202 offset:18432
	ds_read_b128 v[216:219], v202 offset:19456
	ds_read_b128 v[220:223], v202 offset:20480
	ds_read_b128 v[224:227], v202 offset:21504
	ds_read_b128 v[228:231], v202 offset:22528
	ds_read_b128 v[232:235], v202 offset:23552
	global_load_lds_dwordx4 v[184:185], off
	v_lshl_add_u64 v[186:187], v[182:183], 0, v[168:169]
	s_add_i32 m0, s80, 0x2000
	v_lshl_add_u64 v[188:189], v[182:183], 0, s[10:11]
	s_add_i32 s80, s70, s25
	global_load_lds_dwordx4 v[186:187], off
	v_lshl_add_u64 v[190:191], v[188:189], 0, v[170:171]
	s_mov_b32 m0, s80
	v_lshl_add_u64 v[188:189], v[188:189], 0, v[168:169]
	global_load_lds_dwordx4 v[190:191], off
	s_add_i32 m0, s80, 0x2000
	v_lshl_add_u64 v[190:191], s[38:39], 0, v[166:167]
	global_load_lds_dwordx4 v[188:189], off
	v_lshl_add_u64 v[188:189], s[38:39], 0, v[164:165]
	s_mov_b32 m0, s60
	s_nop 0
	global_load_lds_dwordx4 v[188:189], off
	s_mov_b32 m0, s61
	s_nop 0
	global_load_lds_dwordx4 v[190:191], off
	s_waitcnt vmcnt(8)
	s_waitcnt lgkmcnt(0)
	s_barrier
	s_setprio 1
	s_waitcnt lgkmcnt(0)
	v_mfma_scale_f32_16x16x128_f8f6f4 v[94:97], v[26:33], v[204:211], v[94:97], v196, v196 op_sel_hi:[0,0,0]
	v_mfma_scale_f32_16x16x128_f8f6f4 v[90:93], v[18:25], v[204:211], v[90:93], v196, v196 op_sel_hi:[0,0,0]
	v_mfma_scale_f32_16x16x128_f8f6f4 v[86:89], v[26:33], v[212:219], v[86:89], v196, v196 op_sel_hi:[0,0,0]
	v_mfma_scale_f32_16x16x128_f8f6f4 v[78:81], v[18:25], v[212:219], v[78:81], v196, v196 op_sel_hi:[0,0,0]
	v_mfma_scale_f32_16x16x128_f8f6f4 v[70:73], v[26:33], v[220:227], v[70:73], v196, v196 op_sel_hi:[0,0,0]
	v_mfma_scale_f32_16x16x128_f8f6f4 v[62:65], v[18:25], v[220:227], v[62:65], v196, v196 op_sel_hi:[0,0,0]
	v_mfma_scale_f32_16x16x128_f8f6f4 v[54:57], v[26:33], v[228:235], v[54:57], v196, v196 op_sel_hi:[0,0,0]
	v_mfma_scale_f32_16x16x128_f8f6f4 v[46:49], v[18:25], v[228:235], v[46:49], v196, v196 op_sel_hi:[0,0,0]
	s_setprio 0
	s_setprio 1
	v_mfma_scale_f32_16x16x128_f8f6f4 v[82:85], v[10:17], v[204:211], v[82:85], v196, v196 op_sel_hi:[0,0,0]
	v_mfma_scale_f32_16x16x128_f8f6f4 v[74:77], v[2:9], v[204:211], v[74:77], v196, v196 op_sel_hi:[0,0,0]
	v_mfma_scale_f32_16x16x128_f8f6f4 v[66:69], v[10:17], v[212:219], v[66:69], v196, v196 op_sel_hi:[0,0,0]
	v_mfma_scale_f32_16x16x128_f8f6f4 v[58:61], v[2:9], v[212:219], v[58:61], v196, v196 op_sel_hi:[0,0,0]
	v_mfma_scale_f32_16x16x128_f8f6f4 v[50:53], v[10:17], v[220:227], v[50:53], v196, v196 op_sel_hi:[0,0,0]
	v_mfma_scale_f32_16x16x128_f8f6f4 v[42:45], v[2:9], v[220:227], v[42:45], v196, v196 op_sel_hi:[0,0,0]
	s_setprio 2
	s_barrier
	v_mfma_scale_f32_16x16x128_f8f6f4 v[38:41], v[10:17], v[228:235], v[38:41], v196, v196 op_sel_hi:[0,0,0]
	v_mfma_scale_f32_16x16x128_f8f6f4 v[34:37], v[2:9], v[228:235], v[34:37], v196, v196 op_sel_hi:[0,0,0]
	s_setprio 0
	s_nop 0
	s_add_i32 s80, 0, 0x18000
	s_add_i32 s81, 0, 0x1c000
	v_add_u32_e32 v14, s80, v198
	v_add_u32_e32 v30, s81, v198
	ds_read_b128 v[2:5], v14
	ds_read_b128 v[6:9], v14 offset:1024
	ds_read_b128 v[10:13], v14 offset:2048
	ds_read_b128 v[14:17], v14 offset:3072
	ds_read_b128 v[18:21], v30
	ds_read_b128 v[22:25], v30 offset:1024
	ds_read_b128 v[26:29], v30 offset:2048
	ds_read_b128 v[30:33], v30 offset:3072
	s_add_u32 s38, s38, 0xe0000
	s_addc_u32 s39, s39, 0
	s_mov_b32 m0, s62
	v_lshl_add_u64 v[236:237], s[38:39], 0, v[164:165]
	ds_read_b128 v[204:207], v202 offset:32768
	ds_read_b128 v[208:211], v202 offset:33792
	ds_read_b128 v[212:215], v202 offset:34816
	ds_read_b128 v[216:219], v202 offset:35840
	ds_read_b128 v[220:223], v202 offset:36864
	ds_read_b128 v[224:227], v202 offset:37888
	ds_read_b128 v[228:231], v202 offset:38912
	ds_read_b128 v[232:235], v202 offset:39936
	global_load_lds_dwordx4 v[236:237], off
	v_lshl_add_u64 v[236:237], s[38:39], 0, v[166:167]
	s_mov_b32 m0, s63
	s_nop 0
	global_load_lds_dwordx4 v[236:237], off
	s_waitcnt vmcnt(8)
	s_waitcnt lgkmcnt(0)
	s_barrier
	s_setprio 1
	s_waitcnt lgkmcnt(0)
	v_mfma_scale_f32_16x16x128_f8f6f4 v[158:161], v[2:9], v[204:211], v[158:161], v196, v196 op_sel_hi:[0,0,0]
	v_mfma_scale_f32_16x16x128_f8f6f4 v[154:157], v[10:17], v[204:211], v[154:157], v196, v196 op_sel_hi:[0,0,0]
	v_mfma_scale_f32_16x16x128_f8f6f4 v[150:153], v[2:9], v[212:219], v[150:153], v196, v196 op_sel_hi:[0,0,0]
	v_mfma_scale_f32_16x16x128_f8f6f4 v[142:145], v[10:17], v[212:219], v[142:145], v196, v196 op_sel_hi:[0,0,0]
	v_mfma_scale_f32_16x16x128_f8f6f4 v[134:137], v[2:9], v[220:227], v[134:137], v196, v196 op_sel_hi:[0,0,0]
	v_mfma_scale_f32_16x16x128_f8f6f4 v[126:129], v[10:17], v[220:227], v[126:129], v196, v196 op_sel_hi:[0,0,0]
	v_mfma_scale_f32_16x16x128_f8f6f4 v[118:121], v[2:9], v[228:235], v[118:121], v196, v196 op_sel_hi:[0,0,0]
	v_mfma_scale_f32_16x16x128_f8f6f4 v[110:113], v[10:17], v[228:235], v[110:113], v196, v196 op_sel_hi:[0,0,0]
	s_setprio 0
	s_setprio 1
	v_mfma_scale_f32_16x16x128_f8f6f4 v[146:149], v[18:25], v[204:211], v[146:149], v196, v196 op_sel_hi:[0,0,0]
	v_mfma_scale_f32_16x16x128_f8f6f4 v[138:141], v[26:33], v[204:211], v[138:141], v196, v196 op_sel_hi:[0,0,0]
	v_mfma_scale_f32_16x16x128_f8f6f4 v[130:133], v[18:25], v[212:219], v[130:133], v196, v196 op_sel_hi:[0,0,0]
	v_mfma_scale_f32_16x16x128_f8f6f4 v[122:125], v[26:33], v[212:219], v[122:125], v196, v196 op_sel_hi:[0,0,0]
	v_mfma_scale_f32_16x16x128_f8f6f4 v[114:117], v[18:25], v[220:227], v[114:117], v196, v196 op_sel_hi:[0,0,0]
	v_mfma_scale_f32_16x16x128_f8f6f4 v[106:109], v[26:33], v[220:227], v[106:109], v196, v196 op_sel_hi:[0,0,0]
	s_setprio 2
	s_barrier
	v_mfma_scale_f32_16x16x128_f8f6f4 v[102:105], v[18:25], v[228:235], v[102:105], v196, v196 op_sel_hi:[0,0,0]
	v_mfma_scale_f32_16x16x128_f8f6f4 v[98:101], v[26:33], v[228:235], v[98:101], v196, v196 op_sel_hi:[0,0,0]
	s_setprio 0
	s_nop 0
	s_add_i32 s38, s80, s25
	v_lshl_add_u64 v[184:185], v[184:185], 0, s[16:17]
	s_mov_b32 m0, s38
	ds_read_b128 v[204:207], v202 offset:49152
	ds_read_b128 v[208:211], v202 offset:50176
	ds_read_b128 v[212:215], v202 offset:51200
	ds_read_b128 v[216:219], v202 offset:52224
	ds_read_b128 v[220:223], v202 offset:53248
	ds_read_b128 v[224:227], v202 offset:54272
	ds_read_b128 v[228:231], v202 offset:55296
	ds_read_b128 v[232:235], v202 offset:56320
	global_load_lds_dwordx4 v[184:185], off
	v_lshl_add_u64 v[184:185], v[186:187], 0, s[16:17]
	s_add_i32 m0, s38, 0x2000
	v_lshl_add_u64 v[182:183], v[182:183], 0, s[18:19]
	s_add_i32 s38, s81, s25
	global_load_lds_dwordx4 v[184:185], off
	v_lshl_add_u64 v[184:185], v[182:183], 0, v[170:171]
	s_mov_b32 m0, s38
	v_lshl_add_u64 v[182:183], v[182:183], 0, v[168:169]
	global_load_lds_dwordx4 v[184:185], off
	s_add_i32 m0, s38, 0x2000
	s_nop 0
	global_load_lds_dwordx4 v[182:183], off
	v_lshl_add_u64 v[182:183], v[188:189], 0, s[16:17]
	s_mov_b32 m0, s66
	s_nop 0
	global_load_lds_dwordx4 v[182:183], off
	v_lshl_add_u64 v[182:183], v[190:191], 0, s[16:17]
	s_mov_b32 m0, s67
	s_nop 0
	global_load_lds_dwordx4 v[182:183], off
	s_waitcnt vmcnt(8)
	s_waitcnt lgkmcnt(0)
	s_barrier
	s_setprio 1
	s_waitcnt lgkmcnt(0)
	v_mfma_scale_f32_16x16x128_f8f6f4 v[94:97], v[2:9], v[204:211], v[94:97], v196, v196 op_sel_hi:[0,0,0]
	v_mfma_scale_f32_16x16x128_f8f6f4 v[90:93], v[10:17], v[204:211], v[90:93], v196, v196 op_sel_hi:[0,0,0]
	v_mfma_scale_f32_16x16x128_f8f6f4 v[86:89], v[2:9], v[212:219], v[86:89], v196, v196 op_sel_hi:[0,0,0]
	v_mfma_scale_f32_16x16x128_f8f6f4 v[78:81], v[10:17], v[212:219], v[78:81], v196, v196 op_sel_hi:[0,0,0]
	v_mfma_scale_f32_16x16x128_f8f6f4 v[70:73], v[2:9], v[220:227], v[70:73], v196, v196 op_sel_hi:[0,0,0]
	v_mfma_scale_f32_16x16x128_f8f6f4 v[62:65], v[10:17], v[220:227], v[62:65], v196, v196 op_sel_hi:[0,0,0]
	v_mfma_scale_f32_16x16x128_f8f6f4 v[54:57], v[2:9], v[228:235], v[54:57], v196, v196 op_sel_hi:[0,0,0]
	v_mfma_scale_f32_16x16x128_f8f6f4 v[46:49], v[10:17], v[228:235], v[46:49], v196, v196 op_sel_hi:[0,0,0]
	s_setprio 0
	s_setprio 1
	v_mfma_scale_f32_16x16x128_f8f6f4 v[82:85], v[18:25], v[204:211], v[82:85], v196, v196 op_sel_hi:[0,0,0]
	v_mfma_scale_f32_16x16x128_f8f6f4 v[74:77], v[26:33], v[204:211], v[74:77], v196, v196 op_sel_hi:[0,0,0]
	v_mfma_scale_f32_16x16x128_f8f6f4 v[66:69], v[18:25], v[212:219], v[66:69], v196, v196 op_sel_hi:[0,0,0]
	v_mfma_scale_f32_16x16x128_f8f6f4 v[58:61], v[26:33], v[212:219], v[58:61], v196, v196 op_sel_hi:[0,0,0]
	v_mfma_scale_f32_16x16x128_f8f6f4 v[50:53], v[18:25], v[220:227], v[50:53], v196, v196 op_sel_hi:[0,0,0]
	v_mfma_scale_f32_16x16x128_f8f6f4 v[42:45], v[26:33], v[220:227], v[42:45], v196, v196 op_sel_hi:[0,0,0]
	s_setprio 2
	s_barrier
	v_mfma_scale_f32_16x16x128_f8f6f4 v[38:41], v[18:25], v[228:235], v[38:41], v196, v196 op_sel_hi:[0,0,0]
	v_mfma_scale_f32_16x16x128_f8f6f4 v[34:37], v[26:33], v[228:235], v[34:37], v196, v196 op_sel_hi:[0,0,0]
	s_setprio 0
	s_nop 0
	s_add_i32 s79, s79, 2
	s_add_u32 s36, s36, 0x100
	s_addc_u32 s37, s37, 0
	s_cmp_gt_u32 s79, 53
	v_lshl_add_u64 v[180:181], v[180:181], 0, s[22:23]
	s_cbranch_scc0 .LBB0_2038
	s_and_b64 vcc, exec, s[20:21]
	s_cbranch_vccz .LBB0_2041
	s_barrier

.LBB0_2058:
	ds_read_b128 v[26:29], v1
	ds_read_b128 v[30:33], v1 offset:1024
	ds_read_b128 v[18:21], v1 offset:2048
	ds_read_b128 v[22:25], v1 offset:3072
	ds_read_b128 v[10:13], v190
	ds_read_b128 v[14:17], v190 offset:1024
	ds_read_b128 v[2:5], v190 offset:2048
	ds_read_b128 v[6:9], v190 offset:3072
	s_add_i32 s25, s28, 2
	s_add_u32 s80, s26, 0xfff20080
	s_addc_u32 s29, s27, -1
	s_cmp_eq_u32 s69, s28
	s_cselect_b32 s28, s6, s80
	s_cselect_b64 vcc, -1, 0
	s_cselect_b32 s29, s7, s29
	v_cndmask_b32_e32 v179, v177, v175, vcc
	v_cndmask_b32_e32 v178, v176, v174, vcc
	v_lshl_add_u64 v[218:219], s[26:27], 0, v[168:169]
	s_add_i32 m0, s60, 0xc000
	ds_read_b128 v[180:183], v191
	ds_read_b128 v[184:187], v191 offset:1024
	ds_read_b128 v[194:197], v191 offset:2048
	ds_read_b128 v[198:201], v191 offset:3072
	ds_read_b128 v[202:205], v191 offset:4096
	ds_read_b128 v[206:209], v191 offset:5120
	ds_read_b128 v[210:213], v191 offset:6144
	ds_read_b128 v[214:217], v191 offset:7168
	global_load_lds_dwordx4 v[218:219], off
	v_lshl_add_u64 v[218:219], s[26:27], 0, v[170:171]
	s_add_i32 m0, s60, 0xe000
	s_nop 0
	global_load_lds_dwordx4 v[218:219], off
	s_waitcnt vmcnt(8)
	s_waitcnt lgkmcnt(0)
	s_barrier
	s_setprio 1
	s_waitcnt lgkmcnt(0)
	v_mfma_scale_f32_16x16x128_f8f6f4 v[158:161], v[26:33], v[180:187], v[158:161], v188, v188 op_sel_hi:[0,0,0]
	v_mfma_scale_f32_16x16x128_f8f6f4 v[154:157], v[18:25], v[180:187], v[154:157], v188, v188 op_sel_hi:[0,0,0]
	v_mfma_scale_f32_16x16x128_f8f6f4 v[150:153], v[26:33], v[194:201], v[150:153], v188, v188 op_sel_hi:[0,0,0]
	v_mfma_scale_f32_16x16x128_f8f6f4 v[142:145], v[18:25], v[194:201], v[142:145], v188, v188 op_sel_hi:[0,0,0]
	v_mfma_scale_f32_16x16x128_f8f6f4 v[134:137], v[26:33], v[202:209], v[134:137], v188, v188 op_sel_hi:[0,0,0]
	v_mfma_scale_f32_16x16x128_f8f6f4 v[126:129], v[18:25], v[202:209], v[126:129], v188, v188 op_sel_hi:[0,0,0]
	v_mfma_scale_f32_16x16x128_f8f6f4 v[118:121], v[26:33], v[210:217], v[118:121], v188, v188 op_sel_hi:[0,0,0]
	v_mfma_scale_f32_16x16x128_f8f6f4 v[110:113], v[18:25], v[210:217], v[110:113], v188, v188 op_sel_hi:[0,0,0]
	s_setprio 0
	s_setprio 1
	v_mfma_scale_f32_16x16x128_f8f6f4 v[146:149], v[10:17], v[180:187], v[146:149], v188, v188 op_sel_hi:[0,0,0]
	v_mfma_scale_f32_16x16x128_f8f6f4 v[138:141], v[2:9], v[180:187], v[138:141], v188, v188 op_sel_hi:[0,0,0]
	v_mfma_scale_f32_16x16x128_f8f6f4 v[130:133], v[10:17], v[194:201], v[130:133], v188, v188 op_sel_hi:[0,0,0]
	v_mfma_scale_f32_16x16x128_f8f6f4 v[122:125], v[2:9], v[194:201], v[122:125], v188, v188 op_sel_hi:[0,0,0]
	v_mfma_scale_f32_16x16x128_f8f6f4 v[114:117], v[10:17], v[202:209], v[114:117], v188, v188 op_sel_hi:[0,0,0]
	v_mfma_scale_f32_16x16x128_f8f6f4 v[106:109], v[2:9], v[202:209], v[106:109], v188, v188 op_sel_hi:[0,0,0]
	s_setprio 2
	s_barrier
	v_mfma_scale_f32_16x16x128_f8f6f4 v[102:105], v[10:17], v[210:217], v[102:105], v188, v188 op_sel_hi:[0,0,0]
	v_mfma_scale_f32_16x16x128_f8f6f4 v[98:101], v[2:9], v[210:217], v[98:101], v188, v188 op_sel_hi:[0,0,0]
	s_setprio 0
	s_nop 0
	s_add_i32 s80, s71, s34
	v_lshl_add_u64 v[180:181], v[178:179], 0, v[164:165]
	s_mov_b32 m0, s80
	ds_read_b128 v[194:197], v191 offset:16384
	ds_read_b128 v[198:201], v191 offset:17408
	ds_read_b128 v[202:205], v191 offset:18432
	ds_read_b128 v[206:209], v191 offset:19456
	ds_read_b128 v[210:213], v191 offset:20480
	ds_read_b128 v[214:217], v191 offset:21504
	ds_read_b128 v[218:221], v191 offset:22528
	ds_read_b128 v[222:225], v191 offset:23552
	global_load_lds_dwordx4 v[180:181], off
	v_lshl_add_u64 v[182:183], v[178:179], 0, v[166:167]
	s_add_i32 m0, s80, 0x2000
	v_lshl_add_u64 v[184:185], v[178:179], 0, s[10:11]
	s_add_i32 s80, s72, s34
	global_load_lds_dwordx4 v[182:183], off
	v_lshl_add_u64 v[186:187], v[184:185], 0, v[164:165]
	s_mov_b32 m0, s80
	v_lshl_add_u64 v[184:185], v[184:185], 0, v[166:167]
	global_load_lds_dwordx4 v[186:187], off
	s_add_i32 m0, s80, 0x2000
	v_lshl_add_u64 v[186:187], s[28:29], 0, v[166:167]
	global_load_lds_dwordx4 v[184:185], off
	v_lshl_add_u64 v[184:185], s[28:29], 0, v[164:165]
	s_mov_b32 m0, s60
	s_nop 0
	global_load_lds_dwordx4 v[184:185], off
	s_mov_b32 m0, s61
	s_nop 0
	global_load_lds_dwordx4 v[186:187], off
	s_waitcnt vmcnt(8)
	s_waitcnt lgkmcnt(0)
	s_barrier
	s_setprio 1
	s_waitcnt lgkmcnt(0)
	v_mfma_scale_f32_16x16x128_f8f6f4 v[94:97], v[26:33], v[194:201], v[94:97], v188, v188 op_sel_hi:[0,0,0]
	v_mfma_scale_f32_16x16x128_f8f6f4 v[90:93], v[18:25], v[194:201], v[90:93], v188, v188 op_sel_hi:[0,0,0]
	v_mfma_scale_f32_16x16x128_f8f6f4 v[86:89], v[26:33], v[202:209], v[86:89], v188, v188 op_sel_hi:[0,0,0]
	v_mfma_scale_f32_16x16x128_f8f6f4 v[78:81], v[18:25], v[202:209], v[78:81], v188, v188 op_sel_hi:[0,0,0]
	v_mfma_scale_f32_16x16x128_f8f6f4 v[70:73], v[26:33], v[210:217], v[70:73], v188, v188 op_sel_hi:[0,0,0]
	v_mfma_scale_f32_16x16x128_f8f6f4 v[62:65], v[18:25], v[210:217], v[62:65], v188, v188 op_sel_hi:[0,0,0]
	v_mfma_scale_f32_16x16x128_f8f6f4 v[54:57], v[26:33], v[218:225], v[54:57], v188, v188 op_sel_hi:[0,0,0]
	v_mfma_scale_f32_16x16x128_f8f6f4 v[46:49], v[18:25], v[218:225], v[46:49], v188, v188 op_sel_hi:[0,0,0]
	s_setprio 0
	s_setprio 1
	v_mfma_scale_f32_16x16x128_f8f6f4 v[82:85], v[10:17], v[194:201], v[82:85], v188, v188 op_sel_hi:[0,0,0]
	v_mfma_scale_f32_16x16x128_f8f6f4 v[74:77], v[2:9], v[194:201], v[74:77], v188, v188 op_sel_hi:[0,0,0]
	v_mfma_scale_f32_16x16x128_f8f6f4 v[66:69], v[10:17], v[202:209], v[66:69], v188, v188 op_sel_hi:[0,0,0]
	v_mfma_scale_f32_16x16x128_f8f6f4 v[58:61], v[2:9], v[202:209], v[58:61], v188, v188 op_sel_hi:[0,0,0]
	v_mfma_scale_f32_16x16x128_f8f6f4 v[50:53], v[10:17], v[210:217], v[50:53], v188, v188 op_sel_hi:[0,0,0]
	v_mfma_scale_f32_16x16x128_f8f6f4 v[42:45], v[2:9], v[210:217], v[42:45], v188, v188 op_sel_hi:[0,0,0]
	s_setprio 2
	s_barrier
	v_mfma_scale_f32_16x16x128_f8f6f4 v[38:41], v[10:17], v[218:225], v[38:41], v188, v188 op_sel_hi:[0,0,0]
	v_mfma_scale_f32_16x16x128_f8f6f4 v[34:37], v[2:9], v[218:225], v[34:37], v188, v188 op_sel_hi:[0,0,0]
	s_setprio 0
	s_nop 0
	s_add_i32 s80, 0, 0x18000
	s_add_i32 s81, 0, 0x1c000
	v_add_u32_e32 v14, s80, v189
	v_add_u32_e32 v30, s81, v189
	ds_read_b128 v[2:5], v14
	ds_read_b128 v[6:9], v14 offset:1024
	ds_read_b128 v[10:13], v14 offset:2048
	ds_read_b128 v[14:17], v14 offset:3072
	ds_read_b128 v[18:21], v30
	ds_read_b128 v[22:25], v30 offset:1024
	ds_read_b128 v[26:29], v30 offset:2048
	ds_read_b128 v[30:33], v30 offset:3072
	s_add_u32 s28, s28, 0xe0000
	s_addc_u32 s29, s29, 0
	s_mov_b32 m0, s62
	v_lshl_add_u64 v[226:227], s[28:29], 0, v[164:165]
	ds_read_b128 v[194:197], v191 offset:32768
	ds_read_b128 v[198:201], v191 offset:33792
	ds_read_b128 v[202:205], v191 offset:34816
	ds_read_b128 v[206:209], v191 offset:35840
	ds_read_b128 v[210:213], v191 offset:36864
	ds_read_b128 v[214:217], v191 offset:37888
	ds_read_b128 v[218:221], v191 offset:38912
	ds_read_b128 v[222:225], v191 offset:39936
	global_load_lds_dwordx4 v[226:227], off
	v_lshl_add_u64 v[226:227], s[28:29], 0, v[166:167]
	s_mov_b32 m0, s63
	s_nop 0
	global_load_lds_dwordx4 v[226:227], off
	s_waitcnt vmcnt(8)
	s_waitcnt lgkmcnt(0)
	s_barrier
	s_setprio 1
	s_waitcnt lgkmcnt(0)
	v_mfma_scale_f32_16x16x128_f8f6f4 v[158:161], v[2:9], v[194:201], v[158:161], v188, v188 op_sel_hi:[0,0,0]
	v_mfma_scale_f32_16x16x128_f8f6f4 v[154:157], v[10:17], v[194:201], v[154:157], v188, v188 op_sel_hi:[0,0,0]
	v_mfma_scale_f32_16x16x128_f8f6f4 v[150:153], v[2:9], v[202:209], v[150:153], v188, v188 op_sel_hi:[0,0,0]
	v_mfma_scale_f32_16x16x128_f8f6f4 v[142:145], v[10:17], v[202:209], v[142:145], v188, v188 op_sel_hi:[0,0,0]
	v_mfma_scale_f32_16x16x128_f8f6f4 v[134:137], v[2:9], v[210:217], v[134:137], v188, v188 op_sel_hi:[0,0,0]
	v_mfma_scale_f32_16x16x128_f8f6f4 v[126:129], v[10:17], v[210:217], v[126:129], v188, v188 op_sel_hi:[0,0,0]
	v_mfma_scale_f32_16x16x128_f8f6f4 v[118:121], v[2:9], v[218:225], v[118:121], v188, v188 op_sel_hi:[0,0,0]
	v_mfma_scale_f32_16x16x128_f8f6f4 v[110:113], v[10:17], v[218:225], v[110:113], v188, v188 op_sel_hi:[0,0,0]
	s_setprio 0
	s_setprio 1
	v_mfma_scale_f32_16x16x128_f8f6f4 v[146:149], v[18:25], v[194:201], v[146:149], v188, v188 op_sel_hi:[0,0,0]
	v_mfma_scale_f32_16x16x128_f8f6f4 v[138:141], v[26:33], v[194:201], v[138:141], v188, v188 op_sel_hi:[0,0,0]
	v_mfma_scale_f32_16x16x128_f8f6f4 v[130:133], v[18:25], v[202:209], v[130:133], v188, v188 op_sel_hi:[0,0,0]
	v_mfma_scale_f32_16x16x128_f8f6f4 v[122:125], v[26:33], v[202:209], v[122:125], v188, v188 op_sel_hi:[0,0,0]
	v_mfma_scale_f32_16x16x128_f8f6f4 v[114:117], v[18:25], v[210:217], v[114:117], v188, v188 op_sel_hi:[0,0,0]
	v_mfma_scale_f32_16x16x128_f8f6f4 v[106:109], v[26:33], v[210:217], v[106:109], v188, v188 op_sel_hi:[0,0,0]
	s_setprio 2
	s_barrier
	v_mfma_scale_f32_16x16x128_f8f6f4 v[102:105], v[18:25], v[218:225], v[102:105], v188, v188 op_sel_hi:[0,0,0]
	v_mfma_scale_f32_16x16x128_f8f6f4 v[98:101], v[26:33], v[218:225], v[98:101], v188, v188 op_sel_hi:[0,0,0]
	s_setprio 0
	s_nop 0
	s_add_i32 s28, s80, s34
	v_lshl_add_u64 v[180:181], v[180:181], 0, s[14:15]
	s_mov_b32 m0, s28
	ds_read_b128 v[194:197], v191 offset:49152
	ds_read_b128 v[198:201], v191 offset:50176
	ds_read_b128 v[202:205], v191 offset:51200
	ds_read_b128 v[206:209], v191 offset:52224
	ds_read_b128 v[210:213], v191 offset:53248
	ds_read_b128 v[214:217], v191 offset:54272
	ds_read_b128 v[218:221], v191 offset:55296
	ds_read_b128 v[222:225], v191 offset:56320
	global_load_lds_dwordx4 v[180:181], off
	v_lshl_add_u64 v[180:181], v[182:183], 0, s[14:15]
	s_add_i32 m0, s28, 0x2000
	v_lshl_add_u64 v[178:179], v[178:179], 0, s[16:17]
	s_add_i32 s28, s81, s34
	global_load_lds_dwordx4 v[180:181], off
	v_lshl_add_u64 v[180:181], v[178:179], 0, v[164:165]
	s_mov_b32 m0, s28
	v_lshl_add_u64 v[178:179], v[178:179], 0, v[166:167]
	global_load_lds_dwordx4 v[180:181], off
	s_add_i32 m0, s28, 0x2000
	s_nop 0
	global_load_lds_dwordx4 v[178:179], off
	v_lshl_add_u64 v[178:179], v[184:185], 0, s[14:15]
	s_mov_b32 m0, s65
	s_nop 0
	global_load_lds_dwordx4 v[178:179], off
	v_lshl_add_u64 v[178:179], v[186:187], 0, s[14:15]
	s_mov_b32 m0, s66
	s_nop 0
	global_load_lds_dwordx4 v[178:179], off
	s_waitcnt vmcnt(8)
	s_waitcnt lgkmcnt(0)
	s_barrier
	s_setprio 1
	s_waitcnt lgkmcnt(0)
	v_mfma_scale_f32_16x16x128_f8f6f4 v[94:97], v[2:9], v[194:201], v[94:97], v188, v188 op_sel_hi:[0,0,0]
	v_mfma_scale_f32_16x16x128_f8f6f4 v[90:93], v[10:17], v[194:201], v[90:93], v188, v188 op_sel_hi:[0,0,0]
	v_mfma_scale_f32_16x16x128_f8f6f4 v[86:89], v[2:9], v[202:209], v[86:89], v188, v188 op_sel_hi:[0,0,0]
	v_mfma_scale_f32_16x16x128_f8f6f4 v[78:81], v[10:17], v[202:209], v[78:81], v188, v188 op_sel_hi:[0,0,0]
	v_mfma_scale_f32_16x16x128_f8f6f4 v[70:73], v[2:9], v[210:217], v[70:73], v188, v188 op_sel_hi:[0,0,0]
	v_mfma_scale_f32_16x16x128_f8f6f4 v[62:65], v[10:17], v[210:217], v[62:65], v188, v188 op_sel_hi:[0,0,0]
	v_mfma_scale_f32_16x16x128_f8f6f4 v[54:57], v[2:9], v[218:225], v[54:57], v188, v188 op_sel_hi:[0,0,0]
	v_mfma_scale_f32_16x16x128_f8f6f4 v[46:49], v[10:17], v[218:225], v[46:49], v188, v188 op_sel_hi:[0,0,0]
	s_setprio 0
	s_setprio 1
	v_mfma_scale_f32_16x16x128_f8f6f4 v[82:85], v[18:25], v[194:201], v[82:85], v188, v188 op_sel_hi:[0,0,0]
	v_mfma_scale_f32_16x16x128_f8f6f4 v[74:77], v[26:33], v[194:201], v[74:77], v188, v188 op_sel_hi:[0,0,0]
	v_mfma_scale_f32_16x16x128_f8f6f4 v[66:69], v[18:25], v[202:209], v[66:69], v188, v188 op_sel_hi:[0,0,0]
	v_mfma_scale_f32_16x16x128_f8f6f4 v[58:61], v[26:33], v[202:209], v[58:61], v188, v188 op_sel_hi:[0,0,0]
	v_mfma_scale_f32_16x16x128_f8f6f4 v[50:53], v[18:25], v[210:217], v[50:53], v188, v188 op_sel_hi:[0,0,0]
	v_mfma_scale_f32_16x16x128_f8f6f4 v[42:45], v[26:33], v[210:217], v[42:45], v188, v188 op_sel_hi:[0,0,0]
	s_setprio 2
	s_barrier
	v_mfma_scale_f32_16x16x128_f8f6f4 v[38:41], v[18:25], v[218:225], v[38:41], v188, v188 op_sel_hi:[0,0,0]
	v_mfma_scale_f32_16x16x128_f8f6f4 v[34:37], v[26:33], v[218:225], v[34:37], v188, v188 op_sel_hi:[0,0,0]
	s_setprio 0
	s_nop 0
	s_add_u32 s26, s26, 0x100
	s_addc_u32 s27, s27, 0
	v_lshl_add_u64 v[176:177], v[176:177], 0, s[22:23]
	s_cmp_ge_u32 s25, s67
	s_mov_b32 s28, s25
	s_cbranch_scc0 .LBB0_2058
	s_and_b64 vcc, exec, s[20:21]
	s_cbranch_vccz .LBB0_2061
	s_barrier
